# phase F layer 0: rows < L take a copy of the loop body where the 16 flat loads (latent ? LDS : global selects) are ds_read_b128 and the per-step vmcnt(0) waits become lgkmcnt(0); context rows keep the
# speedup vs baseline: 1.0048x; 1.0039x over previous
.LBB0_1365:
	s_cmpk_lt_i32 s0, 0x4000
	s_cbranch_scc1 .Lf_lat_L0
	s_cmp_lg_u32 s1, -1
	s_cselect_b32 s52, s1, 0
	s_cselect_b32 s53, s43, 0
	s_cmp_lg_u32 s45, -1
	s_cselect_b32 s61, s45, 0
	s_cselect_b32 s62, s43, 0
	s_cmpk_lt_i32 s0, 0x4000
	s_cselect_b32 s53, s53, s42
	s_cselect_b32 s52, s52, s33
	s_waitcnt vmcnt(7) lgkmcnt(7)
	v_lshl_add_u64 v[18:19], s[40:41], 0, v[110:111]
	v_lshl_add_u64 v[118:119], s[52:53], 0, v[112:113]
	s_mov_b32 s52, 0x1b41000
	v_add_co_u32_e32 v14, vcc, s52, v18
	ds_read_b128 v[86:89], v134
	ds_read_b128 v[82:85], v134 offset:8192
	ds_read_b128 v[78:81], v134 offset:16384
	ds_read_b128 v[74:77], v134 offset:24576
	ds_read_b128 v[70:73], v134 offset:32768
	ds_read_b128 v[66:69], v134 offset:40960
	ds_read_b128 v[62:65], v134 offset:49152
	ds_read_b128 v[58:61], v134 offset:57344
	ds_read_b128 v[54:57], v135
	ds_read_b128 v[50:53], v136
	ds_read_b128 v[46:49], v137
	ds_read_b128 v[42:45], v138
	ds_read_b128 v[38:41], v139
	ds_read_b128 v[34:37], v140
	s_waitcnt vmcnt(4) lgkmcnt(14)
	ds_read_b128 v[30:33], v141
	ds_read_b128 v[26:29], v142
	v_addc_co_u32_e32 v15, vcc, 0, v19, vcc
	global_load_dwordx4 v[2:5], v[14:15], off offset:3072
	global_load_dwordx4 v[6:9], v[14:15], off offset:2048
	s_mov_b32 s52, 0x1b40000
	v_add_co_u32_e32 v94, vcc, s52, v18
	s_cselect_b32 s63, s62, s55
	s_nop 0
	v_addc_co_u32_e32 v95, vcc, 0, v19, vcc
	s_cselect_b32 s62, s61, s54
	v_lshl_add_u64 v[116:117], s[62:63], 0, v[112:113]
	s_mov_b32 s52, 0x800000
	v_lshl_add_u64 v[120:121], s[40:41], 0, v[108:109]
	s_waitcnt vmcnt(1)
	v_mov_b32_e32 v13, v3
	s_waitcnt vmcnt(0)
	v_mov_b32_e32 v12, v7
	v_mov_b32_e32 v10, v6
	v_mov_b32_e32 v11, v2
	v_pk_mul_f32 v[12:13], v[12:13], v[12:13]
	s_nop 0
	v_pk_fma_f32 v[10:11], v[10:11], v[10:11], v[12:13]
	v_mov_b32_e32 v12, v8
	v_mov_b32_e32 v13, v4
	v_pk_fma_f32 v[10:11], v[12:13], v[12:13], v[10:11]
	v_mov_b32_e32 v12, v9
	v_mov_b32_e32 v13, v5
	v_pk_fma_f32 v[114:115], v[12:13], v[12:13], v[10:11]
	global_load_dwordx4 v[10:13], v[14:15], off offset:1024
	s_nop 0
	global_load_dwordx4 v[14:17], v[14:15], off
	ds_read_b128 v[98:101], v133
	global_load_dwordx4 v[90:93], v[94:95], off offset:1024
	global_load_dwordx4 v[102:105], v[94:95], off
	s_waitcnt vmcnt(3)
	v_mov_b32_e32 v23, v11
	s_waitcnt vmcnt(2)
	v_mov_b32_e32 v22, v15
	v_mov_b32_e32 v20, v14
	v_mov_b32_e32 v21, v10
	v_pk_mul_f32 v[22:23], v[22:23], v[22:23]
	s_waitcnt vmcnt(1)
	v_mul_f32_e32 v215, v91, v91
	v_pk_fma_f32 v[20:21], v[20:21], v[20:21], v[22:23]
	v_mov_b32_e32 v22, v16
	v_mov_b32_e32 v23, v12
	v_pk_fma_f32 v[20:21], v[22:23], v[22:23], v[20:21]
	v_mov_b32_e32 v22, v17
	v_mov_b32_e32 v23, v13
	v_pk_fma_f32 v[124:125], v[22:23], v[22:23], v[20:21]
	global_load_dwordx4 v[18:21], v[94:95], off offset:3072
	global_load_dwordx4 v[22:25], v[94:95], off offset:2048
	s_nop 0
	flat_load_dwordx4 v[94:97], v[118:119]
	flat_load_dwordx4 v[210:213], v[116:117]
	s_waitcnt vmcnt(0)
	v_mul_f32_e32 v216, v103, v103
	v_fmac_f32_e32 v215, v90, v90
	v_fmac_f32_e32 v216, v102, v102
	v_fmac_f32_e32 v215, v92, v92
	v_fmac_f32_e32 v216, v104, v104
	v_fmac_f32_e32 v215, v93, v93
	v_fmac_f32_e32 v216, v105, v105
	v_mul_f32_e32 v190, v19, v19
	v_mul_f32_e32 v214, v23, v23
	v_fmac_f32_e32 v214, v22, v22
	v_fmac_f32_e32 v190, v18, v18
	v_fmac_f32_e32 v214, v24, v24
	v_fmac_f32_e32 v190, v20, v20
	v_fmac_f32_e32 v214, v25, v25
	s_waitcnt lgkmcnt(0)
	v_mov_b32_e32 v122, v210
	v_add_f32_e32 v210, v216, v215
	v_fmac_f32_e32 v190, v21, v21
	v_add_f32_e32 v210, v210, v214
	v_add_f32_e32 v190, v210, v190
	v_add_f32_e32 v124, v190, v124
	v_add_f32_e32 v124, v124, v125
	v_add_f32_e32 v114, v124, v114
	v_add_f32_e32 v114, v114, v115
	ds_bpermute_b32 v115, v1, v114
	v_mov_b32_e32 v124, v102
	v_mov_b32_e32 v125, v104
	v_mov_b32_e32 v104, v103
	v_mov_b32_e32 v123, v212
	s_waitcnt lgkmcnt(0)
	v_add_f32_e32 v114, v114, v115
	ds_bpermute_b32 v115, v128, v114
	v_mov_b32_e32 v212, v211
	v_mov_b32_e32 v210, v98
	v_mov_b32_e32 v211, v100
	v_mov_b32_e32 v100, v99
	s_waitcnt lgkmcnt(0)
	v_add_f32_e32 v114, v114, v115
	ds_bpermute_b32 v115, v129, v114
	v_pk_add_f32 v[126:127], v[122:123], 1.0 op_sel_hi:[1,0]
	v_pk_add_f32 v[122:123], v[212:213], 1.0 op_sel_hi:[1,0]
	s_waitcnt lgkmcnt(0)
	v_add_f32_e32 v114, v114, v115
	ds_bpermute_b32 v115, v130, v114
	s_waitcnt lgkmcnt(0)
	v_add_f32_e32 v114, v114, v115
	ds_bpermute_b32 v115, v131, v114
	s_waitcnt lgkmcnt(0)
	v_add_f32_e32 v114, v114, v115
	ds_bpermute_b32 v115, v132, v114
	s_waitcnt lgkmcnt(0)
	v_add_f32_e32 v114, v114, v115
	v_fmamk_f32 v114, v114, 0x3a000000, v207
	v_cmp_gt_f32_e32 vcc, s52, v114
	v_mul_f32_e32 v115, 0x4b800000, v114
	s_mov_b32 s52, 0x2ec40000
	v_cndmask_b32_e32 v114, v114, v115, vcc
	v_rsq_f32_e32 v114, v114
	s_nop 0
	v_mul_f32_e32 v115, 0x45800000, v114
	v_cndmask_b32_e32 v114, v114, v115, vcc
	v_pk_mul_f32 v[124:125], v[124:125], v[114:115] op_sel_hi:[1,0]
	v_pk_mul_f32 v[102:103], v[104:105], v[114:115] op_sel_hi:[1,0]
	v_pk_mul_f32 v[124:125], v[210:211], v[124:125]
	v_mov_b32_e32 v211, v96
	v_pk_mul_f32 v[98:99], v[100:101], v[102:103]
	v_mov_b32_e32 v96, v95
	v_mov_b32_e32 v210, v94
	v_pk_fma_f32 v[96:97], v[122:123], v[98:99], v[96:97]
	v_pk_fma_f32 v[124:125], v[126:127], v[124:125], v[210:211]
	v_fma_f32 v33, v97, v33, 0
	v_fmac_f32_e32 v33, v125, v32
	v_and_b32_sdwa v98, v97, v208 dst_sel:DWORD dst_unused:UNUSED_PAD src0_sel:WORD_1 src1_sel:DWORD
	v_fmac_f32_e32 v33, v96, v31
	v_and_b32_sdwa v94, v125, v208 dst_sel:DWORD dst_unused:UNUSED_PAD src0_sel:WORD_1 src1_sel:DWORD
	v_and_b32_sdwa v99, v96, v208 dst_sel:DWORD dst_unused:UNUSED_PAD src0_sel:WORD_1 src1_sel:DWORD
	v_add3_u32 v98, v97, v98, s57
	v_fmac_f32_e32 v33, v124, v30
	v_fma_f32 v30, v97, v29, 0
	v_and_b32_sdwa v95, v124, v208 dst_sel:DWORD dst_unused:UNUSED_PAD src0_sel:WORD_1 src1_sel:DWORD
	v_add3_u32 v94, v125, v94, s57
	v_add3_u32 v99, v96, v99, s57
	v_and_b32_e32 v98, 0xffff0000, v98
	v_fma_f32 v89, v97, v89, 0
	v_fma_f32 v85, v97, v85, 0
	v_fma_f32 v81, v97, v81, 0
	v_fma_f32 v77, v97, v77, 0
	v_fma_f32 v73, v97, v73, 0
	v_fma_f32 v69, v97, v69, 0
	v_fma_f32 v65, v97, v65, 0
	v_fma_f32 v61, v97, v61, 0
	v_fma_f32 v57, v97, v57, 0
	v_fma_f32 v53, v97, v53, 0
	v_fma_f32 v49, v97, v49, 0
	v_fma_f32 v45, v97, v45, 0
	v_fma_f32 v41, v97, v41, 0
	v_fma_f32 v37, v97, v37, 0
	v_fmac_f32_e32 v30, v125, v28
	v_add3_u32 v95, v124, v95, s57
	v_and_b32_e32 v100, 0xffff0000, v99
	v_or_b32_sdwa v99, v98, v94 dst_sel:DWORD dst_unused:UNUSED_PAD src0_sel:DWORD src1_sel:WORD_1
	v_add_co_u32_e32 v94, vcc, s52, v120
	v_fmac_f32_e32 v89, v125, v88
	v_fmac_f32_e32 v85, v125, v84
	v_fmac_f32_e32 v81, v125, v80
	v_fmac_f32_e32 v77, v125, v76
	v_fmac_f32_e32 v73, v125, v72
	v_fmac_f32_e32 v69, v125, v68
	v_fmac_f32_e32 v65, v125, v64
	v_fmac_f32_e32 v61, v125, v60
	v_fmac_f32_e32 v57, v125, v56
	v_fmac_f32_e32 v53, v125, v52
	v_fmac_f32_e32 v49, v125, v48
	v_fmac_f32_e32 v45, v125, v44
	v_fmac_f32_e32 v41, v125, v40
	v_fmac_f32_e32 v37, v125, v36
	v_fmac_f32_e32 v30, v96, v27
	v_or_b32_sdwa v98, v100, v95 dst_sel:DWORD dst_unused:UNUSED_PAD src0_sel:DWORD src1_sel:WORD_1
	v_addc_co_u32_e32 v95, vcc, 0, v121, vcc
	v_fmac_f32_e32 v89, v96, v87
	v_fmac_f32_e32 v85, v96, v83
	v_fmac_f32_e32 v81, v96, v79
	v_fmac_f32_e32 v77, v96, v75
	v_fmac_f32_e32 v73, v96, v71
	v_fmac_f32_e32 v69, v96, v67
	v_fmac_f32_e32 v65, v96, v63
	v_fmac_f32_e32 v61, v96, v59
	v_fmac_f32_e32 v57, v96, v55
	v_fmac_f32_e32 v53, v96, v51
	v_fmac_f32_e32 v49, v96, v47
	v_fmac_f32_e32 v45, v96, v43
	v_fmac_f32_e32 v41, v96, v39
	v_fmac_f32_e32 v37, v96, v35
	v_fmac_f32_e32 v30, v124, v26
	global_store_dwordx2 v[94:95], v[98:99], off
	v_fmac_f32_e32 v89, v124, v86
	v_fmac_f32_e32 v85, v124, v82
	v_fmac_f32_e32 v81, v124, v78
	v_fmac_f32_e32 v77, v124, v74
	v_fmac_f32_e32 v73, v124, v70
	v_fmac_f32_e32 v69, v124, v66
	v_fmac_f32_e32 v65, v124, v62
	v_fmac_f32_e32 v61, v124, v58
	v_fmac_f32_e32 v57, v124, v54
	v_fmac_f32_e32 v53, v124, v50
	v_fmac_f32_e32 v49, v124, v46
	v_fmac_f32_e32 v45, v124, v42
	v_fmac_f32_e32 v41, v124, v38
	v_fmac_f32_e32 v37, v124, v34
	ds_read_b128 v[96:99], v143
	flat_load_dwordx4 v[100:103], v[118:119] offset:1024
	flat_load_dwordx4 v[120:123], v[116:117] offset:1024
	v_mov_b32_e32 v26, v90
	v_mov_b32_e32 v27, v92
	v_pk_mul_f32 v[26:27], v[26:27], v[114:115] op_sel_hi:[1,0]
	s_waitcnt lgkmcnt(0)
	v_mov_b32_e32 v28, v96
	v_mov_b32_e32 v29, v98
	v_pk_mul_f32 v[26:27], v[26:27], v[28:29]
	v_mov_b32_e32 v92, v91
	v_mov_b32_e32 v98, v97
	s_waitcnt vmcnt(0)
	v_mov_b32_e32 v34, v100
	v_mov_b32_e32 v28, v120
	v_mov_b32_e32 v29, v122
	v_pk_add_f32 v[28:29], v[28:29], 1.0 op_sel_hi:[1,0]
	v_mov_b32_e32 v35, v102
	v_pk_fma_f32 v[26:27], v[26:27], v[28:29], v[34:35]
	v_pk_mul_f32 v[28:29], v[92:93], v[114:115] op_sel_hi:[1,0]
	ds_read_b128 v[90:93], v134 offset:1024
	v_mov_b32_e32 v122, v121
	v_pk_mul_f32 v[28:29], v[28:29], v[98:99]
	v_pk_add_f32 v[34:35], v[122:123], 1.0 op_sel_hi:[1,0]
	v_mov_b32_e32 v102, v101
	v_pk_fma_f32 v[28:29], v[28:29], v[34:35], v[102:103]
	v_and_b32_sdwa v31, v27, v208 dst_sel:DWORD dst_unused:UNUSED_PAD src0_sel:WORD_1 src1_sel:DWORD
	s_waitcnt lgkmcnt(0)
	v_fmac_f32_e32 v89, v29, v93
	v_fmac_f32_e32 v89, v27, v92
	v_fmac_f32_e32 v89, v28, v91
	v_fmac_f32_e32 v89, v26, v90
	ds_read_b128 v[90:93], v134 offset:9216
	v_and_b32_sdwa v34, v29, v208 dst_sel:DWORD dst_unused:UNUSED_PAD src0_sel:WORD_1 src1_sel:DWORD
	v_and_b32_sdwa v35, v28, v208 dst_sel:DWORD dst_unused:UNUSED_PAD src0_sel:WORD_1 src1_sel:DWORD
	v_and_b32_sdwa v32, v26, v208 dst_sel:DWORD dst_unused:UNUSED_PAD src0_sel:WORD_1 src1_sel:DWORD
	v_add3_u32 v34, v29, v34, s57
	s_waitcnt lgkmcnt(0)
	v_fmac_f32_e32 v85, v29, v93
	v_fmac_f32_e32 v85, v27, v92
	v_fmac_f32_e32 v85, v28, v91
	v_fmac_f32_e32 v85, v26, v90
	ds_read_b128 v[90:93], v134 offset:17408
	v_add3_u32 v35, v28, v35, s57
	v_add3_u32 v32, v26, v32, s57
	v_add3_u32 v31, v27, v31, s57
	v_and_b32_e32 v34, 0xffff0000, v34
	s_waitcnt lgkmcnt(0)
	v_fmac_f32_e32 v81, v29, v93
	v_fmac_f32_e32 v81, v27, v92
	v_fmac_f32_e32 v81, v28, v91
	v_fmac_f32_e32 v81, v26, v90
	ds_read_b128 v[90:93], v134 offset:25600
	v_and_b32_e32 v36, 0xffff0000, v35
	v_or_b32_sdwa v35, v34, v31 dst_sel:DWORD dst_unused:UNUSED_PAD src0_sel:DWORD src1_sel:WORD_1
	v_or_b32_sdwa v34, v36, v32 dst_sel:DWORD dst_unused:UNUSED_PAD src0_sel:DWORD src1_sel:WORD_1
	global_store_dwordx2 v[94:95], v[34:35], off offset:512
	s_waitcnt lgkmcnt(0)
	v_fmac_f32_e32 v77, v29, v93
	v_fmac_f32_e32 v77, v27, v92
	v_fmac_f32_e32 v77, v28, v91
	v_fmac_f32_e32 v77, v26, v90
	ds_read_b128 v[90:93], v134 offset:33792
	s_waitcnt lgkmcnt(0)
	v_fmac_f32_e32 v73, v29, v93
	v_fmac_f32_e32 v73, v27, v92
	v_fmac_f32_e32 v73, v28, v91
	v_fmac_f32_e32 v73, v26, v90
	ds_read_b128 v[90:93], v134 offset:41984
	s_waitcnt lgkmcnt(0)
	v_fmac_f32_e32 v69, v29, v93
	v_fmac_f32_e32 v69, v27, v92
	v_fmac_f32_e32 v69, v28, v91
	v_fmac_f32_e32 v69, v26, v90
	ds_read_b128 v[90:93], v134 offset:50176
	s_waitcnt lgkmcnt(0)
	v_fmac_f32_e32 v65, v29, v93
	v_fmac_f32_e32 v65, v27, v92
	v_fmac_f32_e32 v65, v28, v91
	v_fmac_f32_e32 v65, v26, v90
	ds_read_b128 v[90:93], v134 offset:58368
	s_waitcnt lgkmcnt(0)
	v_fmac_f32_e32 v61, v29, v93
	v_fmac_f32_e32 v61, v27, v92
	v_fmac_f32_e32 v61, v28, v91
	v_fmac_f32_e32 v61, v26, v90
	ds_read_b128 v[90:93], v144
	s_waitcnt lgkmcnt(0)
	v_fmac_f32_e32 v57, v29, v93
	v_fmac_f32_e32 v57, v27, v92
	v_fmac_f32_e32 v57, v28, v91
	v_fmac_f32_e32 v57, v26, v90
	ds_read_b128 v[90:93], v145
	s_waitcnt lgkmcnt(0)
	v_fmac_f32_e32 v53, v29, v93
	v_fmac_f32_e32 v53, v27, v92
	v_fmac_f32_e32 v53, v28, v91
	v_fmac_f32_e32 v53, v26, v90
	ds_read_b128 v[90:93], v146
	s_waitcnt lgkmcnt(0)
	v_fmac_f32_e32 v49, v29, v93
	v_fmac_f32_e32 v49, v27, v92
	v_fmac_f32_e32 v49, v28, v91
	v_fmac_f32_e32 v49, v26, v90
	ds_read_b128 v[90:93], v147
	s_waitcnt lgkmcnt(0)
	v_fmac_f32_e32 v45, v29, v93
	v_fmac_f32_e32 v45, v27, v92
	v_fmac_f32_e32 v45, v28, v91
	v_fmac_f32_e32 v45, v26, v90
	ds_read_b128 v[90:93], v148
	s_waitcnt lgkmcnt(0)
	v_fmac_f32_e32 v41, v29, v93
	v_fmac_f32_e32 v41, v27, v92
	v_fmac_f32_e32 v41, v28, v91
	v_fmac_f32_e32 v41, v26, v90
	ds_read_b128 v[90:93], v149
	s_waitcnt lgkmcnt(0)
	v_fmac_f32_e32 v37, v29, v93
	v_fmac_f32_e32 v37, v27, v92
	v_fmac_f32_e32 v37, v28, v91
	v_fmac_f32_e32 v37, v26, v90
	ds_read_b128 v[90:93], v150
	s_waitcnt lgkmcnt(0)
	v_fmac_f32_e32 v33, v29, v93
	v_fmac_f32_e32 v33, v27, v92
	v_fmac_f32_e32 v33, v28, v91
	v_fmac_f32_e32 v33, v26, v90
	ds_read_b128 v[90:93], v151
	s_waitcnt lgkmcnt(0)
	v_fmac_f32_e32 v30, v29, v93
	v_fmac_f32_e32 v30, v27, v92
	v_fmac_f32_e32 v30, v28, v91
	v_fmac_f32_e32 v30, v26, v90
	ds_read_b128 v[90:93], v152
	flat_load_dwordx4 v[96:99], v[118:119] offset:2048
	flat_load_dwordx4 v[100:103], v[116:117] offset:2048
	v_mov_b32_e32 v27, v24
	v_mov_b32_e32 v24, v23
	v_mov_b32_e32 v26, v22
	s_waitcnt lgkmcnt(0)
	v_mov_b32_e32 v29, v92
	v_pk_mul_f32 v[22:23], v[24:25], v[114:115] op_sel_hi:[1,0]
	v_mov_b32_e32 v92, v91
	v_mov_b32_e32 v28, v90
	v_pk_mul_f32 v[22:23], v[22:23], v[92:93]
	ds_read_b128 v[90:93], v134 offset:2048
	v_pk_mul_f32 v[26:27], v[26:27], v[114:115] op_sel_hi:[1,0]
	s_waitcnt vmcnt(0)
	v_mov_b32_e32 v35, v98
	v_pk_mul_f32 v[26:27], v[26:27], v[28:29]
	v_mov_b32_e32 v29, v102
	v_mov_b32_e32 v102, v101
	v_mov_b32_e32 v28, v100
	v_pk_add_f32 v[24:25], v[102:103], 1.0 op_sel_hi:[1,0]
	v_mov_b32_e32 v98, v97
	v_pk_add_f32 v[28:29], v[28:29], 1.0 op_sel_hi:[1,0]
	v_mov_b32_e32 v34, v96
	v_pk_fma_f32 v[22:23], v[22:23], v[24:25], v[98:99]
	v_pk_fma_f32 v[26:27], v[26:27], v[28:29], v[34:35]
	s_waitcnt lgkmcnt(0)
	v_fmac_f32_e32 v89, v23, v93
	v_fmac_f32_e32 v89, v27, v92
	v_fmac_f32_e32 v89, v22, v91
	v_fmac_f32_e32 v89, v26, v90
	ds_read_b128 v[90:93], v134 offset:10240
	v_and_b32_sdwa v25, v26, v208 dst_sel:DWORD dst_unused:UNUSED_PAD src0_sel:WORD_1 src1_sel:DWORD
	v_add3_u32 v28, v26, v25, s57
	v_and_b32_sdwa v25, v23, v208 dst_sel:DWORD dst_unused:UNUSED_PAD src0_sel:WORD_1 src1_sel:DWORD
	v_and_b32_sdwa v29, v22, v208 dst_sel:DWORD dst_unused:UNUSED_PAD src0_sel:WORD_1 src1_sel:DWORD
	s_waitcnt lgkmcnt(0)
	v_fmac_f32_e32 v85, v23, v93
	v_fmac_f32_e32 v85, v27, v92
	v_fmac_f32_e32 v85, v22, v91
	v_fmac_f32_e32 v85, v26, v90
	ds_read_b128 v[90:93], v134 offset:18432
	v_and_b32_sdwa v24, v27, v208 dst_sel:DWORD dst_unused:UNUSED_PAD src0_sel:WORD_1 src1_sel:DWORD
	v_add3_u32 v25, v23, v25, s57
	v_add3_u32 v29, v22, v29, s57
	v_add3_u32 v24, v27, v24, s57
	s_waitcnt lgkmcnt(0)
	v_fmac_f32_e32 v81, v23, v93
	v_fmac_f32_e32 v81, v27, v92
	v_fmac_f32_e32 v81, v22, v91
	v_fmac_f32_e32 v81, v26, v90
	ds_read_b128 v[90:93], v134 offset:26624
	v_and_b32_e32 v25, 0xffff0000, v25
	v_and_b32_e32 v29, 0xffff0000, v29
	v_or_b32_sdwa v25, v25, v24 dst_sel:DWORD dst_unused:UNUSED_PAD src0_sel:DWORD src1_sel:WORD_1
	v_or_b32_sdwa v24, v29, v28 dst_sel:DWORD dst_unused:UNUSED_PAD src0_sel:DWORD src1_sel:WORD_1
	s_waitcnt lgkmcnt(0)
	v_fmac_f32_e32 v77, v23, v93
	v_fmac_f32_e32 v77, v27, v92
	v_fmac_f32_e32 v77, v22, v91
	v_fmac_f32_e32 v77, v26, v90
	ds_read_b128 v[90:93], v134 offset:34816
	global_store_dwordx2 v[94:95], v[24:25], off offset:1024
	s_waitcnt lgkmcnt(0)
	v_fmac_f32_e32 v73, v23, v93
	v_fmac_f32_e32 v73, v27, v92
	v_fmac_f32_e32 v73, v22, v91
	v_fmac_f32_e32 v73, v26, v90
	ds_read_b128 v[90:93], v134 offset:43008
	s_waitcnt lgkmcnt(0)
	v_fmac_f32_e32 v69, v23, v93
	v_fmac_f32_e32 v69, v27, v92
	v_fmac_f32_e32 v69, v22, v91
	v_fmac_f32_e32 v69, v26, v90
	ds_read_b128 v[90:93], v134 offset:51200
	s_waitcnt lgkmcnt(0)
	v_fmac_f32_e32 v65, v23, v93
	v_fmac_f32_e32 v65, v27, v92
	v_fmac_f32_e32 v65, v22, v91
	v_fmac_f32_e32 v65, v26, v90
	ds_read_b128 v[90:93], v134 offset:59392
	s_waitcnt lgkmcnt(0)
	v_fmac_f32_e32 v61, v23, v93
	v_fmac_f32_e32 v61, v27, v92
	v_fmac_f32_e32 v61, v22, v91
	v_fmac_f32_e32 v61, v26, v90
	ds_read_b128 v[90:93], v153
	s_waitcnt lgkmcnt(0)
	v_fmac_f32_e32 v57, v23, v93
	v_fmac_f32_e32 v57, v27, v92
	v_fmac_f32_e32 v57, v22, v91
	v_fmac_f32_e32 v57, v26, v90
	ds_read_b128 v[90:93], v154
	s_waitcnt lgkmcnt(0)
	v_fmac_f32_e32 v53, v23, v93
	v_fmac_f32_e32 v53, v27, v92
	v_fmac_f32_e32 v53, v22, v91
	v_fmac_f32_e32 v53, v26, v90
	ds_read_b128 v[90:93], v155
	s_waitcnt lgkmcnt(0)
	v_fmac_f32_e32 v49, v23, v93
	v_fmac_f32_e32 v49, v27, v92
	v_fmac_f32_e32 v49, v22, v91
	v_fmac_f32_e32 v49, v26, v90
	ds_read_b128 v[90:93], v156
	s_waitcnt lgkmcnt(0)
	v_fmac_f32_e32 v45, v23, v93
	v_fmac_f32_e32 v45, v27, v92
	v_fmac_f32_e32 v45, v22, v91
	v_fmac_f32_e32 v45, v26, v90
	ds_read_b128 v[90:93], v157
	s_waitcnt lgkmcnt(0)
	v_fmac_f32_e32 v41, v23, v93
	v_fmac_f32_e32 v41, v27, v92
	v_fmac_f32_e32 v41, v22, v91
	v_fmac_f32_e32 v41, v26, v90
	ds_read_b128 v[90:93], v158
	s_waitcnt lgkmcnt(0)
	v_fmac_f32_e32 v37, v23, v93
	v_fmac_f32_e32 v37, v27, v92
	v_fmac_f32_e32 v37, v22, v91
	v_fmac_f32_e32 v37, v26, v90
	ds_read_b128 v[90:93], v159
	s_waitcnt lgkmcnt(0)
	v_fmac_f32_e32 v33, v23, v93
	v_fmac_f32_e32 v33, v27, v92
	v_fmac_f32_e32 v33, v22, v91
	v_fmac_f32_e32 v33, v26, v90
	ds_read_b128 v[90:93], v160
	s_waitcnt lgkmcnt(0)
	v_fmac_f32_e32 v30, v23, v93
	v_fmac_f32_e32 v30, v27, v92
	v_fmac_f32_e32 v30, v22, v91
	v_fmac_f32_e32 v30, v26, v90
	ds_read_b128 v[24:27], v161
	flat_load_dwordx4 v[90:93], v[118:119] offset:3072
	flat_load_dwordx4 v[96:99], v[116:117] offset:3072
	v_mov_b32_e32 v22, v18
	v_mov_b32_e32 v23, v20
	v_pk_mul_f32 v[22:23], v[22:23], v[114:115] op_sel_hi:[1,0]
	s_waitcnt lgkmcnt(0)
	v_mov_b32_e32 v28, v24
	v_mov_b32_e32 v29, v26
	v_pk_mul_f32 v[22:23], v[22:23], v[28:29]
	v_mov_b32_e32 v20, v19
	v_pk_mul_f32 v[18:19], v[20:21], v[114:115] op_sel_hi:[1,0]
	v_mov_b32_e32 v26, v25
	v_pk_mul_f32 v[18:19], v[18:19], v[26:27]
	s_waitcnt vmcnt(0)
	v_mov_b32_e32 v34, v90
	v_mov_b32_e32 v28, v96
	v_mov_b32_e32 v29, v98
	v_pk_add_f32 v[28:29], v[28:29], 1.0 op_sel_hi:[1,0]
	v_mov_b32_e32 v35, v92
	v_mov_b32_e32 v98, v97
	v_pk_fma_f32 v[22:23], v[22:23], v[28:29], v[34:35]
	v_pk_add_f32 v[20:21], v[98:99], 1.0 op_sel_hi:[1,0]
	v_mov_b32_e32 v92, v91
	v_pk_fma_f32 v[18:19], v[18:19], v[20:21], v[92:93]
	v_and_b32_sdwa v21, v22, v208 dst_sel:DWORD dst_unused:UNUSED_PAD src0_sel:WORD_1 src1_sel:DWORD
	v_add3_u32 v24, v22, v21, s57
	v_and_b32_sdwa v21, v19, v208 dst_sel:DWORD dst_unused:UNUSED_PAD src0_sel:WORD_1 src1_sel:DWORD
	v_and_b32_sdwa v25, v18, v208 dst_sel:DWORD dst_unused:UNUSED_PAD src0_sel:WORD_1 src1_sel:DWORD
	v_and_b32_sdwa v20, v23, v208 dst_sel:DWORD dst_unused:UNUSED_PAD src0_sel:WORD_1 src1_sel:DWORD
	v_add3_u32 v21, v19, v21, s57
	v_add3_u32 v25, v18, v25, s57
	v_add3_u32 v20, v23, v20, s57
	v_and_b32_e32 v21, 0xffff0000, v21
	v_and_b32_e32 v25, 0xffff0000, v25
	v_or_b32_sdwa v21, v21, v20 dst_sel:DWORD dst_unused:UNUSED_PAD src0_sel:DWORD src1_sel:WORD_1
	v_or_b32_sdwa v20, v25, v24 dst_sel:DWORD dst_unused:UNUSED_PAD src0_sel:DWORD src1_sel:WORD_1
	ds_read_b128 v[24:27], v134 offset:3072
	global_store_dwordx2 v[94:95], v[20:21], off offset:1536
	s_waitcnt lgkmcnt(0)
	v_fmac_f32_e32 v89, v19, v27
	v_fmac_f32_e32 v89, v23, v26
	v_fmac_f32_e32 v89, v18, v25
	v_fmac_f32_e32 v89, v22, v24
	ds_read_b128 v[24:27], v134 offset:11264
	s_waitcnt lgkmcnt(0)
	v_fmac_f32_e32 v85, v19, v27
	v_fmac_f32_e32 v85, v23, v26
	v_fmac_f32_e32 v85, v18, v25
	v_fmac_f32_e32 v85, v22, v24
	ds_read_b128 v[24:27], v134 offset:19456
	s_waitcnt lgkmcnt(0)
	v_fmac_f32_e32 v81, v19, v27
	v_fmac_f32_e32 v81, v23, v26
	v_fmac_f32_e32 v81, v18, v25
	v_fmac_f32_e32 v81, v22, v24
	ds_read_b128 v[24:27], v134 offset:27648
	s_waitcnt lgkmcnt(0)
	v_fmac_f32_e32 v77, v19, v27
	v_fmac_f32_e32 v77, v23, v26
	v_fmac_f32_e32 v77, v18, v25
	v_fmac_f32_e32 v77, v22, v24
	ds_read_b128 v[24:27], v134 offset:35840
	s_waitcnt lgkmcnt(0)
	v_fmac_f32_e32 v73, v19, v27
	v_fmac_f32_e32 v73, v23, v26
	v_fmac_f32_e32 v73, v18, v25
	v_fmac_f32_e32 v73, v22, v24
	ds_read_b128 v[24:27], v134 offset:44032
	s_waitcnt lgkmcnt(0)
	v_fmac_f32_e32 v69, v19, v27
	v_fmac_f32_e32 v69, v23, v26
	v_fmac_f32_e32 v69, v18, v25
	v_fmac_f32_e32 v69, v22, v24
	ds_read_b128 v[24:27], v134 offset:52224
	s_waitcnt lgkmcnt(0)
	v_fmac_f32_e32 v65, v19, v27
	v_fmac_f32_e32 v65, v23, v26
	v_fmac_f32_e32 v65, v18, v25
	v_fmac_f32_e32 v65, v22, v24
	ds_read_b128 v[24:27], v134 offset:60416
	s_waitcnt lgkmcnt(0)
	v_fmac_f32_e32 v61, v19, v27
	v_fmac_f32_e32 v61, v23, v26
	v_fmac_f32_e32 v61, v18, v25
	v_fmac_f32_e32 v61, v22, v24
	ds_read_b128 v[24:27], v162
	s_waitcnt lgkmcnt(0)
	v_fmac_f32_e32 v57, v19, v27
	v_fmac_f32_e32 v57, v23, v26
	v_fmac_f32_e32 v57, v18, v25
	v_fmac_f32_e32 v57, v22, v24
	ds_read_b128 v[24:27], v163
	s_waitcnt lgkmcnt(0)
	v_fmac_f32_e32 v53, v19, v27
	v_fmac_f32_e32 v53, v23, v26
	v_fmac_f32_e32 v53, v18, v25
	v_fmac_f32_e32 v53, v22, v24
	ds_read_b128 v[24:27], v164
	s_waitcnt lgkmcnt(0)
	v_fmac_f32_e32 v49, v19, v27
	v_fmac_f32_e32 v49, v23, v26
	v_fmac_f32_e32 v49, v18, v25
	v_fmac_f32_e32 v49, v22, v24
	ds_read_b128 v[24:27], v165
	s_waitcnt lgkmcnt(0)
	v_fmac_f32_e32 v45, v19, v27
	v_fmac_f32_e32 v45, v23, v26
	v_fmac_f32_e32 v45, v18, v25
	v_fmac_f32_e32 v45, v22, v24
	ds_read_b128 v[24:27], v166
	s_waitcnt lgkmcnt(0)
	v_fmac_f32_e32 v41, v19, v27
	v_fmac_f32_e32 v41, v23, v26
	v_fmac_f32_e32 v41, v18, v25
	v_fmac_f32_e32 v41, v22, v24
	ds_read_b128 v[24:27], v167
	s_waitcnt lgkmcnt(0)
	v_fmac_f32_e32 v37, v19, v27
	v_fmac_f32_e32 v37, v23, v26
	v_fmac_f32_e32 v37, v18, v25
	v_fmac_f32_e32 v37, v22, v24
	ds_read_b128 v[24:27], v168
	s_waitcnt lgkmcnt(0)
	v_fmac_f32_e32 v33, v19, v27
	v_fmac_f32_e32 v33, v23, v26
	v_fmac_f32_e32 v33, v18, v25
	v_fmac_f32_e32 v33, v22, v24
	ds_read_b128 v[24:27], v169
	s_waitcnt lgkmcnt(0)
	v_fmac_f32_e32 v30, v19, v27
	v_fmac_f32_e32 v30, v23, v26
	v_fmac_f32_e32 v30, v18, v25
	v_fmac_f32_e32 v30, v22, v24
	v_add_co_u32_e32 v18, vcc, s56, v118
	ds_read_b128 v[24:27], v170
	s_nop 0
	v_addc_co_u32_e32 v19, vcc, 0, v119, vcc
	v_add_co_u32_e32 v20, vcc, s56, v116
	flat_load_dwordx4 v[90:93], v[18:19]
	s_nop 0
	v_addc_co_u32_e32 v21, vcc, 0, v117, vcc
	flat_load_dwordx4 v[96:99], v[20:21]
	v_mov_b32_e32 v22, v14
	v_mov_b32_e32 v23, v16
	v_pk_mul_f32 v[22:23], v[22:23], v[114:115] op_sel_hi:[1,0]
	s_waitcnt lgkmcnt(0)
	v_mov_b32_e32 v28, v24
	v_mov_b32_e32 v29, v26
	v_pk_mul_f32 v[22:23], v[22:23], v[28:29]
	v_mov_b32_e32 v16, v15
	v_pk_mul_f32 v[14:15], v[16:17], v[114:115] op_sel_hi:[1,0]
	v_mov_b32_e32 v26, v25
	v_pk_mul_f32 v[14:15], v[14:15], v[26:27]
	s_waitcnt vmcnt(0)
	v_mov_b32_e32 v34, v90
	v_mov_b32_e32 v35, v92
	v_mov_b32_e32 v92, v91
	v_mov_b32_e32 v28, v96
	v_mov_b32_e32 v29, v98
	v_pk_add_f32 v[28:29], v[28:29], 1.0 op_sel_hi:[1,0]
	v_mov_b32_e32 v98, v97
	v_pk_fma_f32 v[22:23], v[22:23], v[28:29], v[34:35]
	v_pk_add_f32 v[16:17], v[98:99], 1.0 op_sel_hi:[1,0]
	s_nop 0
	v_pk_fma_f32 v[14:15], v[14:15], v[16:17], v[92:93]
	v_and_b32_sdwa v17, v22, v208 dst_sel:DWORD dst_unused:UNUSED_PAD src0_sel:WORD_1 src1_sel:DWORD
	v_add3_u32 v24, v22, v17, s57
	v_and_b32_sdwa v17, v15, v208 dst_sel:DWORD dst_unused:UNUSED_PAD src0_sel:WORD_1 src1_sel:DWORD
	v_and_b32_sdwa v25, v14, v208 dst_sel:DWORD dst_unused:UNUSED_PAD src0_sel:WORD_1 src1_sel:DWORD
	v_and_b32_sdwa v16, v23, v208 dst_sel:DWORD dst_unused:UNUSED_PAD src0_sel:WORD_1 src1_sel:DWORD
	v_add3_u32 v17, v15, v17, s57
	v_add3_u32 v25, v14, v25, s57
	v_add3_u32 v16, v23, v16, s57
	v_and_b32_e32 v17, 0xffff0000, v17
	v_and_b32_e32 v25, 0xffff0000, v25
	v_or_b32_sdwa v17, v17, v16 dst_sel:DWORD dst_unused:UNUSED_PAD src0_sel:DWORD src1_sel:WORD_1
	v_or_b32_sdwa v16, v25, v24 dst_sel:DWORD dst_unused:UNUSED_PAD src0_sel:DWORD src1_sel:WORD_1
	ds_read_b128 v[24:27], v134 offset:4096
	global_store_dwordx2 v[94:95], v[16:17], off offset:2048
	s_waitcnt lgkmcnt(0)
	v_fmac_f32_e32 v89, v15, v27
	v_fmac_f32_e32 v89, v23, v26
	v_fmac_f32_e32 v89, v14, v25
	v_fmac_f32_e32 v89, v22, v24
	ds_read_b128 v[24:27], v134 offset:12288
	s_waitcnt lgkmcnt(0)
	v_fmac_f32_e32 v85, v15, v27
	v_fmac_f32_e32 v85, v23, v26
	v_fmac_f32_e32 v85, v14, v25
	v_fmac_f32_e32 v85, v22, v24
	ds_read_b128 v[24:27], v134 offset:20480
	s_waitcnt lgkmcnt(0)
	v_fmac_f32_e32 v81, v15, v27
	v_fmac_f32_e32 v81, v23, v26
	v_fmac_f32_e32 v81, v14, v25
	v_fmac_f32_e32 v81, v22, v24
	ds_read_b128 v[24:27], v134 offset:28672
	s_waitcnt lgkmcnt(0)
	v_fmac_f32_e32 v77, v15, v27
	v_fmac_f32_e32 v77, v23, v26
	v_fmac_f32_e32 v77, v14, v25
	v_fmac_f32_e32 v77, v22, v24
	ds_read_b128 v[24:27], v134 offset:36864
	s_waitcnt lgkmcnt(0)
	v_fmac_f32_e32 v73, v15, v27
	v_fmac_f32_e32 v73, v23, v26
	v_fmac_f32_e32 v73, v14, v25
	v_fmac_f32_e32 v73, v22, v24
	ds_read_b128 v[24:27], v134 offset:45056
	s_waitcnt lgkmcnt(0)
	v_fmac_f32_e32 v69, v15, v27
	v_fmac_f32_e32 v69, v23, v26
	v_fmac_f32_e32 v69, v14, v25
	v_fmac_f32_e32 v69, v22, v24
	ds_read_b128 v[24:27], v134 offset:53248
	s_waitcnt lgkmcnt(0)
	v_fmac_f32_e32 v65, v15, v27
	v_fmac_f32_e32 v65, v23, v26
	v_fmac_f32_e32 v65, v14, v25
	v_fmac_f32_e32 v65, v22, v24
	ds_read_b128 v[24:27], v134 offset:61440
	s_waitcnt lgkmcnt(0)
	v_fmac_f32_e32 v61, v15, v27
	v_fmac_f32_e32 v61, v23, v26
	v_fmac_f32_e32 v61, v14, v25
	v_fmac_f32_e32 v61, v22, v24
	ds_read_b128 v[24:27], v171
	s_waitcnt lgkmcnt(0)
	v_fmac_f32_e32 v57, v15, v27
	v_fmac_f32_e32 v57, v23, v26
	v_fmac_f32_e32 v57, v14, v25
	v_fmac_f32_e32 v57, v22, v24
	ds_read_b128 v[24:27], v172
	s_waitcnt lgkmcnt(0)
	v_fmac_f32_e32 v53, v15, v27
	v_fmac_f32_e32 v53, v23, v26
	v_fmac_f32_e32 v53, v14, v25
	v_fmac_f32_e32 v53, v22, v24
	ds_read_b128 v[24:27], v173
	s_waitcnt lgkmcnt(0)
	v_fmac_f32_e32 v49, v15, v27
	v_fmac_f32_e32 v49, v23, v26
	v_fmac_f32_e32 v49, v14, v25
	v_fmac_f32_e32 v49, v22, v24
	ds_read_b128 v[24:27], v174
	s_waitcnt lgkmcnt(0)
	v_fmac_f32_e32 v45, v15, v27
	v_fmac_f32_e32 v45, v23, v26
	v_fmac_f32_e32 v45, v14, v25
	v_fmac_f32_e32 v45, v22, v24
	ds_read_b128 v[24:27], v175
	s_waitcnt lgkmcnt(0)
	v_fmac_f32_e32 v41, v15, v27
	v_fmac_f32_e32 v41, v23, v26
	v_fmac_f32_e32 v41, v14, v25
	v_fmac_f32_e32 v41, v22, v24
	ds_read_b128 v[24:27], v176
	s_waitcnt lgkmcnt(0)
	v_fmac_f32_e32 v37, v15, v27
	v_fmac_f32_e32 v37, v23, v26
	v_fmac_f32_e32 v37, v14, v25
	v_fmac_f32_e32 v37, v22, v24
	ds_read_b128 v[24:27], v177
	s_waitcnt lgkmcnt(0)
	v_fmac_f32_e32 v33, v15, v27
	v_fmac_f32_e32 v33, v23, v26
	v_fmac_f32_e32 v33, v14, v25
	v_fmac_f32_e32 v33, v22, v24
	ds_read_b128 v[24:27], v178
	s_waitcnt lgkmcnt(0)
	v_fmac_f32_e32 v30, v15, v27
	v_fmac_f32_e32 v30, v23, v26
	v_fmac_f32_e32 v30, v14, v25
	v_fmac_f32_e32 v30, v22, v24
	ds_read_b128 v[22:25], v179
	flat_load_dwordx4 v[26:29], v[18:19] offset:1024
	flat_load_dwordx4 v[90:93], v[20:21] offset:1024
	v_mov_b32_e32 v15, v12
	v_mov_b32_e32 v12, v11
	v_mov_b32_e32 v14, v10
	s_waitcnt lgkmcnt(0)
	v_mov_b32_e32 v17, v24
	v_pk_mul_f32 v[10:11], v[12:13], v[114:115] op_sel_hi:[1,0]
	v_mov_b32_e32 v24, v23
	v_mov_b32_e32 v16, v22
	v_pk_mul_f32 v[10:11], v[10:11], v[24:25]
	ds_read_b128 v[22:25], v134 offset:5120
	v_pk_mul_f32 v[14:15], v[14:15], v[114:115] op_sel_hi:[1,0]
	s_waitcnt vmcnt(0)
	v_mov_b32_e32 v35, v28
	v_pk_mul_f32 v[14:15], v[14:15], v[16:17]
	v_mov_b32_e32 v17, v92
	v_mov_b32_e32 v92, v91
	v_mov_b32_e32 v16, v90
	v_pk_add_f32 v[12:13], v[92:93], 1.0 op_sel_hi:[1,0]
	v_mov_b32_e32 v28, v27
	v_pk_add_f32 v[16:17], v[16:17], 1.0 op_sel_hi:[1,0]
	v_mov_b32_e32 v34, v26
	v_pk_fma_f32 v[10:11], v[10:11], v[12:13], v[28:29]
	v_pk_fma_f32 v[14:15], v[14:15], v[16:17], v[34:35]
	s_waitcnt lgkmcnt(0)
	v_fmac_f32_e32 v89, v11, v25
	v_fmac_f32_e32 v89, v15, v24
	v_fmac_f32_e32 v89, v10, v23
	v_fmac_f32_e32 v89, v14, v22
	ds_read_b128 v[22:25], v134 offset:13312
	v_and_b32_sdwa v13, v14, v208 dst_sel:DWORD dst_unused:UNUSED_PAD src0_sel:WORD_1 src1_sel:DWORD
	v_add3_u32 v16, v14, v13, s57
	v_and_b32_sdwa v13, v11, v208 dst_sel:DWORD dst_unused:UNUSED_PAD src0_sel:WORD_1 src1_sel:DWORD
	v_and_b32_sdwa v17, v10, v208 dst_sel:DWORD dst_unused:UNUSED_PAD src0_sel:WORD_1 src1_sel:DWORD
	s_waitcnt lgkmcnt(0)
	v_fmac_f32_e32 v85, v11, v25
	v_fmac_f32_e32 v85, v15, v24
	v_fmac_f32_e32 v85, v10, v23
	v_fmac_f32_e32 v85, v14, v22
	ds_read_b128 v[22:25], v134 offset:21504
	v_and_b32_sdwa v12, v15, v208 dst_sel:DWORD dst_unused:UNUSED_PAD src0_sel:WORD_1 src1_sel:DWORD
	v_add3_u32 v13, v11, v13, s57
	v_add3_u32 v17, v10, v17, s57
	v_add3_u32 v12, v15, v12, s57
	s_waitcnt lgkmcnt(0)
	v_fmac_f32_e32 v81, v11, v25
	v_fmac_f32_e32 v81, v15, v24
	v_fmac_f32_e32 v81, v10, v23
	v_fmac_f32_e32 v81, v14, v22
	ds_read_b128 v[22:25], v134 offset:29696
	v_and_b32_e32 v13, 0xffff0000, v13
	v_and_b32_e32 v17, 0xffff0000, v17
	v_or_b32_sdwa v13, v13, v12 dst_sel:DWORD dst_unused:UNUSED_PAD src0_sel:DWORD src1_sel:WORD_1
	v_or_b32_sdwa v12, v17, v16 dst_sel:DWORD dst_unused:UNUSED_PAD src0_sel:DWORD src1_sel:WORD_1
	s_waitcnt lgkmcnt(0)
	v_fmac_f32_e32 v77, v11, v25
	v_fmac_f32_e32 v77, v15, v24
	v_fmac_f32_e32 v77, v10, v23
	v_fmac_f32_e32 v77, v14, v22
	ds_read_b128 v[22:25], v134 offset:37888
	global_store_dwordx2 v[94:95], v[12:13], off offset:2560
	s_waitcnt lgkmcnt(0)
	v_fmac_f32_e32 v73, v11, v25
	v_fmac_f32_e32 v73, v15, v24
	v_fmac_f32_e32 v73, v10, v23
	v_fmac_f32_e32 v73, v14, v22
	ds_read_b128 v[22:25], v134 offset:46080
	s_waitcnt lgkmcnt(0)
	v_fmac_f32_e32 v69, v11, v25
	v_fmac_f32_e32 v69, v15, v24
	v_fmac_f32_e32 v69, v10, v23
	v_fmac_f32_e32 v69, v14, v22
	ds_read_b128 v[22:25], v134 offset:54272
	s_waitcnt lgkmcnt(0)
	v_fmac_f32_e32 v65, v11, v25
	v_fmac_f32_e32 v65, v15, v24
	v_fmac_f32_e32 v65, v10, v23
	v_fmac_f32_e32 v65, v14, v22
	ds_read_b128 v[22:25], v134 offset:62464
	s_waitcnt lgkmcnt(0)
	v_fmac_f32_e32 v61, v11, v25
	v_fmac_f32_e32 v61, v15, v24
	v_fmac_f32_e32 v61, v10, v23
	v_fmac_f32_e32 v61, v14, v22
	ds_read_b128 v[22:25], v180
	s_waitcnt lgkmcnt(0)
	v_fmac_f32_e32 v57, v11, v25
	v_fmac_f32_e32 v57, v15, v24
	v_fmac_f32_e32 v57, v10, v23
	v_fmac_f32_e32 v57, v14, v22
	ds_read_b128 v[22:25], v181
	s_waitcnt lgkmcnt(0)
	v_fmac_f32_e32 v53, v11, v25
	v_fmac_f32_e32 v53, v15, v24
	v_fmac_f32_e32 v53, v10, v23
	v_fmac_f32_e32 v53, v14, v22
	ds_read_b128 v[22:25], v182
	s_waitcnt lgkmcnt(0)
	v_fmac_f32_e32 v49, v11, v25
	v_fmac_f32_e32 v49, v15, v24
	v_fmac_f32_e32 v49, v10, v23
	v_fmac_f32_e32 v49, v14, v22
	ds_read_b128 v[22:25], v183
	s_waitcnt lgkmcnt(0)
	v_fmac_f32_e32 v45, v11, v25
	v_fmac_f32_e32 v45, v15, v24
	v_fmac_f32_e32 v45, v10, v23
	v_fmac_f32_e32 v45, v14, v22
	ds_read_b128 v[22:25], v184
	s_waitcnt lgkmcnt(0)
	v_fmac_f32_e32 v41, v11, v25
	v_fmac_f32_e32 v41, v15, v24
	v_fmac_f32_e32 v41, v10, v23
	v_fmac_f32_e32 v41, v14, v22
	ds_read_b128 v[22:25], v185
	s_waitcnt lgkmcnt(0)
	v_fmac_f32_e32 v37, v11, v25
	v_fmac_f32_e32 v37, v15, v24
	v_fmac_f32_e32 v37, v10, v23
	v_fmac_f32_e32 v37, v14, v22
	ds_read_b128 v[22:25], v186
	s_waitcnt lgkmcnt(0)
	v_fmac_f32_e32 v33, v11, v25
	v_fmac_f32_e32 v33, v15, v24
	v_fmac_f32_e32 v33, v10, v23
	v_fmac_f32_e32 v33, v14, v22
	ds_read_b128 v[22:25], v187
	s_waitcnt lgkmcnt(0)
	v_fmac_f32_e32 v30, v11, v25
	v_fmac_f32_e32 v30, v15, v24
	v_fmac_f32_e32 v30, v10, v23
	v_fmac_f32_e32 v30, v14, v22
	ds_read_b128 v[12:15], v188
	flat_load_dwordx4 v[22:25], v[18:19] offset:2048
	flat_load_dwordx4 v[26:29], v[20:21] offset:2048
	v_mov_b32_e32 v10, v6
	v_mov_b32_e32 v11, v8
	v_pk_mul_f32 v[10:11], v[10:11], v[114:115] op_sel_hi:[1,0]
	s_waitcnt lgkmcnt(0)
	v_mov_b32_e32 v16, v12
	v_mov_b32_e32 v17, v14
	v_pk_mul_f32 v[10:11], v[10:11], v[16:17]
	v_mov_b32_e32 v8, v7
	v_pk_mul_f32 v[6:7], v[8:9], v[114:115] op_sel_hi:[1,0]
	v_mov_b32_e32 v14, v13
	v_pk_mul_f32 v[6:7], v[6:7], v[14:15]
	s_waitcnt vmcnt(0)
	v_mov_b32_e32 v34, v22
	v_mov_b32_e32 v16, v26
	v_mov_b32_e32 v17, v28
	v_pk_add_f32 v[16:17], v[16:17], 1.0 op_sel_hi:[1,0]
	v_mov_b32_e32 v35, v24
	v_mov_b32_e32 v28, v27
	v_pk_fma_f32 v[10:11], v[10:11], v[16:17], v[34:35]
	v_pk_add_f32 v[8:9], v[28:29], 1.0 op_sel_hi:[1,0]
	v_mov_b32_e32 v24, v23
	v_pk_fma_f32 v[6:7], v[6:7], v[8:9], v[24:25]
	v_and_b32_sdwa v9, v10, v208 dst_sel:DWORD dst_unused:UNUSED_PAD src0_sel:WORD_1 src1_sel:DWORD
	v_add3_u32 v12, v10, v9, s57
	v_and_b32_sdwa v9, v7, v208 dst_sel:DWORD dst_unused:UNUSED_PAD src0_sel:WORD_1 src1_sel:DWORD
	v_and_b32_sdwa v13, v6, v208 dst_sel:DWORD dst_unused:UNUSED_PAD src0_sel:WORD_1 src1_sel:DWORD
	v_and_b32_sdwa v8, v11, v208 dst_sel:DWORD dst_unused:UNUSED_PAD src0_sel:WORD_1 src1_sel:DWORD
	v_add3_u32 v9, v7, v9, s57
	v_add3_u32 v13, v6, v13, s57
	v_add3_u32 v8, v11, v8, s57
	v_and_b32_e32 v9, 0xffff0000, v9
	v_and_b32_e32 v13, 0xffff0000, v13
	v_or_b32_sdwa v9, v9, v8 dst_sel:DWORD dst_unused:UNUSED_PAD src0_sel:DWORD src1_sel:WORD_1
	v_or_b32_sdwa v8, v13, v12 dst_sel:DWORD dst_unused:UNUSED_PAD src0_sel:DWORD src1_sel:WORD_1
	ds_read_b128 v[12:15], v134 offset:6144
	global_store_dwordx2 v[94:95], v[8:9], off offset:3072
	s_waitcnt lgkmcnt(0)
	v_fmac_f32_e32 v89, v7, v15
	v_fmac_f32_e32 v89, v11, v14
	v_fmac_f32_e32 v89, v6, v13
	v_fmac_f32_e32 v89, v10, v12
	ds_read_b128 v[12:15], v134 offset:14336
	s_waitcnt lgkmcnt(0)
	v_fmac_f32_e32 v85, v7, v15
	v_fmac_f32_e32 v85, v11, v14
	v_fmac_f32_e32 v85, v6, v13
	v_fmac_f32_e32 v85, v10, v12
	ds_read_b128 v[12:15], v134 offset:22528
	s_waitcnt lgkmcnt(0)
	v_fmac_f32_e32 v81, v7, v15
	v_fmac_f32_e32 v81, v11, v14
	v_fmac_f32_e32 v81, v6, v13
	v_fmac_f32_e32 v81, v10, v12
	ds_read_b128 v[12:15], v134 offset:30720
	s_waitcnt lgkmcnt(0)
	v_fmac_f32_e32 v77, v7, v15
	v_fmac_f32_e32 v77, v11, v14
	v_fmac_f32_e32 v77, v6, v13
	v_fmac_f32_e32 v77, v10, v12
	ds_read_b128 v[12:15], v134 offset:38912
	s_waitcnt lgkmcnt(0)
	v_fmac_f32_e32 v73, v7, v15
	v_fmac_f32_e32 v73, v11, v14
	v_fmac_f32_e32 v73, v6, v13
	v_fmac_f32_e32 v73, v10, v12
	ds_read_b128 v[12:15], v134 offset:47104
	s_waitcnt lgkmcnt(0)
	v_fmac_f32_e32 v69, v7, v15
	v_fmac_f32_e32 v69, v11, v14
	v_fmac_f32_e32 v69, v6, v13
	v_fmac_f32_e32 v69, v10, v12
	ds_read_b128 v[12:15], v134 offset:55296
	s_waitcnt lgkmcnt(0)
	v_fmac_f32_e32 v65, v7, v15
	v_fmac_f32_e32 v65, v11, v14
	v_fmac_f32_e32 v65, v6, v13
	v_fmac_f32_e32 v65, v10, v12
	ds_read_b128 v[12:15], v134 offset:63488
	s_waitcnt lgkmcnt(0)
	v_fmac_f32_e32 v61, v7, v15
	v_fmac_f32_e32 v61, v11, v14
	v_fmac_f32_e32 v61, v6, v13
	v_fmac_f32_e32 v61, v10, v12
	ds_read_b128 v[12:15], v189
	s_waitcnt lgkmcnt(0)
	v_fmac_f32_e32 v57, v7, v15
	v_fmac_f32_e32 v57, v11, v14
	v_fmac_f32_e32 v57, v6, v13
	v_fmac_f32_e32 v57, v10, v12
	ds_read_b128 v[12:15], v191
	s_waitcnt lgkmcnt(0)
	v_fmac_f32_e32 v53, v7, v15
	v_fmac_f32_e32 v53, v11, v14
	v_fmac_f32_e32 v53, v6, v13
	v_fmac_f32_e32 v53, v10, v12
	ds_read_b128 v[12:15], v192
	s_waitcnt lgkmcnt(0)
	v_fmac_f32_e32 v49, v7, v15
	v_fmac_f32_e32 v49, v11, v14
	v_fmac_f32_e32 v49, v6, v13
	v_fmac_f32_e32 v49, v10, v12
	ds_read_b128 v[12:15], v193
	s_waitcnt lgkmcnt(0)
	v_fmac_f32_e32 v45, v7, v15
	v_fmac_f32_e32 v45, v11, v14
	v_fmac_f32_e32 v45, v6, v13
	v_fmac_f32_e32 v45, v10, v12
	ds_read_b128 v[12:15], v194
	s_waitcnt lgkmcnt(0)
	v_fmac_f32_e32 v41, v7, v15
	v_fmac_f32_e32 v41, v11, v14
	v_fmac_f32_e32 v41, v6, v13
	v_fmac_f32_e32 v41, v10, v12
	ds_read_b128 v[12:15], v195
	s_waitcnt lgkmcnt(0)
	v_fmac_f32_e32 v37, v7, v15
	v_fmac_f32_e32 v37, v11, v14
	v_fmac_f32_e32 v37, v6, v13
	v_fmac_f32_e32 v37, v10, v12
	ds_read_b128 v[12:15], v196
	s_waitcnt lgkmcnt(0)
	v_fmac_f32_e32 v33, v7, v15
	v_fmac_f32_e32 v33, v11, v14
	v_fmac_f32_e32 v33, v6, v13
	v_fmac_f32_e32 v33, v10, v12
	ds_read_b128 v[12:15], v197
	s_waitcnt lgkmcnt(0)
	v_fmac_f32_e32 v30, v7, v15
	v_fmac_f32_e32 v30, v11, v14
	v_fmac_f32_e32 v30, v6, v13
	v_fmac_f32_e32 v30, v10, v12
	ds_read_b128 v[8:11], v198
	flat_load_dwordx4 v[12:15], v[18:19] offset:3072
	s_nop 0
	flat_load_dwordx4 v[16:19], v[20:21] offset:3072
	v_mov_b32_e32 v6, v2
	v_mov_b32_e32 v7, v4
	v_pk_mul_f32 v[6:7], v[6:7], v[114:115] op_sel_hi:[1,0]
	s_waitcnt lgkmcnt(0)
	v_mov_b32_e32 v20, v8
	v_mov_b32_e32 v21, v10
	v_pk_mul_f32 v[6:7], v[6:7], v[20:21]
	v_mov_b32_e32 v4, v3
	v_pk_mul_f32 v[2:3], v[4:5], v[114:115] op_sel_hi:[1,0]
	v_mov_b32_e32 v10, v9
	v_pk_mul_f32 v[2:3], v[2:3], v[10:11]
	s_waitcnt vmcnt(0)
	v_mov_b32_e32 v22, v12
	v_mov_b32_e32 v20, v16
	v_mov_b32_e32 v21, v18
	v_pk_add_f32 v[20:21], v[20:21], 1.0 op_sel_hi:[1,0]
	v_mov_b32_e32 v23, v14
	v_mov_b32_e32 v18, v17
	v_pk_fma_f32 v[6:7], v[6:7], v[20:21], v[22:23]
	v_pk_add_f32 v[4:5], v[18:19], 1.0 op_sel_hi:[1,0]
	v_mov_b32_e32 v14, v13
	v_pk_fma_f32 v[2:3], v[2:3], v[4:5], v[14:15]
	v_and_b32_sdwa v5, v6, v208 dst_sel:DWORD dst_unused:UNUSED_PAD src0_sel:WORD_1 src1_sel:DWORD
	v_add3_u32 v8, v6, v5, s57
	v_and_b32_sdwa v5, v3, v208 dst_sel:DWORD dst_unused:UNUSED_PAD src0_sel:WORD_1 src1_sel:DWORD
	v_and_b32_sdwa v9, v2, v208 dst_sel:DWORD dst_unused:UNUSED_PAD src0_sel:WORD_1 src1_sel:DWORD
	v_and_b32_sdwa v4, v7, v208 dst_sel:DWORD dst_unused:UNUSED_PAD src0_sel:WORD_1 src1_sel:DWORD
	v_add3_u32 v5, v3, v5, s57
	v_add3_u32 v9, v2, v9, s57
	v_add3_u32 v4, v7, v4, s57
	v_and_b32_e32 v5, 0xffff0000, v5
	v_and_b32_e32 v9, 0xffff0000, v9
	v_or_b32_sdwa v5, v5, v4 dst_sel:DWORD dst_unused:UNUSED_PAD src0_sel:DWORD src1_sel:WORD_1
	v_or_b32_sdwa v4, v9, v8 dst_sel:DWORD dst_unused:UNUSED_PAD src0_sel:DWORD src1_sel:WORD_1
	ds_read_b128 v[8:11], v134 offset:7168
	global_store_dwordx2 v[94:95], v[4:5], off offset:3584
	s_waitcnt lgkmcnt(0)
	v_fmac_f32_e32 v89, v3, v11
	v_fmac_f32_e32 v89, v7, v10
	v_fmac_f32_e32 v89, v2, v9
	v_fmac_f32_e32 v89, v6, v8
	ds_read_b128 v[8:11], v134 offset:15360
	s_waitcnt lgkmcnt(0)
	v_fmac_f32_e32 v85, v3, v11
	v_fmac_f32_e32 v85, v7, v10
	v_fmac_f32_e32 v85, v2, v9
	v_fmac_f32_e32 v85, v6, v8
	ds_read_b128 v[8:11], v134 offset:23552
	s_waitcnt lgkmcnt(0)
	v_fmac_f32_e32 v81, v3, v11
	v_fmac_f32_e32 v81, v7, v10
	v_fmac_f32_e32 v81, v2, v9
	v_fmac_f32_e32 v81, v6, v8
	ds_read_b128 v[8:11], v134 offset:31744
	s_waitcnt lgkmcnt(0)
	v_fmac_f32_e32 v77, v3, v11
	v_fmac_f32_e32 v77, v7, v10
	v_fmac_f32_e32 v77, v2, v9
	v_fmac_f32_e32 v77, v6, v8
	ds_read_b128 v[8:11], v134 offset:39936
	s_waitcnt lgkmcnt(0)
	v_fmac_f32_e32 v73, v3, v11
	v_fmac_f32_e32 v73, v7, v10
	v_fmac_f32_e32 v73, v2, v9
	v_fmac_f32_e32 v73, v6, v8
	ds_read_b128 v[8:11], v134 offset:48128
	s_waitcnt lgkmcnt(0)
	v_fmac_f32_e32 v69, v3, v11
	v_fmac_f32_e32 v69, v7, v10
	v_fmac_f32_e32 v69, v2, v9
	v_fmac_f32_e32 v69, v6, v8
	ds_read_b128 v[8:11], v134 offset:56320
	s_waitcnt lgkmcnt(0)
	v_fmac_f32_e32 v65, v3, v11
	v_fmac_f32_e32 v65, v7, v10
	v_fmac_f32_e32 v65, v2, v9
	v_fmac_f32_e32 v65, v6, v8
	ds_read_b128 v[8:11], v134 offset:64512
	s_waitcnt lgkmcnt(0)
	v_fmac_f32_e32 v61, v3, v11
	v_fmac_f32_e32 v61, v7, v10
	v_fmac_f32_e32 v61, v2, v9
	v_fmac_f32_e32 v61, v6, v8
	ds_read_b128 v[8:11], v199
	s_waitcnt lgkmcnt(0)
	v_fmac_f32_e32 v57, v3, v11
	v_fmac_f32_e32 v57, v7, v10
	v_fmac_f32_e32 v57, v2, v9
	v_fmac_f32_e32 v57, v6, v8
	ds_read_b128 v[8:11], v200
	s_waitcnt lgkmcnt(0)
	v_fmac_f32_e32 v53, v3, v11
	v_fmac_f32_e32 v53, v7, v10
	v_fmac_f32_e32 v53, v2, v9
	v_fmac_f32_e32 v53, v6, v8
	ds_read_b128 v[8:11], v201
	s_waitcnt lgkmcnt(0)
	v_fmac_f32_e32 v49, v3, v11
	v_fmac_f32_e32 v49, v7, v10
	v_fmac_f32_e32 v49, v2, v9
	v_fmac_f32_e32 v49, v6, v8
	ds_read_b128 v[8:11], v202
	s_waitcnt lgkmcnt(0)
	v_fmac_f32_e32 v45, v3, v11
	v_fmac_f32_e32 v45, v7, v10
	v_fmac_f32_e32 v45, v2, v9
	v_fmac_f32_e32 v45, v6, v8
	ds_read_b128 v[8:11], v203
	s_waitcnt lgkmcnt(0)
	v_fmac_f32_e32 v41, v3, v11
	v_fmac_f32_e32 v41, v7, v10
	v_fmac_f32_e32 v41, v2, v9
	v_fmac_f32_e32 v41, v6, v8
	ds_read_b128 v[8:11], v204
	s_waitcnt lgkmcnt(0)
	v_fmac_f32_e32 v37, v3, v11
	v_fmac_f32_e32 v37, v7, v10
	v_fmac_f32_e32 v37, v2, v9
	v_fmac_f32_e32 v37, v6, v8
	ds_read_b128 v[8:11], v205
	s_waitcnt lgkmcnt(0)
	v_fmac_f32_e32 v33, v3, v11
	v_fmac_f32_e32 v33, v7, v10
	v_fmac_f32_e32 v33, v2, v9
	v_fmac_f32_e32 v33, v6, v8
	ds_read_b128 v[8:11], v206
	s_waitcnt lgkmcnt(0)
	v_fmac_f32_e32 v30, v3, v11
	v_fmac_f32_e32 v30, v7, v10
	v_fmac_f32_e32 v30, v2, v9
	v_fmac_f32_e32 v30, v6, v8
	ds_bpermute_b32 v6, v1, v81
	ds_bpermute_b32 v7, v1, v77
	ds_bpermute_b32 v22, v1, v49
	ds_bpermute_b32 v10, v1, v73
	ds_bpermute_b32 v24, v1, v41
	s_waitcnt lgkmcnt(4)
	v_add_f32_e32 v6, v81, v6
	ds_bpermute_b32 v8, v128, v6
	s_waitcnt lgkmcnt(4)
	v_add_f32_e32 v7, v77, v7
	ds_bpermute_b32 v9, v128, v7
	s_waitcnt lgkmcnt(4)
	v_add_f32_e32 v22, v49, v22
	ds_bpermute_b32 v23, v128, v22
	s_waitcnt lgkmcnt(2)
	v_add_f32_e32 v6, v6, v8
	ds_bpermute_b32 v8, v129, v6
	s_waitcnt lgkmcnt(2)
	v_add_f32_e32 v7, v7, v9
	ds_bpermute_b32 v9, v129, v7
	s_waitcnt lgkmcnt(2)
	v_add_f32_e32 v22, v22, v23
	ds_bpermute_b32 v23, v129, v22
	s_waitcnt lgkmcnt(2)
	v_add_f32_e32 v6, v6, v8
	ds_bpermute_b32 v8, v130, v6
	s_waitcnt lgkmcnt(2)
	v_add_f32_e32 v7, v7, v9
	ds_bpermute_b32 v9, v130, v7
	v_add_f32_e32 v10, v73, v10
	s_waitcnt lgkmcnt(2)
	v_add_f32_e32 v22, v22, v23
	s_waitcnt lgkmcnt(1)
	v_add_f32_e32 v6, v6, v8
	ds_bpermute_b32 v8, v131, v6
	s_waitcnt lgkmcnt(1)
	v_add_f32_e32 v9, v7, v9
	ds_bpermute_b32 v12, v131, v9
	v_add_f32_e32 v23, v41, v24
	ds_bpermute_b32 v11, v128, v10
	s_waitcnt lgkmcnt(2)
	v_add_f32_e32 v6, v6, v8
	ds_bpermute_b32 v8, v1, v69
	ds_bpermute_b32 v24, v128, v23
	ds_bpermute_b32 v27, v130, v22
	s_waitcnt lgkmcnt(3)
	v_add_f32_e32 v10, v10, v11
	ds_bpermute_b32 v11, v129, v10
	s_waitcnt lgkmcnt(3)
	v_add_f32_e32 v13, v69, v8
	ds_bpermute_b32 v14, v128, v13
	v_add_f32_e32 v8, v9, v12
	s_waitcnt lgkmcnt(3)
	v_add_f32_e32 v23, v23, v24
	ds_bpermute_b32 v24, v129, v23
	s_waitcnt lgkmcnt(2)
	v_add_f32_e32 v10, v10, v11
	s_waitcnt lgkmcnt(1)
	v_add_f32_e32 v12, v13, v14
	ds_bpermute_b32 v14, v1, v65
	v_add_f32_e32 v22, v22, v27
	s_waitcnt lgkmcnt(1)
	v_add_f32_e32 v23, v23, v24
	ds_bpermute_b32 v11, v130, v10
	ds_bpermute_b32 v27, v131, v22
	s_waitcnt lgkmcnt(2)
	v_add_f32_e32 v14, v65, v14
	ds_bpermute_b32 v15, v128, v14
	ds_bpermute_b32 v24, v130, v23
	s_waitcnt lgkmcnt(3)
	v_add_f32_e32 v10, v10, v11
	s_waitcnt lgkmcnt(2)
	v_add_f32_e32 v22, v22, v27
	ds_bpermute_b32 v11, v131, v10
	s_waitcnt lgkmcnt(2)
	v_add_f32_e32 v14, v14, v15
	ds_bpermute_b32 v15, v129, v14
	s_waitcnt lgkmcnt(2)
	v_add_f32_e32 v27, v23, v24
	ds_bpermute_b32 v28, v131, v27
	ds_bpermute_b32 v2, v1, v89
	ds_bpermute_b32 v3, v1, v85
	s_waitcnt lgkmcnt(3)
	v_add_f32_e32 v14, v14, v15
	ds_bpermute_b32 v15, v130, v14
	v_add_f32_e32 v10, v10, v11
	ds_bpermute_b32 v11, v1, v61
	ds_bpermute_b32 v18, v1, v57
	ds_bpermute_b32 v29, v1, v37
	s_waitcnt lgkmcnt(3)
	v_add_f32_e32 v14, v14, v15
	ds_bpermute_b32 v15, v131, v14
	ds_bpermute_b32 v31, v1, v30
	v_add_f32_e32 v2, v89, v2
	v_add_f32_e32 v3, v85, v3
	s_waitcnt lgkmcnt(4)
	v_add_f32_e32 v16, v61, v11
	s_waitcnt lgkmcnt(1)
	v_add_f32_e32 v14, v14, v15
	ds_bpermute_b32 v15, v1, v53
	v_add_f32_e32 v18, v57, v18
	v_add_f32_e32 v29, v37, v29
	s_waitcnt lgkmcnt(1)
	v_add_f32_e32 v30, v30, v31
	ds_bpermute_b32 v4, v128, v2
	s_waitcnt lgkmcnt(1)
	v_add_f32_e32 v20, v53, v15
	ds_bpermute_b32 v21, v128, v20
	ds_bpermute_b32 v5, v128, v3
	ds_bpermute_b32 v17, v128, v16
	ds_bpermute_b32 v19, v128, v18
	ds_bpermute_b32 v32, v128, v29
	s_waitcnt lgkmcnt(4)
	v_add_f32_e32 v20, v20, v21
	ds_bpermute_b32 v21, v129, v20
	ds_bpermute_b32 v31, v128, v30
	v_add_f32_e32 v2, v2, v4
	s_waitcnt lgkmcnt(5)
	v_add_f32_e32 v3, v3, v5
	s_waitcnt lgkmcnt(4)
	v_add_f32_e32 v16, v16, v17
	s_waitcnt lgkmcnt(1)
	v_add_f32_e32 v20, v20, v21
	ds_bpermute_b32 v21, v130, v20
	v_add_f32_e32 v18, v18, v19
	v_add_f32_e32 v29, v29, v32
	s_waitcnt lgkmcnt(1)
	v_add_f32_e32 v30, v30, v31
	ds_bpermute_b32 v4, v129, v2
	s_waitcnt lgkmcnt(1)
	v_add_f32_e32 v20, v20, v21
	ds_bpermute_b32 v21, v1, v45
	ds_bpermute_b32 v25, v131, v20
	ds_bpermute_b32 v5, v129, v3
	ds_bpermute_b32 v13, v129, v12
	ds_bpermute_b32 v17, v129, v16
	s_waitcnt lgkmcnt(4)
	v_add_f32_e32 v21, v45, v21
	ds_bpermute_b32 v26, v128, v21
	s_waitcnt lgkmcnt(4)
	v_add_f32_e32 v20, v20, v25
	ds_bpermute_b32 v19, v129, v18
	ds_bpermute_b32 v32, v129, v29
	ds_bpermute_b32 v31, v129, v30
	s_waitcnt lgkmcnt(3)
	v_add_f32_e32 v21, v21, v26
	ds_bpermute_b32 v26, v129, v21
	v_add_f32_e32 v2, v2, v4
	v_add_f32_e32 v3, v3, v5
	v_add_f32_e32 v12, v12, v13
	v_add_f32_e32 v16, v16, v17
	s_waitcnt lgkmcnt(0)
	v_add_f32_e32 v25, v21, v26
	ds_bpermute_b32 v26, v130, v25
	v_add_f32_e32 v18, v18, v19
	v_add_f32_e32 v29, v29, v32
	v_add_f32_e32 v30, v30, v31
	ds_bpermute_b32 v4, v130, v2
	s_waitcnt lgkmcnt(1)
	v_add_f32_e32 v25, v25, v26
	ds_bpermute_b32 v26, v131, v25
	ds_bpermute_b32 v5, v130, v3
	ds_bpermute_b32 v13, v130, v12
	ds_bpermute_b32 v17, v130, v16
	ds_bpermute_b32 v19, v130, v18
	s_waitcnt lgkmcnt(4)
	v_add_f32_e32 v24, v25, v26
	v_add_f32_e32 v26, v27, v28
	ds_bpermute_b32 v28, v1, v33
	ds_bpermute_b32 v32, v130, v29
	ds_bpermute_b32 v31, v130, v30
	v_add_f32_e32 v2, v2, v4
	s_waitcnt lgkmcnt(6)
	v_add_f32_e32 v3, v3, v5
	s_waitcnt lgkmcnt(2)
	v_add_f32_e32 v28, v33, v28
	ds_bpermute_b32 v33, v128, v28
	v_add_f32_e32 v12, v12, v13
	v_add_f32_e32 v16, v16, v17
	v_add_f32_e32 v18, v18, v19
	s_waitcnt lgkmcnt(2)
	v_add_f32_e32 v29, v29, v32
	s_waitcnt lgkmcnt(0)
	v_add_f32_e32 v28, v28, v33
	ds_bpermute_b32 v33, v129, v28
	v_add_f32_e32 v35, v30, v31
	ds_bpermute_b32 v4, v131, v2
	ds_bpermute_b32 v5, v131, v3
	ds_bpermute_b32 v13, v131, v12
	s_waitcnt lgkmcnt(3)
	v_add_f32_e32 v28, v28, v33
	ds_bpermute_b32 v33, v130, v28
	ds_bpermute_b32 v17, v131, v16
	ds_bpermute_b32 v19, v131, v18
	ds_bpermute_b32 v32, v131, v29
	ds_bpermute_b32 v36, v131, v35
	s_waitcnt lgkmcnt(4)
	v_add_f32_e32 v33, v28, v33
	ds_bpermute_b32 v34, v131, v33
	v_add_f32_e32 v2, v2, v4
	v_add_f32_e32 v3, v3, v5
	v_add_f32_e32 v12, v12, v13
	s_waitcnt lgkmcnt(4)
	v_add_f32_e32 v16, v16, v17
	s_waitcnt lgkmcnt(3)
	v_add_f32_e32 v18, v18, v19
	s_waitcnt lgkmcnt(2)
	v_add_f32_e32 v28, v29, v32
	s_waitcnt lgkmcnt(0)
	v_add_f32_e32 v29, v33, v34
	v_add_f32_e32 v32, v35, v36
	ds_bpermute_b32 v4, v132, v2
	ds_bpermute_b32 v5, v132, v3
	ds_bpermute_b32 v7, v132, v6
	ds_bpermute_b32 v9, v132, v8
	ds_bpermute_b32 v11, v132, v10
	ds_bpermute_b32 v13, v132, v12
	ds_bpermute_b32 v15, v132, v14
	ds_bpermute_b32 v17, v132, v16
	ds_bpermute_b32 v19, v132, v18
	ds_bpermute_b32 v21, v132, v20
	ds_bpermute_b32 v23, v132, v22
	ds_bpermute_b32 v25, v132, v24
	ds_bpermute_b32 v27, v132, v26
	ds_bpermute_b32 v30, v132, v28
	ds_bpermute_b32 v31, v132, v29
	ds_bpermute_b32 v33, v132, v32
	s_and_saveexec_b64 s[52:53], s[2:3]
	s_cbranch_execz .LBB0_1364
	s_waitcnt lgkmcnt(14)
	v_add_f32_e32 v2, v2, v4
	v_add_f32_e32 v3, v3, v5
	s_mov_b32 s61, 0xff61b1e6
	v_max3_f32 v4, v2, s61, v3
	s_waitcnt lgkmcnt(13)
	v_add_f32_e32 v5, v6, v7
	s_waitcnt lgkmcnt(12)
	v_add_f32_e32 v6, v8, v9
	v_max3_f32 v4, v4, v5, v6
	s_waitcnt lgkmcnt(11)
	v_add_f32_e32 v7, v10, v11
	s_waitcnt lgkmcnt(10)
	v_add_f32_e32 v8, v12, v13
	v_max3_f32 v4, v4, v7, v8
	s_waitcnt lgkmcnt(9)
	v_add_f32_e32 v11, v14, v15
	s_waitcnt lgkmcnt(8)
	v_add_f32_e32 v15, v16, v17
	v_max3_f32 v4, v4, v11, v15
	s_waitcnt lgkmcnt(7)
	v_add_f32_e32 v16, v18, v19
	s_waitcnt lgkmcnt(6)
	v_add_f32_e32 v17, v20, v21
	v_max3_f32 v4, v4, v16, v17
	s_waitcnt lgkmcnt(5)
	v_add_f32_e32 v18, v22, v23
	s_waitcnt lgkmcnt(4)
	v_add_f32_e32 v19, v24, v25
	v_max3_f32 v4, v4, v18, v19
	s_waitcnt lgkmcnt(3)
	v_add_f32_e32 v14, v26, v27
	s_waitcnt lgkmcnt(2)
	v_add_f32_e32 v13, v28, v30
	s_waitcnt lgkmcnt(0)
	v_add_f32_e32 v32, v32, v33
	v_max3_f32 v4, v4, v14, v13
	v_add_f32_e32 v10, v29, v31
	v_max3_f32 v12, v4, v10, v32
	v_sub_f32_e32 v4, v32, v12
	v_mul_f32_e32 v9, 0x3fb8aa3b, v4
	v_fma_f32 v20, v4, s58, -v9
	v_rndne_f32_e32 v21, v9
	v_fmac_f32_e32 v20, 0x32a5705f, v4
	v_sub_f32_e32 v9, v9, v21
	v_add_f32_e32 v9, v9, v20
	v_exp_f32_e32 v9, v9
	v_cvt_i32_f32_e32 v20, v21
	v_cmp_ngt_f32_e32 vcc, s59, v4
	v_sub_f32_e32 v2, v2, v12
	v_sub_f32_e32 v3, v3, v12
	v_ldexp_f32 v9, v9, v20
	v_cndmask_b32_e32 v9, 0, v9, vcc
	v_cmp_nlt_f32_e32 vcc, s60, v4
	v_mul_f32_e32 v4, 0x3fb8aa3b, v2
	v_fma_f32 v20, v2, s58, -v4
	v_rndne_f32_e32 v21, v4
	v_fmac_f32_e32 v20, 0x32a5705f, v2
	v_sub_f32_e32 v4, v4, v21
	v_add_f32_e32 v4, v4, v20
	v_exp_f32_e32 v4, v4
	v_cvt_i32_f32_e32 v20, v21
	v_cndmask_b32_e32 v9, v209, v9, vcc
	v_cmp_ngt_f32_e32 vcc, s59, v2
	v_sub_f32_e32 v17, v17, v12
	v_ldexp_f32 v4, v4, v20
	v_cndmask_b32_e32 v4, 0, v4, vcc
	v_cmp_nlt_f32_e32 vcc, s60, v2
	v_sub_f32_e32 v18, v18, v12
	v_sub_f32_e32 v19, v19, v12
	v_cndmask_b32_e32 v2, v209, v4, vcc
	v_mul_f32_e32 v4, 0x3fb8aa3b, v3
	v_fma_f32 v20, v3, s58, -v4
	v_rndne_f32_e32 v21, v4
	v_fmac_f32_e32 v20, 0x32a5705f, v3
	v_sub_f32_e32 v4, v4, v21
	v_add_f32_e32 v4, v4, v20
	v_exp_f32_e32 v4, v4
	v_cvt_i32_f32_e32 v20, v21
	v_cmp_ngt_f32_e32 vcc, s59, v3
	v_sub_f32_e32 v14, v14, v12
	v_sub_f32_e32 v13, v13, v12
	v_ldexp_f32 v4, v4, v20
	v_cndmask_b32_e32 v4, 0, v4, vcc
	v_cmp_nlt_f32_e32 vcc, s60, v3
	v_sub_f32_e32 v10, v10, v12
	s_nop 0
	v_cndmask_b32_e32 v3, v209, v4, vcc
	v_sub_f32_e32 v4, v5, v12
	v_mul_f32_e32 v5, 0x3fb8aa3b, v4
	v_fma_f32 v21, v4, s58, -v5
	v_rndne_f32_e32 v22, v5
	v_fmac_f32_e32 v21, 0x32a5705f, v4
	v_sub_f32_e32 v5, v5, v22
	v_add_f32_e32 v5, v5, v21
	v_exp_f32_e32 v5, v5
	v_cvt_i32_f32_e32 v21, v22
	v_cmp_ngt_f32_e32 vcc, s59, v4
	v_add_f32_e32 v20, v2, v3
	v_ldexp_f32 v5, v5, v21
	v_cndmask_b32_e32 v5, 0, v5, vcc
	v_cmp_nlt_f32_e32 vcc, s60, v4
	s_nop 1
	v_cndmask_b32_e32 v4, v209, v5, vcc
	v_sub_f32_e32 v5, v6, v12
	v_mul_f32_e32 v6, 0x3fb8aa3b, v5
	v_fma_f32 v21, v5, s58, -v6
	v_rndne_f32_e32 v22, v6
	v_fmac_f32_e32 v21, 0x32a5705f, v5
	v_sub_f32_e32 v6, v6, v22
	v_add_f32_e32 v6, v6, v21
	v_exp_f32_e32 v6, v6
	v_cvt_i32_f32_e32 v21, v22
	v_cmp_ngt_f32_e32 vcc, s59, v5
	v_add_f32_e32 v20, v4, v20
	v_ldexp_f32 v6, v6, v21
	v_cndmask_b32_e32 v6, 0, v6, vcc
	v_cmp_nlt_f32_e32 vcc, s60, v5
	s_nop 1
	v_cndmask_b32_e32 v5, v209, v6, vcc
	v_sub_f32_e32 v6, v7, v12
	v_mul_f32_e32 v7, 0x3fb8aa3b, v6
	v_fma_f32 v21, v6, s58, -v7
	v_rndne_f32_e32 v22, v7
	v_fmac_f32_e32 v21, 0x32a5705f, v6
	v_sub_f32_e32 v7, v7, v22
	v_add_f32_e32 v7, v7, v21
	v_exp_f32_e32 v7, v7
	v_cvt_i32_f32_e32 v21, v22
	v_cmp_ngt_f32_e32 vcc, s59, v6
	v_add_f32_e32 v20, v5, v20
	v_ldexp_f32 v7, v7, v21
	v_cndmask_b32_e32 v7, 0, v7, vcc
	v_cmp_nlt_f32_e32 vcc, s60, v6
	s_nop 1
	v_cndmask_b32_e32 v6, v209, v7, vcc
	v_sub_f32_e32 v7, v8, v12
	v_mul_f32_e32 v8, 0x3fb8aa3b, v7
	v_fma_f32 v21, v7, s58, -v8
	v_rndne_f32_e32 v22, v8
	v_fmac_f32_e32 v21, 0x32a5705f, v7
	v_sub_f32_e32 v8, v8, v22
	v_add_f32_e32 v8, v8, v21
	v_exp_f32_e32 v8, v8
	v_cvt_i32_f32_e32 v21, v22
	v_cmp_ngt_f32_e32 vcc, s59, v7
	v_add_f32_e32 v20, v6, v20
	v_ldexp_f32 v8, v8, v21
	v_cndmask_b32_e32 v8, 0, v8, vcc
	v_cmp_nlt_f32_e32 vcc, s60, v7
	s_nop 1
	v_cndmask_b32_e32 v7, v209, v8, vcc
	v_sub_f32_e32 v8, v11, v12
	v_mul_f32_e32 v11, 0x3fb8aa3b, v8
	v_fma_f32 v21, v8, s58, -v11
	v_rndne_f32_e32 v22, v11
	v_fmac_f32_e32 v21, 0x32a5705f, v8
	v_sub_f32_e32 v11, v11, v22
	v_add_f32_e32 v11, v11, v21
	v_exp_f32_e32 v11, v11
	v_cvt_i32_f32_e32 v21, v22
	v_cmp_ngt_f32_e32 vcc, s59, v8
	v_add_f32_e32 v20, v7, v20
	v_ldexp_f32 v11, v11, v21
	v_cndmask_b32_e32 v11, 0, v11, vcc
	v_cmp_nlt_f32_e32 vcc, s60, v8
	s_nop 1
	v_cndmask_b32_e32 v8, v209, v11, vcc
	v_sub_f32_e32 v11, v15, v12
	v_mul_f32_e32 v15, 0x3fb8aa3b, v11
	v_fma_f32 v21, v11, s58, -v15
	v_rndne_f32_e32 v22, v15
	v_fmac_f32_e32 v21, 0x32a5705f, v11
	v_sub_f32_e32 v15, v15, v22
	v_add_f32_e32 v15, v15, v21
	v_exp_f32_e32 v15, v15
	v_cvt_i32_f32_e32 v21, v22
	v_cmp_ngt_f32_e32 vcc, s59, v11
	v_add_f32_e32 v20, v8, v20
	v_ldexp_f32 v15, v15, v21
	v_cndmask_b32_e32 v15, 0, v15, vcc
	v_cmp_nlt_f32_e32 vcc, s60, v11
	s_nop 1
	v_cndmask_b32_e32 v11, v209, v15, vcc
	v_sub_f32_e32 v15, v16, v12
	v_mul_f32_e32 v16, 0x3fb8aa3b, v15
	v_fma_f32 v21, v15, s58, -v16
	v_rndne_f32_e32 v22, v16
	v_fmac_f32_e32 v21, 0x32a5705f, v15
	v_sub_f32_e32 v16, v16, v22
	v_add_f32_e32 v16, v16, v21
	v_exp_f32_e32 v16, v16
	v_cvt_i32_f32_e32 v21, v22
	v_cmp_ngt_f32_e32 vcc, s59, v15
	v_add_f32_e32 v20, v11, v20
	v_mul_f32_e32 v12, 0x3fb8aa3b, v10
	v_ldexp_f32 v16, v16, v21
	v_cndmask_b32_e32 v16, 0, v16, vcc
	v_cmp_nlt_f32_e32 vcc, s60, v15
	s_nop 1
	v_cndmask_b32_e32 v15, v209, v16, vcc
	v_add_f32_e32 v16, v15, v20
	v_mul_f32_e32 v20, 0x3fb8aa3b, v17
	v_fma_f32 v21, v17, s58, -v20
	v_rndne_f32_e32 v22, v20
	v_fmac_f32_e32 v21, 0x32a5705f, v17
	v_sub_f32_e32 v20, v20, v22
	v_add_f32_e32 v20, v20, v21
	v_exp_f32_e32 v20, v20
	v_cvt_i32_f32_e32 v21, v22
	v_cmp_ngt_f32_e32 vcc, s59, v17
	v_ldexp_f32 v20, v20, v21
	s_nop 0
	v_cndmask_b32_e32 v20, 0, v20, vcc
	v_cmp_nlt_f32_e32 vcc, s60, v17
	s_nop 1
	v_cndmask_b32_e32 v17, v209, v20, vcc
	v_mul_f32_e32 v20, 0x3fb8aa3b, v18
	v_fma_f32 v21, v18, s58, -v20
	v_rndne_f32_e32 v22, v20
	v_fmac_f32_e32 v21, 0x32a5705f, v18
	v_sub_f32_e32 v20, v20, v22
	v_add_f32_e32 v20, v20, v21
	v_exp_f32_e32 v20, v20
	v_cvt_i32_f32_e32 v21, v22
	v_cmp_ngt_f32_e32 vcc, s59, v18
	v_add_f32_e32 v16, v17, v16
	v_ldexp_f32 v20, v20, v21
	v_cndmask_b32_e32 v20, 0, v20, vcc
	v_cmp_nlt_f32_e32 vcc, s60, v18
	s_nop 1
	v_cndmask_b32_e32 v18, v209, v20, vcc
	v_mul_f32_e32 v20, 0x3fb8aa3b, v19
	v_fma_f32 v21, v19, s58, -v20
	v_rndne_f32_e32 v22, v20
	v_fmac_f32_e32 v21, 0x32a5705f, v19
	v_sub_f32_e32 v20, v20, v22
	v_add_f32_e32 v20, v20, v21
	v_exp_f32_e32 v20, v20
	v_cvt_i32_f32_e32 v21, v22
	v_cmp_ngt_f32_e32 vcc, s59, v19
	v_add_f32_e32 v16, v18, v16
	v_ldexp_f32 v20, v20, v21
	v_cndmask_b32_e32 v20, 0, v20, vcc
	v_cmp_nlt_f32_e32 vcc, s60, v19
	s_nop 1
	v_cndmask_b32_e32 v19, v209, v20, vcc
	v_mul_f32_e32 v20, 0x3fb8aa3b, v14
	v_fma_f32 v21, v14, s58, -v20
	v_rndne_f32_e32 v22, v20
	v_fmac_f32_e32 v21, 0x32a5705f, v14
	v_sub_f32_e32 v20, v20, v22
	v_add_f32_e32 v20, v20, v21
	v_exp_f32_e32 v20, v20
	v_cvt_i32_f32_e32 v21, v22
	v_cmp_ngt_f32_e32 vcc, s59, v14
	v_add_f32_e32 v16, v19, v16
	v_ldexp_f32 v20, v20, v21
	v_cndmask_b32_e32 v20, 0, v20, vcc
	v_cmp_nlt_f32_e32 vcc, s60, v14
	s_nop 1
	v_cndmask_b32_e32 v14, v209, v20, vcc
	v_mul_f32_e32 v20, 0x3fb8aa3b, v13
	v_fma_f32 v21, v13, s58, -v20
	v_rndne_f32_e32 v22, v20
	v_fmac_f32_e32 v21, 0x32a5705f, v13
	v_sub_f32_e32 v20, v20, v22
	v_add_f32_e32 v20, v20, v21
	v_exp_f32_e32 v20, v20
	v_cvt_i32_f32_e32 v21, v22
	v_cmp_ngt_f32_e32 vcc, s59, v13
	v_add_f32_e32 v16, v14, v16
	v_ldexp_f32 v20, v20, v21
	v_cndmask_b32_e32 v20, 0, v20, vcc
	v_cmp_nlt_f32_e32 vcc, s60, v13
	v_rndne_f32_e32 v21, v12
	s_nop 0
	v_cndmask_b32_e32 v13, v209, v20, vcc
	v_fma_f32 v20, v10, s58, -v12
	v_fmac_f32_e32 v20, 0x32a5705f, v10
	v_sub_f32_e32 v12, v12, v21
	v_add_f32_e32 v12, v12, v20
	v_exp_f32_e32 v12, v12
	v_cvt_i32_f32_e32 v20, v21
	v_cmp_ngt_f32_e32 vcc, s59, v10
	v_add_f32_e32 v16, v13, v16
	v_ldexp_f32 v12, v12, v20
	v_cndmask_b32_e32 v12, 0, v12, vcc
	v_cmp_nlt_f32_e32 vcc, s60, v10
	s_nop 1
	v_cndmask_b32_e32 v12, v209, v12, vcc
	v_add_f32_e32 v10, v12, v16
	v_add_f32_e32 v10, v9, v10
	v_div_scale_f32 v16, s[62:63], v10, v10, v9
	v_rcp_f32_e32 v20, v16
	s_nop 0
	v_fma_f32 v21, -v16, v20, 1.0
	v_fmac_f32_e32 v20, v21, v20
	v_div_scale_f32 v21, vcc, v9, v10, v9
	v_mul_f32_e32 v22, v21, v20
	v_fma_f32 v23, -v16, v22, v21
	v_fmac_f32_e32 v22, v23, v20
	v_fma_f32 v16, -v16, v22, v21
	v_div_fmas_f32 v16, v16, v20, v22
	v_div_fixup_f32 v9, v16, v10, v9
	v_div_scale_f32 v16, s[62:63], v10, v10, v12
	v_rcp_f32_e32 v20, v16
	s_nop 0
	v_fma_f32 v21, -v16, v20, 1.0
	v_fmac_f32_e32 v20, v21, v20
	v_div_scale_f32 v21, vcc, v12, v10, v12
	v_mul_f32_e32 v22, v21, v20
	v_fma_f32 v23, -v16, v22, v21
	v_fmac_f32_e32 v22, v23, v20
	v_fma_f32 v16, -v16, v22, v21
	v_div_fmas_f32 v16, v16, v20, v22
	v_div_fixup_f32 v12, v16, v10, v12
	v_div_scale_f32 v16, s[62:63], v10, v10, v13
	v_rcp_f32_e32 v20, v16
	s_nop 0
	v_fma_f32 v21, -v16, v20, 1.0
	v_fmac_f32_e32 v20, v21, v20
	v_div_scale_f32 v21, vcc, v13, v10, v13
	v_mul_f32_e32 v22, v21, v20
	v_fma_f32 v23, -v16, v22, v21
	v_fmac_f32_e32 v22, v23, v20
	v_fma_f32 v16, -v16, v22, v21
	v_div_fmas_f32 v16, v16, v20, v22
	v_div_fixup_f32 v13, v16, v10, v13
	v_div_scale_f32 v16, s[62:63], v10, v10, v14
	v_rcp_f32_e32 v20, v16
	s_nop 0
	v_fma_f32 v21, -v16, v20, 1.0
	v_fmac_f32_e32 v20, v21, v20
	v_div_scale_f32 v21, vcc, v14, v10, v14
	v_mul_f32_e32 v22, v21, v20
	v_fma_f32 v23, -v16, v22, v21
	v_fmac_f32_e32 v22, v23, v20
	v_fma_f32 v16, -v16, v22, v21
	v_div_fmas_f32 v16, v16, v20, v22
	v_div_fixup_f32 v14, v16, v10, v14
	v_div_scale_f32 v16, s[62:63], v10, v10, v19
	v_rcp_f32_e32 v20, v16
	s_nop 0
	v_fma_f32 v21, -v16, v20, 1.0
	v_fmac_f32_e32 v20, v21, v20
	v_div_scale_f32 v21, vcc, v19, v10, v19
	v_mul_f32_e32 v22, v21, v20
	v_fma_f32 v23, -v16, v22, v21
	v_fmac_f32_e32 v22, v23, v20
	v_fma_f32 v16, -v16, v22, v21
	v_div_fmas_f32 v16, v16, v20, v22
	v_div_fixup_f32 v16, v16, v10, v19
	v_div_scale_f32 v19, s[62:63], v10, v10, v18
	v_rcp_f32_e32 v20, v19
	s_nop 0
	v_fma_f32 v21, -v19, v20, 1.0
	v_fmac_f32_e32 v20, v21, v20
	v_div_scale_f32 v21, vcc, v18, v10, v18
	v_mul_f32_e32 v22, v21, v20
	v_fma_f32 v23, -v19, v22, v21
	v_fmac_f32_e32 v22, v23, v20
	v_fma_f32 v19, -v19, v22, v21
	v_div_fmas_f32 v19, v19, v20, v22
	v_div_fixup_f32 v18, v19, v10, v18
	v_div_scale_f32 v19, s[62:63], v10, v10, v17
	v_rcp_f32_e32 v20, v19
	s_nop 0
	v_fma_f32 v21, -v19, v20, 1.0
	v_fmac_f32_e32 v20, v21, v20
	v_div_scale_f32 v21, vcc, v17, v10, v17
	v_mul_f32_e32 v22, v21, v20
	v_fma_f32 v23, -v19, v22, v21
	v_fmac_f32_e32 v22, v23, v20
	v_fma_f32 v19, -v19, v22, v21
	v_div_fmas_f32 v19, v19, v20, v22
	v_div_fixup_f32 v17, v19, v10, v17
	v_div_scale_f32 v19, s[62:63], v10, v10, v15
	v_rcp_f32_e32 v20, v19
	s_nop 0
	v_fma_f32 v21, -v19, v20, 1.0
	v_fmac_f32_e32 v20, v21, v20
	v_div_scale_f32 v21, vcc, v15, v10, v15
	v_mul_f32_e32 v22, v21, v20
	v_fma_f32 v23, -v19, v22, v21
	v_fmac_f32_e32 v22, v23, v20
	v_fma_f32 v19, -v19, v22, v21
	v_div_fmas_f32 v19, v19, v20, v22
	v_div_fixup_f32 v15, v19, v10, v15
	v_div_scale_f32 v19, s[62:63], v10, v10, v11
	v_rcp_f32_e32 v20, v19
	s_nop 0
	v_fma_f32 v21, -v19, v20, 1.0
	v_fmac_f32_e32 v20, v21, v20
	v_div_scale_f32 v21, vcc, v11, v10, v11
	v_mul_f32_e32 v22, v21, v20
	v_fma_f32 v23, -v19, v22, v21
	v_fmac_f32_e32 v22, v23, v20
	v_fma_f32 v19, -v19, v22, v21
	v_div_fmas_f32 v19, v19, v20, v22
	v_div_fixup_f32 v11, v19, v10, v11
	v_div_scale_f32 v19, s[62:63], v10, v10, v8
	v_rcp_f32_e32 v20, v19
	s_nop 0
	v_fma_f32 v21, -v19, v20, 1.0
	v_fmac_f32_e32 v20, v21, v20
	v_div_scale_f32 v21, vcc, v8, v10, v8
	v_mul_f32_e32 v22, v21, v20
	v_fma_f32 v23, -v19, v22, v21
	v_fmac_f32_e32 v22, v23, v20
	v_fma_f32 v19, -v19, v22, v21
	v_div_fmas_f32 v19, v19, v20, v22
	v_div_fixup_f32 v8, v19, v10, v8
	v_div_scale_f32 v19, s[62:63], v10, v10, v7
	v_rcp_f32_e32 v20, v19
	s_nop 0
	v_fma_f32 v21, -v19, v20, 1.0
	v_fmac_f32_e32 v20, v21, v20
	v_div_scale_f32 v21, vcc, v7, v10, v7
	v_mul_f32_e32 v22, v21, v20
	v_fma_f32 v23, -v19, v22, v21
	v_fmac_f32_e32 v22, v23, v20
	v_fma_f32 v19, -v19, v22, v21
	v_div_fmas_f32 v19, v19, v20, v22
	v_div_fixup_f32 v7, v19, v10, v7
	v_div_scale_f32 v19, s[62:63], v10, v10, v6
	v_rcp_f32_e32 v20, v19
	s_nop 0
	v_fma_f32 v21, -v19, v20, 1.0
	v_fmac_f32_e32 v20, v21, v20
	v_div_scale_f32 v21, vcc, v6, v10, v6
	v_mul_f32_e32 v22, v21, v20
	v_fma_f32 v23, -v19, v22, v21
	v_fmac_f32_e32 v22, v23, v20
	v_fma_f32 v19, -v19, v22, v21
	v_div_fmas_f32 v19, v19, v20, v22
	v_div_fixup_f32 v6, v19, v10, v6
	v_div_scale_f32 v19, s[62:63], v10, v10, v5
	v_rcp_f32_e32 v20, v19
	s_nop 0
	v_fma_f32 v21, -v19, v20, 1.0
	v_fmac_f32_e32 v20, v21, v20
	v_div_scale_f32 v21, vcc, v5, v10, v5
	v_mul_f32_e32 v22, v21, v20
	v_fma_f32 v23, -v19, v22, v21
	v_fmac_f32_e32 v22, v23, v20
	v_fma_f32 v19, -v19, v22, v21
	v_div_fmas_f32 v19, v19, v20, v22
	v_div_fixup_f32 v5, v19, v10, v5
	v_div_scale_f32 v19, s[62:63], v10, v10, v4
	v_rcp_f32_e32 v20, v19
	s_nop 0
	v_fma_f32 v21, -v19, v20, 1.0
	v_fmac_f32_e32 v20, v21, v20
	v_div_scale_f32 v21, vcc, v4, v10, v4
	v_mul_f32_e32 v22, v21, v20
	v_fma_f32 v23, -v19, v22, v21
	v_fmac_f32_e32 v22, v23, v20
	v_fma_f32 v19, -v19, v22, v21
	v_div_fmas_f32 v19, v19, v20, v22
	v_div_fixup_f32 v4, v19, v10, v4
	v_div_scale_f32 v19, s[62:63], v10, v10, v3
	v_rcp_f32_e32 v20, v19
	s_nop 0
	v_fma_f32 v21, -v19, v20, 1.0
	v_fmac_f32_e32 v20, v21, v20
	v_div_scale_f32 v21, vcc, v3, v10, v3
	v_mul_f32_e32 v22, v21, v20
	v_fma_f32 v23, -v19, v22, v21
	v_fmac_f32_e32 v22, v23, v20
	v_fma_f32 v19, -v19, v22, v21
	v_div_fmas_f32 v19, v19, v20, v22
	v_div_fixup_f32 v3, v19, v10, v3
	v_div_scale_f32 v19, s[62:63], v10, v10, v2
	v_rcp_f32_e32 v20, v19
	s_nop 0
	v_fma_f32 v21, -v19, v20, 1.0
	v_fmac_f32_e32 v20, v21, v20
	v_div_scale_f32 v21, vcc, v2, v10, v2
	v_mul_f32_e32 v22, v21, v20
	v_fma_f32 v23, -v19, v22, v21
	v_fmac_f32_e32 v22, v23, v20
	v_fma_f32 v19, -v19, v22, v21
	v_div_fmas_f32 v19, v19, v20, v22
	v_div_fixup_f32 v2, v19, v10, v2
	v_cndmask_b32_e64 v2, 0, v2, s[36:37]
	v_cndmask_b32_e64 v2, v2, v3, s[34:35]
	v_cndmask_b32_e64 v2, v2, v4, s[30:31]
	v_cndmask_b32_e64 v2, v2, v5, s[28:29]
	v_cndmask_b32_e64 v2, v2, v6, s[26:27]
	v_cndmask_b32_e64 v2, v2, v7, s[24:25]
	v_cndmask_b32_e64 v2, v2, v8, s[22:23]
	v_cndmask_b32_e64 v2, v2, v11, s[20:21]
	v_cndmask_b32_e64 v2, v2, v15, s[18:19]
	v_cndmask_b32_e64 v2, v2, v17, s[16:17]
	v_cndmask_b32_e64 v2, v2, v18, s[14:15]
	v_cndmask_b32_e64 v2, v2, v16, s[12:13]
	v_cndmask_b32_e64 v2, v2, v14, s[10:11]
	v_cndmask_b32_e64 v2, v2, v13, s[8:9]
	v_cndmask_b32_e64 v2, v2, v12, s[6:7]
	v_cndmask_b32_e64 v4, v2, v9, s[4:5]
	v_lshl_add_u64 v[2:3], s[40:41], 0, v[106:107]
	global_store_dword v[2:3], v4, off
	s_branch .LBB0_1364
.Lf_lat_L0:
	s_cmp_lg_u32 s1, -1
	s_cselect_b32 s52, s1, 0
	s_cselect_b32 s53, s43, 0
	s_cmp_lg_u32 s45, -1
	s_cselect_b32 s61, s45, 0
	s_cselect_b32 s62, s43, 0
	s_cmpk_lt_i32 s0, 0x4000
	s_cselect_b32 s53, s53, s42
	s_cselect_b32 s52, s52, s33
	s_waitcnt vmcnt(7) lgkmcnt(7)
	v_lshl_add_u64 v[18:19], s[40:41], 0, v[110:111]
	v_lshl_add_u64 v[118:119], s[52:53], 0, v[112:113]
	s_mov_b32 s52, 0x1b41000
	v_add_co_u32_e32 v14, vcc, s52, v18
	ds_read_b128 v[86:89], v134
	ds_read_b128 v[82:85], v134 offset:8192
	ds_read_b128 v[78:81], v134 offset:16384
	ds_read_b128 v[74:77], v134 offset:24576
	ds_read_b128 v[70:73], v134 offset:32768
	ds_read_b128 v[66:69], v134 offset:40960
	ds_read_b128 v[62:65], v134 offset:49152
	ds_read_b128 v[58:61], v134 offset:57344
	ds_read_b128 v[54:57], v135
	ds_read_b128 v[50:53], v136
	ds_read_b128 v[46:49], v137
	ds_read_b128 v[42:45], v138
	ds_read_b128 v[38:41], v139
	ds_read_b128 v[34:37], v140
	s_waitcnt vmcnt(4) lgkmcnt(14)
	ds_read_b128 v[30:33], v141
	ds_read_b128 v[26:29], v142
	v_addc_co_u32_e32 v15, vcc, 0, v19, vcc
	global_load_dwordx4 v[2:5], v[14:15], off offset:3072
	global_load_dwordx4 v[6:9], v[14:15], off offset:2048
	s_mov_b32 s52, 0x1b40000
	v_add_co_u32_e32 v94, vcc, s52, v18
	s_cselect_b32 s63, s62, s55
	s_nop 0
	v_addc_co_u32_e32 v95, vcc, 0, v19, vcc
	s_cselect_b32 s62, s61, s54
	v_lshl_add_u64 v[116:117], s[62:63], 0, v[112:113]
	s_mov_b32 s52, 0x800000
	v_lshl_add_u64 v[120:121], s[40:41], 0, v[108:109]
	s_waitcnt vmcnt(1)
	v_mov_b32_e32 v13, v3
	s_waitcnt vmcnt(0)
	v_mov_b32_e32 v12, v7
	v_mov_b32_e32 v10, v6
	v_mov_b32_e32 v11, v2
	v_pk_mul_f32 v[12:13], v[12:13], v[12:13]
	s_nop 0
	v_pk_fma_f32 v[10:11], v[10:11], v[10:11], v[12:13]
	v_mov_b32_e32 v12, v8
	v_mov_b32_e32 v13, v4
	v_pk_fma_f32 v[10:11], v[12:13], v[12:13], v[10:11]
	v_mov_b32_e32 v12, v9
	v_mov_b32_e32 v13, v5
	v_pk_fma_f32 v[114:115], v[12:13], v[12:13], v[10:11]
	global_load_dwordx4 v[10:13], v[14:15], off offset:1024
	s_nop 0
	global_load_dwordx4 v[14:17], v[14:15], off
	ds_read_b128 v[98:101], v133
	global_load_dwordx4 v[90:93], v[94:95], off offset:1024
	global_load_dwordx4 v[102:105], v[94:95], off
	s_waitcnt vmcnt(3)
	v_mov_b32_e32 v23, v11
	s_waitcnt vmcnt(2)
	v_mov_b32_e32 v22, v15
	v_mov_b32_e32 v20, v14
	v_mov_b32_e32 v21, v10
	v_pk_mul_f32 v[22:23], v[22:23], v[22:23]
	s_waitcnt vmcnt(1)
	v_mul_f32_e32 v215, v91, v91
	v_pk_fma_f32 v[20:21], v[20:21], v[20:21], v[22:23]
	v_mov_b32_e32 v22, v16
	v_mov_b32_e32 v23, v12
	v_pk_fma_f32 v[20:21], v[22:23], v[22:23], v[20:21]
	v_mov_b32_e32 v22, v17
	v_mov_b32_e32 v23, v13
	v_pk_fma_f32 v[124:125], v[22:23], v[22:23], v[20:21]
	global_load_dwordx4 v[18:21], v[94:95], off offset:3072
	global_load_dwordx4 v[22:25], v[94:95], off offset:2048
	s_nop 0
	ds_read_b128 v[94:97], v118
	ds_read_b128 v[210:213], v116
	s_waitcnt vmcnt(0) lgkmcnt(0)
	v_mul_f32_e32 v216, v103, v103
	v_fmac_f32_e32 v215, v90, v90
	v_fmac_f32_e32 v216, v102, v102
	v_fmac_f32_e32 v215, v92, v92
	v_fmac_f32_e32 v216, v104, v104
	v_fmac_f32_e32 v215, v93, v93
	v_fmac_f32_e32 v216, v105, v105
	v_mul_f32_e32 v190, v19, v19
	v_mul_f32_e32 v214, v23, v23
	v_fmac_f32_e32 v214, v22, v22
	v_fmac_f32_e32 v190, v18, v18
	v_fmac_f32_e32 v214, v24, v24
	v_fmac_f32_e32 v190, v20, v20
	v_fmac_f32_e32 v214, v25, v25
	s_waitcnt lgkmcnt(0)
	v_mov_b32_e32 v122, v210
	v_add_f32_e32 v210, v216, v215
	v_fmac_f32_e32 v190, v21, v21
	v_add_f32_e32 v210, v210, v214
	v_add_f32_e32 v190, v210, v190
	v_add_f32_e32 v124, v190, v124
	v_add_f32_e32 v124, v124, v125
	v_add_f32_e32 v114, v124, v114
	v_add_f32_e32 v114, v114, v115
	ds_bpermute_b32 v115, v1, v114
	v_mov_b32_e32 v124, v102
	v_mov_b32_e32 v125, v104
	v_mov_b32_e32 v104, v103
	v_mov_b32_e32 v123, v212
	s_waitcnt lgkmcnt(0)
	v_add_f32_e32 v114, v114, v115
	ds_bpermute_b32 v115, v128, v114
	v_mov_b32_e32 v212, v211
	v_mov_b32_e32 v210, v98
	v_mov_b32_e32 v211, v100
	v_mov_b32_e32 v100, v99
	s_waitcnt lgkmcnt(0)
	v_add_f32_e32 v114, v114, v115
	ds_bpermute_b32 v115, v129, v114
	v_pk_add_f32 v[126:127], v[122:123], 1.0 op_sel_hi:[1,0]
	v_pk_add_f32 v[122:123], v[212:213], 1.0 op_sel_hi:[1,0]
	s_waitcnt lgkmcnt(0)
	v_add_f32_e32 v114, v114, v115
	ds_bpermute_b32 v115, v130, v114
	s_waitcnt lgkmcnt(0)
	v_add_f32_e32 v114, v114, v115
	ds_bpermute_b32 v115, v131, v114
	s_waitcnt lgkmcnt(0)
	v_add_f32_e32 v114, v114, v115
	ds_bpermute_b32 v115, v132, v114
	s_waitcnt lgkmcnt(0)
	v_add_f32_e32 v114, v114, v115
	v_fmamk_f32 v114, v114, 0x3a000000, v207
	v_cmp_gt_f32_e32 vcc, s52, v114
	v_mul_f32_e32 v115, 0x4b800000, v114
	s_mov_b32 s52, 0x2ec40000
	v_cndmask_b32_e32 v114, v114, v115, vcc
	v_rsq_f32_e32 v114, v114
	s_nop 0
	v_mul_f32_e32 v115, 0x45800000, v114
	v_cndmask_b32_e32 v114, v114, v115, vcc
	v_pk_mul_f32 v[124:125], v[124:125], v[114:115] op_sel_hi:[1,0]
	v_pk_mul_f32 v[102:103], v[104:105], v[114:115] op_sel_hi:[1,0]
	v_pk_mul_f32 v[124:125], v[210:211], v[124:125]
	v_mov_b32_e32 v211, v96
	v_pk_mul_f32 v[98:99], v[100:101], v[102:103]
	v_mov_b32_e32 v96, v95
	v_mov_b32_e32 v210, v94
	v_pk_fma_f32 v[96:97], v[122:123], v[98:99], v[96:97]
	v_pk_fma_f32 v[124:125], v[126:127], v[124:125], v[210:211]
	v_fma_f32 v33, v97, v33, 0
	v_fmac_f32_e32 v33, v125, v32
	v_and_b32_sdwa v98, v97, v208 dst_sel:DWORD dst_unused:UNUSED_PAD src0_sel:WORD_1 src1_sel:DWORD
	v_fmac_f32_e32 v33, v96, v31
	v_and_b32_sdwa v94, v125, v208 dst_sel:DWORD dst_unused:UNUSED_PAD src0_sel:WORD_1 src1_sel:DWORD
	v_and_b32_sdwa v99, v96, v208 dst_sel:DWORD dst_unused:UNUSED_PAD src0_sel:WORD_1 src1_sel:DWORD
	v_add3_u32 v98, v97, v98, s57
	v_fmac_f32_e32 v33, v124, v30
	v_fma_f32 v30, v97, v29, 0
	v_and_b32_sdwa v95, v124, v208 dst_sel:DWORD dst_unused:UNUSED_PAD src0_sel:WORD_1 src1_sel:DWORD
	v_add3_u32 v94, v125, v94, s57
	v_add3_u32 v99, v96, v99, s57
	v_and_b32_e32 v98, 0xffff0000, v98
	v_fma_f32 v89, v97, v89, 0
	v_fma_f32 v85, v97, v85, 0
	v_fma_f32 v81, v97, v81, 0
	v_fma_f32 v77, v97, v77, 0
	v_fma_f32 v73, v97, v73, 0
	v_fma_f32 v69, v97, v69, 0
	v_fma_f32 v65, v97, v65, 0
	v_fma_f32 v61, v97, v61, 0
	v_fma_f32 v57, v97, v57, 0
	v_fma_f32 v53, v97, v53, 0
	v_fma_f32 v49, v97, v49, 0
	v_fma_f32 v45, v97, v45, 0
	v_fma_f32 v41, v97, v41, 0
	v_fma_f32 v37, v97, v37, 0
	v_fmac_f32_e32 v30, v125, v28
	v_add3_u32 v95, v124, v95, s57
	v_and_b32_e32 v100, 0xffff0000, v99
	v_or_b32_sdwa v99, v98, v94 dst_sel:DWORD dst_unused:UNUSED_PAD src0_sel:DWORD src1_sel:WORD_1
	v_add_co_u32_e32 v94, vcc, s52, v120
	v_fmac_f32_e32 v89, v125, v88
	v_fmac_f32_e32 v85, v125, v84
	v_fmac_f32_e32 v81, v125, v80
	v_fmac_f32_e32 v77, v125, v76
	v_fmac_f32_e32 v73, v125, v72
	v_fmac_f32_e32 v69, v125, v68
	v_fmac_f32_e32 v65, v125, v64
	v_fmac_f32_e32 v61, v125, v60
	v_fmac_f32_e32 v57, v125, v56
	v_fmac_f32_e32 v53, v125, v52
	v_fmac_f32_e32 v49, v125, v48
	v_fmac_f32_e32 v45, v125, v44
	v_fmac_f32_e32 v41, v125, v40
	v_fmac_f32_e32 v37, v125, v36
	v_fmac_f32_e32 v30, v96, v27
	v_or_b32_sdwa v98, v100, v95 dst_sel:DWORD dst_unused:UNUSED_PAD src0_sel:DWORD src1_sel:WORD_1
	v_addc_co_u32_e32 v95, vcc, 0, v121, vcc
	v_fmac_f32_e32 v89, v96, v87
	v_fmac_f32_e32 v85, v96, v83
	v_fmac_f32_e32 v81, v96, v79
	v_fmac_f32_e32 v77, v96, v75
	v_fmac_f32_e32 v73, v96, v71
	v_fmac_f32_e32 v69, v96, v67
	v_fmac_f32_e32 v65, v96, v63
	v_fmac_f32_e32 v61, v96, v59
	v_fmac_f32_e32 v57, v96, v55
	v_fmac_f32_e32 v53, v96, v51
	v_fmac_f32_e32 v49, v96, v47
	v_fmac_f32_e32 v45, v96, v43
	v_fmac_f32_e32 v41, v96, v39
	v_fmac_f32_e32 v37, v96, v35
	v_fmac_f32_e32 v30, v124, v26
	global_store_dwordx2 v[94:95], v[98:99], off
	v_fmac_f32_e32 v89, v124, v86
	v_fmac_f32_e32 v85, v124, v82
	v_fmac_f32_e32 v81, v124, v78
	v_fmac_f32_e32 v77, v124, v74
	v_fmac_f32_e32 v73, v124, v70
	v_fmac_f32_e32 v69, v124, v66
	v_fmac_f32_e32 v65, v124, v62
	v_fmac_f32_e32 v61, v124, v58
	v_fmac_f32_e32 v57, v124, v54
	v_fmac_f32_e32 v53, v124, v50
	v_fmac_f32_e32 v49, v124, v46
	v_fmac_f32_e32 v45, v124, v42
	v_fmac_f32_e32 v41, v124, v38
	v_fmac_f32_e32 v37, v124, v34
	ds_read_b128 v[96:99], v143
	ds_read_b128 v[100:103], v118 offset:1024
	ds_read_b128 v[120:123], v116 offset:1024
	v_mov_b32_e32 v26, v90
	v_mov_b32_e32 v27, v92
	v_pk_mul_f32 v[26:27], v[26:27], v[114:115] op_sel_hi:[1,0]
	s_waitcnt lgkmcnt(0)
	v_mov_b32_e32 v28, v96
	v_mov_b32_e32 v29, v98
	v_pk_mul_f32 v[26:27], v[26:27], v[28:29]
	v_mov_b32_e32 v92, v91
	v_mov_b32_e32 v98, v97
	s_waitcnt lgkmcnt(0)
	v_mov_b32_e32 v34, v100
	v_mov_b32_e32 v28, v120
	v_mov_b32_e32 v29, v122
	v_pk_add_f32 v[28:29], v[28:29], 1.0 op_sel_hi:[1,0]
	v_mov_b32_e32 v35, v102
	v_pk_fma_f32 v[26:27], v[26:27], v[28:29], v[34:35]
	v_pk_mul_f32 v[28:29], v[92:93], v[114:115] op_sel_hi:[1,0]
	ds_read_b128 v[90:93], v134 offset:1024
	v_mov_b32_e32 v122, v121
	v_pk_mul_f32 v[28:29], v[28:29], v[98:99]
	v_pk_add_f32 v[34:35], v[122:123], 1.0 op_sel_hi:[1,0]
	v_mov_b32_e32 v102, v101
	v_pk_fma_f32 v[28:29], v[28:29], v[34:35], v[102:103]
	v_and_b32_sdwa v31, v27, v208 dst_sel:DWORD dst_unused:UNUSED_PAD src0_sel:WORD_1 src1_sel:DWORD
	s_waitcnt lgkmcnt(0)
	v_fmac_f32_e32 v89, v29, v93
	v_fmac_f32_e32 v89, v27, v92
	v_fmac_f32_e32 v89, v28, v91
	v_fmac_f32_e32 v89, v26, v90
	ds_read_b128 v[90:93], v134 offset:9216
	v_and_b32_sdwa v34, v29, v208 dst_sel:DWORD dst_unused:UNUSED_PAD src0_sel:WORD_1 src1_sel:DWORD
	v_and_b32_sdwa v35, v28, v208 dst_sel:DWORD dst_unused:UNUSED_PAD src0_sel:WORD_1 src1_sel:DWORD
	v_and_b32_sdwa v32, v26, v208 dst_sel:DWORD dst_unused:UNUSED_PAD src0_sel:WORD_1 src1_sel:DWORD
	v_add3_u32 v34, v29, v34, s57
	s_waitcnt lgkmcnt(0)
	v_fmac_f32_e32 v85, v29, v93
	v_fmac_f32_e32 v85, v27, v92
	v_fmac_f32_e32 v85, v28, v91
	v_fmac_f32_e32 v85, v26, v90
	ds_read_b128 v[90:93], v134 offset:17408
	v_add3_u32 v35, v28, v35, s57
	v_add3_u32 v32, v26, v32, s57
	v_add3_u32 v31, v27, v31, s57
	v_and_b32_e32 v34, 0xffff0000, v34
	s_waitcnt lgkmcnt(0)
	v_fmac_f32_e32 v81, v29, v93
	v_fmac_f32_e32 v81, v27, v92
	v_fmac_f32_e32 v81, v28, v91
	v_fmac_f32_e32 v81, v26, v90
	ds_read_b128 v[90:93], v134 offset:25600
	v_and_b32_e32 v36, 0xffff0000, v35
	v_or_b32_sdwa v35, v34, v31 dst_sel:DWORD dst_unused:UNUSED_PAD src0_sel:DWORD src1_sel:WORD_1
	v_or_b32_sdwa v34, v36, v32 dst_sel:DWORD dst_unused:UNUSED_PAD src0_sel:DWORD src1_sel:WORD_1
	global_store_dwordx2 v[94:95], v[34:35], off offset:512
	s_waitcnt lgkmcnt(0)
	v_fmac_f32_e32 v77, v29, v93
	v_fmac_f32_e32 v77, v27, v92
	v_fmac_f32_e32 v77, v28, v91
	v_fmac_f32_e32 v77, v26, v90
	ds_read_b128 v[90:93], v134 offset:33792
	s_waitcnt lgkmcnt(0)
	v_fmac_f32_e32 v73, v29, v93
	v_fmac_f32_e32 v73, v27, v92
	v_fmac_f32_e32 v73, v28, v91
	v_fmac_f32_e32 v73, v26, v90
	ds_read_b128 v[90:93], v134 offset:41984
	s_waitcnt lgkmcnt(0)
	v_fmac_f32_e32 v69, v29, v93
	v_fmac_f32_e32 v69, v27, v92
	v_fmac_f32_e32 v69, v28, v91
	v_fmac_f32_e32 v69, v26, v90
	ds_read_b128 v[90:93], v134 offset:50176
	s_waitcnt lgkmcnt(0)
	v_fmac_f32_e32 v65, v29, v93
	v_fmac_f32_e32 v65, v27, v92
	v_fmac_f32_e32 v65, v28, v91
	v_fmac_f32_e32 v65, v26, v90
	ds_read_b128 v[90:93], v134 offset:58368
	s_waitcnt lgkmcnt(0)
	v_fmac_f32_e32 v61, v29, v93
	v_fmac_f32_e32 v61, v27, v92
	v_fmac_f32_e32 v61, v28, v91
	v_fmac_f32_e32 v61, v26, v90
	ds_read_b128 v[90:93], v144
	s_waitcnt lgkmcnt(0)
	v_fmac_f32_e32 v57, v29, v93
	v_fmac_f32_e32 v57, v27, v92
	v_fmac_f32_e32 v57, v28, v91
	v_fmac_f32_e32 v57, v26, v90
	ds_read_b128 v[90:93], v145
	s_waitcnt lgkmcnt(0)
	v_fmac_f32_e32 v53, v29, v93
	v_fmac_f32_e32 v53, v27, v92
	v_fmac_f32_e32 v53, v28, v91
	v_fmac_f32_e32 v53, v26, v90
	ds_read_b128 v[90:93], v146
	s_waitcnt lgkmcnt(0)
	v_fmac_f32_e32 v49, v29, v93
	v_fmac_f32_e32 v49, v27, v92
	v_fmac_f32_e32 v49, v28, v91
	v_fmac_f32_e32 v49, v26, v90
	ds_read_b128 v[90:93], v147
	s_waitcnt lgkmcnt(0)
	v_fmac_f32_e32 v45, v29, v93
	v_fmac_f32_e32 v45, v27, v92
	v_fmac_f32_e32 v45, v28, v91
	v_fmac_f32_e32 v45, v26, v90
	ds_read_b128 v[90:93], v148
	s_waitcnt lgkmcnt(0)
	v_fmac_f32_e32 v41, v29, v93
	v_fmac_f32_e32 v41, v27, v92
	v_fmac_f32_e32 v41, v28, v91
	v_fmac_f32_e32 v41, v26, v90
	ds_read_b128 v[90:93], v149
	s_waitcnt lgkmcnt(0)
	v_fmac_f32_e32 v37, v29, v93
	v_fmac_f32_e32 v37, v27, v92
	v_fmac_f32_e32 v37, v28, v91
	v_fmac_f32_e32 v37, v26, v90
	ds_read_b128 v[90:93], v150
	s_waitcnt lgkmcnt(0)
	v_fmac_f32_e32 v33, v29, v93
	v_fmac_f32_e32 v33, v27, v92
	v_fmac_f32_e32 v33, v28, v91
	v_fmac_f32_e32 v33, v26, v90
	ds_read_b128 v[90:93], v151
	s_waitcnt lgkmcnt(0)
	v_fmac_f32_e32 v30, v29, v93
	v_fmac_f32_e32 v30, v27, v92
	v_fmac_f32_e32 v30, v28, v91
	v_fmac_f32_e32 v30, v26, v90
	ds_read_b128 v[90:93], v152
	ds_read_b128 v[96:99], v118 offset:2048
	ds_read_b128 v[100:103], v116 offset:2048
	v_mov_b32_e32 v27, v24
	v_mov_b32_e32 v24, v23
	v_mov_b32_e32 v26, v22
	s_waitcnt lgkmcnt(0)
	v_mov_b32_e32 v29, v92
	v_pk_mul_f32 v[22:23], v[24:25], v[114:115] op_sel_hi:[1,0]
	v_mov_b32_e32 v92, v91
	v_mov_b32_e32 v28, v90
	v_pk_mul_f32 v[22:23], v[22:23], v[92:93]
	ds_read_b128 v[90:93], v134 offset:2048
	v_pk_mul_f32 v[26:27], v[26:27], v[114:115] op_sel_hi:[1,0]
	s_waitcnt lgkmcnt(0)
	v_mov_b32_e32 v35, v98
	v_pk_mul_f32 v[26:27], v[26:27], v[28:29]
	v_mov_b32_e32 v29, v102
	v_mov_b32_e32 v102, v101
	v_mov_b32_e32 v28, v100
	v_pk_add_f32 v[24:25], v[102:103], 1.0 op_sel_hi:[1,0]
	v_mov_b32_e32 v98, v97
	v_pk_add_f32 v[28:29], v[28:29], 1.0 op_sel_hi:[1,0]
	v_mov_b32_e32 v34, v96
	v_pk_fma_f32 v[22:23], v[22:23], v[24:25], v[98:99]
	v_pk_fma_f32 v[26:27], v[26:27], v[28:29], v[34:35]
	s_waitcnt lgkmcnt(0)
	v_fmac_f32_e32 v89, v23, v93
	v_fmac_f32_e32 v89, v27, v92
	v_fmac_f32_e32 v89, v22, v91
	v_fmac_f32_e32 v89, v26, v90
	ds_read_b128 v[90:93], v134 offset:10240
	v_and_b32_sdwa v25, v26, v208 dst_sel:DWORD dst_unused:UNUSED_PAD src0_sel:WORD_1 src1_sel:DWORD
	v_add3_u32 v28, v26, v25, s57
	v_and_b32_sdwa v25, v23, v208 dst_sel:DWORD dst_unused:UNUSED_PAD src0_sel:WORD_1 src1_sel:DWORD
	v_and_b32_sdwa v29, v22, v208 dst_sel:DWORD dst_unused:UNUSED_PAD src0_sel:WORD_1 src1_sel:DWORD
	s_waitcnt lgkmcnt(0)
	v_fmac_f32_e32 v85, v23, v93
	v_fmac_f32_e32 v85, v27, v92
	v_fmac_f32_e32 v85, v22, v91
	v_fmac_f32_e32 v85, v26, v90
	ds_read_b128 v[90:93], v134 offset:18432
	v_and_b32_sdwa v24, v27, v208 dst_sel:DWORD dst_unused:UNUSED_PAD src0_sel:WORD_1 src1_sel:DWORD
	v_add3_u32 v25, v23, v25, s57
	v_add3_u32 v29, v22, v29, s57
	v_add3_u32 v24, v27, v24, s57
	s_waitcnt lgkmcnt(0)
	v_fmac_f32_e32 v81, v23, v93
	v_fmac_f32_e32 v81, v27, v92
	v_fmac_f32_e32 v81, v22, v91
	v_fmac_f32_e32 v81, v26, v90
	ds_read_b128 v[90:93], v134 offset:26624
	v_and_b32_e32 v25, 0xffff0000, v25
	v_and_b32_e32 v29, 0xffff0000, v29
	v_or_b32_sdwa v25, v25, v24 dst_sel:DWORD dst_unused:UNUSED_PAD src0_sel:DWORD src1_sel:WORD_1
	v_or_b32_sdwa v24, v29, v28 dst_sel:DWORD dst_unused:UNUSED_PAD src0_sel:DWORD src1_sel:WORD_1
	s_waitcnt lgkmcnt(0)
	v_fmac_f32_e32 v77, v23, v93
	v_fmac_f32_e32 v77, v27, v92
	v_fmac_f32_e32 v77, v22, v91
	v_fmac_f32_e32 v77, v26, v90
	ds_read_b128 v[90:93], v134 offset:34816
	global_store_dwordx2 v[94:95], v[24:25], off offset:1024
	s_waitcnt lgkmcnt(0)
	v_fmac_f32_e32 v73, v23, v93
	v_fmac_f32_e32 v73, v27, v92
	v_fmac_f32_e32 v73, v22, v91
	v_fmac_f32_e32 v73, v26, v90
	ds_read_b128 v[90:93], v134 offset:43008
	s_waitcnt lgkmcnt(0)
	v_fmac_f32_e32 v69, v23, v93
	v_fmac_f32_e32 v69, v27, v92
	v_fmac_f32_e32 v69, v22, v91
	v_fmac_f32_e32 v69, v26, v90
	ds_read_b128 v[90:93], v134 offset:51200
	s_waitcnt lgkmcnt(0)
	v_fmac_f32_e32 v65, v23, v93
	v_fmac_f32_e32 v65, v27, v92
	v_fmac_f32_e32 v65, v22, v91
	v_fmac_f32_e32 v65, v26, v90
	ds_read_b128 v[90:93], v134 offset:59392
	s_waitcnt lgkmcnt(0)
	v_fmac_f32_e32 v61, v23, v93
	v_fmac_f32_e32 v61, v27, v92
	v_fmac_f32_e32 v61, v22, v91
	v_fmac_f32_e32 v61, v26, v90
	ds_read_b128 v[90:93], v153
	s_waitcnt lgkmcnt(0)
	v_fmac_f32_e32 v57, v23, v93
	v_fmac_f32_e32 v57, v27, v92
	v_fmac_f32_e32 v57, v22, v91
	v_fmac_f32_e32 v57, v26, v90
	ds_read_b128 v[90:93], v154
	s_waitcnt lgkmcnt(0)
	v_fmac_f32_e32 v53, v23, v93
	v_fmac_f32_e32 v53, v27, v92
	v_fmac_f32_e32 v53, v22, v91
	v_fmac_f32_e32 v53, v26, v90
	ds_read_b128 v[90:93], v155
	s_waitcnt lgkmcnt(0)
	v_fmac_f32_e32 v49, v23, v93
	v_fmac_f32_e32 v49, v27, v92
	v_fmac_f32_e32 v49, v22, v91
	v_fmac_f32_e32 v49, v26, v90
	ds_read_b128 v[90:93], v156
	s_waitcnt lgkmcnt(0)
	v_fmac_f32_e32 v45, v23, v93
	v_fmac_f32_e32 v45, v27, v92
	v_fmac_f32_e32 v45, v22, v91
	v_fmac_f32_e32 v45, v26, v90
	ds_read_b128 v[90:93], v157
	s_waitcnt lgkmcnt(0)
	v_fmac_f32_e32 v41, v23, v93
	v_fmac_f32_e32 v41, v27, v92
	v_fmac_f32_e32 v41, v22, v91
	v_fmac_f32_e32 v41, v26, v90
	ds_read_b128 v[90:93], v158
	s_waitcnt lgkmcnt(0)
	v_fmac_f32_e32 v37, v23, v93
	v_fmac_f32_e32 v37, v27, v92
	v_fmac_f32_e32 v37, v22, v91
	v_fmac_f32_e32 v37, v26, v90
	ds_read_b128 v[90:93], v159
	s_waitcnt lgkmcnt(0)
	v_fmac_f32_e32 v33, v23, v93
	v_fmac_f32_e32 v33, v27, v92
	v_fmac_f32_e32 v33, v22, v91
	v_fmac_f32_e32 v33, v26, v90
	ds_read_b128 v[90:93], v160
	s_waitcnt lgkmcnt(0)
	v_fmac_f32_e32 v30, v23, v93
	v_fmac_f32_e32 v30, v27, v92
	v_fmac_f32_e32 v30, v22, v91
	v_fmac_f32_e32 v30, v26, v90
	ds_read_b128 v[24:27], v161
	ds_read_b128 v[90:93], v118 offset:3072
	ds_read_b128 v[96:99], v116 offset:3072
	v_mov_b32_e32 v22, v18
	v_mov_b32_e32 v23, v20
	v_pk_mul_f32 v[22:23], v[22:23], v[114:115] op_sel_hi:[1,0]
	s_waitcnt lgkmcnt(0)
	v_mov_b32_e32 v28, v24
	v_mov_b32_e32 v29, v26
	v_pk_mul_f32 v[22:23], v[22:23], v[28:29]
	v_mov_b32_e32 v20, v19
	v_pk_mul_f32 v[18:19], v[20:21], v[114:115] op_sel_hi:[1,0]
	v_mov_b32_e32 v26, v25
	v_pk_mul_f32 v[18:19], v[18:19], v[26:27]
	s_waitcnt lgkmcnt(0)
	v_mov_b32_e32 v34, v90
	v_mov_b32_e32 v28, v96
	v_mov_b32_e32 v29, v98
	v_pk_add_f32 v[28:29], v[28:29], 1.0 op_sel_hi:[1,0]
	v_mov_b32_e32 v35, v92
	v_mov_b32_e32 v98, v97
	v_pk_fma_f32 v[22:23], v[22:23], v[28:29], v[34:35]
	v_pk_add_f32 v[20:21], v[98:99], 1.0 op_sel_hi:[1,0]
	v_mov_b32_e32 v92, v91
	v_pk_fma_f32 v[18:19], v[18:19], v[20:21], v[92:93]
	v_and_b32_sdwa v21, v22, v208 dst_sel:DWORD dst_unused:UNUSED_PAD src0_sel:WORD_1 src1_sel:DWORD
	v_add3_u32 v24, v22, v21, s57
	v_and_b32_sdwa v21, v19, v208 dst_sel:DWORD dst_unused:UNUSED_PAD src0_sel:WORD_1 src1_sel:DWORD
	v_and_b32_sdwa v25, v18, v208 dst_sel:DWORD dst_unused:UNUSED_PAD src0_sel:WORD_1 src1_sel:DWORD
	v_and_b32_sdwa v20, v23, v208 dst_sel:DWORD dst_unused:UNUSED_PAD src0_sel:WORD_1 src1_sel:DWORD
	v_add3_u32 v21, v19, v21, s57
	v_add3_u32 v25, v18, v25, s57
	v_add3_u32 v20, v23, v20, s57
	v_and_b32_e32 v21, 0xffff0000, v21
	v_and_b32_e32 v25, 0xffff0000, v25
	v_or_b32_sdwa v21, v21, v20 dst_sel:DWORD dst_unused:UNUSED_PAD src0_sel:DWORD src1_sel:WORD_1
	v_or_b32_sdwa v20, v25, v24 dst_sel:DWORD dst_unused:UNUSED_PAD src0_sel:DWORD src1_sel:WORD_1
	ds_read_b128 v[24:27], v134 offset:3072
	global_store_dwordx2 v[94:95], v[20:21], off offset:1536
	s_waitcnt lgkmcnt(0)
	v_fmac_f32_e32 v89, v19, v27
	v_fmac_f32_e32 v89, v23, v26
	v_fmac_f32_e32 v89, v18, v25
	v_fmac_f32_e32 v89, v22, v24
	ds_read_b128 v[24:27], v134 offset:11264
	s_waitcnt lgkmcnt(0)
	v_fmac_f32_e32 v85, v19, v27
	v_fmac_f32_e32 v85, v23, v26
	v_fmac_f32_e32 v85, v18, v25
	v_fmac_f32_e32 v85, v22, v24
	ds_read_b128 v[24:27], v134 offset:19456
	s_waitcnt lgkmcnt(0)
	v_fmac_f32_e32 v81, v19, v27
	v_fmac_f32_e32 v81, v23, v26
	v_fmac_f32_e32 v81, v18, v25
	v_fmac_f32_e32 v81, v22, v24
	ds_read_b128 v[24:27], v134 offset:27648
	s_waitcnt lgkmcnt(0)
	v_fmac_f32_e32 v77, v19, v27
	v_fmac_f32_e32 v77, v23, v26
	v_fmac_f32_e32 v77, v18, v25
	v_fmac_f32_e32 v77, v22, v24
	ds_read_b128 v[24:27], v134 offset:35840
	s_waitcnt lgkmcnt(0)
	v_fmac_f32_e32 v73, v19, v27
	v_fmac_f32_e32 v73, v23, v26
	v_fmac_f32_e32 v73, v18, v25
	v_fmac_f32_e32 v73, v22, v24
	ds_read_b128 v[24:27], v134 offset:44032
	s_waitcnt lgkmcnt(0)
	v_fmac_f32_e32 v69, v19, v27
	v_fmac_f32_e32 v69, v23, v26
	v_fmac_f32_e32 v69, v18, v25
	v_fmac_f32_e32 v69, v22, v24
	ds_read_b128 v[24:27], v134 offset:52224
	s_waitcnt lgkmcnt(0)
	v_fmac_f32_e32 v65, v19, v27
	v_fmac_f32_e32 v65, v23, v26
	v_fmac_f32_e32 v65, v18, v25
	v_fmac_f32_e32 v65, v22, v24
	ds_read_b128 v[24:27], v134 offset:60416
	s_waitcnt lgkmcnt(0)
	v_fmac_f32_e32 v61, v19, v27
	v_fmac_f32_e32 v61, v23, v26
	v_fmac_f32_e32 v61, v18, v25
	v_fmac_f32_e32 v61, v22, v24
	ds_read_b128 v[24:27], v162
	s_waitcnt lgkmcnt(0)
	v_fmac_f32_e32 v57, v19, v27
	v_fmac_f32_e32 v57, v23, v26
	v_fmac_f32_e32 v57, v18, v25
	v_fmac_f32_e32 v57, v22, v24
	ds_read_b128 v[24:27], v163
	s_waitcnt lgkmcnt(0)
	v_fmac_f32_e32 v53, v19, v27
	v_fmac_f32_e32 v53, v23, v26
	v_fmac_f32_e32 v53, v18, v25
	v_fmac_f32_e32 v53, v22, v24
	ds_read_b128 v[24:27], v164
	s_waitcnt lgkmcnt(0)
	v_fmac_f32_e32 v49, v19, v27
	v_fmac_f32_e32 v49, v23, v26
	v_fmac_f32_e32 v49, v18, v25
	v_fmac_f32_e32 v49, v22, v24
	ds_read_b128 v[24:27], v165
	s_waitcnt lgkmcnt(0)
	v_fmac_f32_e32 v45, v19, v27
	v_fmac_f32_e32 v45, v23, v26
	v_fmac_f32_e32 v45, v18, v25
	v_fmac_f32_e32 v45, v22, v24
	ds_read_b128 v[24:27], v166
	s_waitcnt lgkmcnt(0)
	v_fmac_f32_e32 v41, v19, v27
	v_fmac_f32_e32 v41, v23, v26
	v_fmac_f32_e32 v41, v18, v25
	v_fmac_f32_e32 v41, v22, v24
	ds_read_b128 v[24:27], v167
	s_waitcnt lgkmcnt(0)
	v_fmac_f32_e32 v37, v19, v27
	v_fmac_f32_e32 v37, v23, v26
	v_fmac_f32_e32 v37, v18, v25
	v_fmac_f32_e32 v37, v22, v24
	ds_read_b128 v[24:27], v168
	s_waitcnt lgkmcnt(0)
	v_fmac_f32_e32 v33, v19, v27
	v_fmac_f32_e32 v33, v23, v26
	v_fmac_f32_e32 v33, v18, v25
	v_fmac_f32_e32 v33, v22, v24
	ds_read_b128 v[24:27], v169
	s_waitcnt lgkmcnt(0)
	v_fmac_f32_e32 v30, v19, v27
	v_fmac_f32_e32 v30, v23, v26
	v_fmac_f32_e32 v30, v18, v25
	v_fmac_f32_e32 v30, v22, v24
	v_add_co_u32_e32 v18, vcc, s56, v118
	ds_read_b128 v[24:27], v170
	s_nop 0
	v_addc_co_u32_e32 v19, vcc, 0, v119, vcc
	v_add_co_u32_e32 v20, vcc, s56, v116
	ds_read_b128 v[90:93], v18
	s_nop 0
	v_addc_co_u32_e32 v21, vcc, 0, v117, vcc
	ds_read_b128 v[96:99], v20
	v_mov_b32_e32 v22, v14
	v_mov_b32_e32 v23, v16
	v_pk_mul_f32 v[22:23], v[22:23], v[114:115] op_sel_hi:[1,0]
	s_waitcnt lgkmcnt(0)
	v_mov_b32_e32 v28, v24
	v_mov_b32_e32 v29, v26
	v_pk_mul_f32 v[22:23], v[22:23], v[28:29]
	v_mov_b32_e32 v16, v15
	v_pk_mul_f32 v[14:15], v[16:17], v[114:115] op_sel_hi:[1,0]
	v_mov_b32_e32 v26, v25
	v_pk_mul_f32 v[14:15], v[14:15], v[26:27]
	s_waitcnt lgkmcnt(0)
	v_mov_b32_e32 v34, v90
	v_mov_b32_e32 v35, v92
	v_mov_b32_e32 v92, v91
	v_mov_b32_e32 v28, v96
	v_mov_b32_e32 v29, v98
	v_pk_add_f32 v[28:29], v[28:29], 1.0 op_sel_hi:[1,0]
	v_mov_b32_e32 v98, v97
	v_pk_fma_f32 v[22:23], v[22:23], v[28:29], v[34:35]
	v_pk_add_f32 v[16:17], v[98:99], 1.0 op_sel_hi:[1,0]
	s_nop 0
	v_pk_fma_f32 v[14:15], v[14:15], v[16:17], v[92:93]
	v_and_b32_sdwa v17, v22, v208 dst_sel:DWORD dst_unused:UNUSED_PAD src0_sel:WORD_1 src1_sel:DWORD
	v_add3_u32 v24, v22, v17, s57
	v_and_b32_sdwa v17, v15, v208 dst_sel:DWORD dst_unused:UNUSED_PAD src0_sel:WORD_1 src1_sel:DWORD
	v_and_b32_sdwa v25, v14, v208 dst_sel:DWORD dst_unused:UNUSED_PAD src0_sel:WORD_1 src1_sel:DWORD
	v_and_b32_sdwa v16, v23, v208 dst_sel:DWORD dst_unused:UNUSED_PAD src0_sel:WORD_1 src1_sel:DWORD
	v_add3_u32 v17, v15, v17, s57
	v_add3_u32 v25, v14, v25, s57
	v_add3_u32 v16, v23, v16, s57
	v_and_b32_e32 v17, 0xffff0000, v17
	v_and_b32_e32 v25, 0xffff0000, v25
	v_or_b32_sdwa v17, v17, v16 dst_sel:DWORD dst_unused:UNUSED_PAD src0_sel:DWORD src1_sel:WORD_1
	v_or_b32_sdwa v16, v25, v24 dst_sel:DWORD dst_unused:UNUSED_PAD src0_sel:DWORD src1_sel:WORD_1
	ds_read_b128 v[24:27], v134 offset:4096
	global_store_dwordx2 v[94:95], v[16:17], off offset:2048
	s_waitcnt lgkmcnt(0)
	v_fmac_f32_e32 v89, v15, v27
	v_fmac_f32_e32 v89, v23, v26
	v_fmac_f32_e32 v89, v14, v25
	v_fmac_f32_e32 v89, v22, v24
	ds_read_b128 v[24:27], v134 offset:12288
	s_waitcnt lgkmcnt(0)
	v_fmac_f32_e32 v85, v15, v27
	v_fmac_f32_e32 v85, v23, v26
	v_fmac_f32_e32 v85, v14, v25
	v_fmac_f32_e32 v85, v22, v24
	ds_read_b128 v[24:27], v134 offset:20480
	s_waitcnt lgkmcnt(0)
	v_fmac_f32_e32 v81, v15, v27
	v_fmac_f32_e32 v81, v23, v26
	v_fmac_f32_e32 v81, v14, v25
	v_fmac_f32_e32 v81, v22, v24
	ds_read_b128 v[24:27], v134 offset:28672
	s_waitcnt lgkmcnt(0)
	v_fmac_f32_e32 v77, v15, v27
	v_fmac_f32_e32 v77, v23, v26
	v_fmac_f32_e32 v77, v14, v25
	v_fmac_f32_e32 v77, v22, v24
	ds_read_b128 v[24:27], v134 offset:36864
	s_waitcnt lgkmcnt(0)
	v_fmac_f32_e32 v73, v15, v27
	v_fmac_f32_e32 v73, v23, v26
	v_fmac_f32_e32 v73, v14, v25
	v_fmac_f32_e32 v73, v22, v24
	ds_read_b128 v[24:27], v134 offset:45056
	s_waitcnt lgkmcnt(0)
	v_fmac_f32_e32 v69, v15, v27
	v_fmac_f32_e32 v69, v23, v26
	v_fmac_f32_e32 v69, v14, v25
	v_fmac_f32_e32 v69, v22, v24
	ds_read_b128 v[24:27], v134 offset:53248
	s_waitcnt lgkmcnt(0)
	v_fmac_f32_e32 v65, v15, v27
	v_fmac_f32_e32 v65, v23, v26
	v_fmac_f32_e32 v65, v14, v25
	v_fmac_f32_e32 v65, v22, v24
	ds_read_b128 v[24:27], v134 offset:61440
	s_waitcnt lgkmcnt(0)
	v_fmac_f32_e32 v61, v15, v27
	v_fmac_f32_e32 v61, v23, v26
	v_fmac_f32_e32 v61, v14, v25
	v_fmac_f32_e32 v61, v22, v24
	ds_read_b128 v[24:27], v171
	s_waitcnt lgkmcnt(0)
	v_fmac_f32_e32 v57, v15, v27
	v_fmac_f32_e32 v57, v23, v26
	v_fmac_f32_e32 v57, v14, v25
	v_fmac_f32_e32 v57, v22, v24
	ds_read_b128 v[24:27], v172
	s_waitcnt lgkmcnt(0)
	v_fmac_f32_e32 v53, v15, v27
	v_fmac_f32_e32 v53, v23, v26
	v_fmac_f32_e32 v53, v14, v25
	v_fmac_f32_e32 v53, v22, v24
	ds_read_b128 v[24:27], v173
	s_waitcnt lgkmcnt(0)
	v_fmac_f32_e32 v49, v15, v27
	v_fmac_f32_e32 v49, v23, v26
	v_fmac_f32_e32 v49, v14, v25
	v_fmac_f32_e32 v49, v22, v24
	ds_read_b128 v[24:27], v174
	s_waitcnt lgkmcnt(0)
	v_fmac_f32_e32 v45, v15, v27
	v_fmac_f32_e32 v45, v23, v26
	v_fmac_f32_e32 v45, v14, v25
	v_fmac_f32_e32 v45, v22, v24
	ds_read_b128 v[24:27], v175
	s_waitcnt lgkmcnt(0)
	v_fmac_f32_e32 v41, v15, v27
	v_fmac_f32_e32 v41, v23, v26
	v_fmac_f32_e32 v41, v14, v25
	v_fmac_f32_e32 v41, v22, v24
	ds_read_b128 v[24:27], v176
	s_waitcnt lgkmcnt(0)
	v_fmac_f32_e32 v37, v15, v27
	v_fmac_f32_e32 v37, v23, v26
	v_fmac_f32_e32 v37, v14, v25
	v_fmac_f32_e32 v37, v22, v24
	ds_read_b128 v[24:27], v177
	s_waitcnt lgkmcnt(0)
	v_fmac_f32_e32 v33, v15, v27
	v_fmac_f32_e32 v33, v23, v26
	v_fmac_f32_e32 v33, v14, v25
	v_fmac_f32_e32 v33, v22, v24
	ds_read_b128 v[24:27], v178
	s_waitcnt lgkmcnt(0)
	v_fmac_f32_e32 v30, v15, v27
	v_fmac_f32_e32 v30, v23, v26
	v_fmac_f32_e32 v30, v14, v25
	v_fmac_f32_e32 v30, v22, v24
	ds_read_b128 v[22:25], v179
	ds_read_b128 v[26:29], v18 offset:1024
	ds_read_b128 v[90:93], v20 offset:1024
	v_mov_b32_e32 v15, v12
	v_mov_b32_e32 v12, v11
	v_mov_b32_e32 v14, v10
	s_waitcnt lgkmcnt(0)
	v_mov_b32_e32 v17, v24
	v_pk_mul_f32 v[10:11], v[12:13], v[114:115] op_sel_hi:[1,0]
	v_mov_b32_e32 v24, v23
	v_mov_b32_e32 v16, v22
	v_pk_mul_f32 v[10:11], v[10:11], v[24:25]
	ds_read_b128 v[22:25], v134 offset:5120
	v_pk_mul_f32 v[14:15], v[14:15], v[114:115] op_sel_hi:[1,0]
	s_waitcnt lgkmcnt(0)
	v_mov_b32_e32 v35, v28
	v_pk_mul_f32 v[14:15], v[14:15], v[16:17]
	v_mov_b32_e32 v17, v92
	v_mov_b32_e32 v92, v91
	v_mov_b32_e32 v16, v90
	v_pk_add_f32 v[12:13], v[92:93], 1.0 op_sel_hi:[1,0]
	v_mov_b32_e32 v28, v27
	v_pk_add_f32 v[16:17], v[16:17], 1.0 op_sel_hi:[1,0]
	v_mov_b32_e32 v34, v26
	v_pk_fma_f32 v[10:11], v[10:11], v[12:13], v[28:29]
	v_pk_fma_f32 v[14:15], v[14:15], v[16:17], v[34:35]
	s_waitcnt lgkmcnt(0)
	v_fmac_f32_e32 v89, v11, v25
	v_fmac_f32_e32 v89, v15, v24
	v_fmac_f32_e32 v89, v10, v23
	v_fmac_f32_e32 v89, v14, v22
	ds_read_b128 v[22:25], v134 offset:13312
	v_and_b32_sdwa v13, v14, v208 dst_sel:DWORD dst_unused:UNUSED_PAD src0_sel:WORD_1 src1_sel:DWORD
	v_add3_u32 v16, v14, v13, s57
	v_and_b32_sdwa v13, v11, v208 dst_sel:DWORD dst_unused:UNUSED_PAD src0_sel:WORD_1 src1_sel:DWORD
	v_and_b32_sdwa v17, v10, v208 dst_sel:DWORD dst_unused:UNUSED_PAD src0_sel:WORD_1 src1_sel:DWORD
	s_waitcnt lgkmcnt(0)
	v_fmac_f32_e32 v85, v11, v25
	v_fmac_f32_e32 v85, v15, v24
	v_fmac_f32_e32 v85, v10, v23
	v_fmac_f32_e32 v85, v14, v22
	ds_read_b128 v[22:25], v134 offset:21504
	v_and_b32_sdwa v12, v15, v208 dst_sel:DWORD dst_unused:UNUSED_PAD src0_sel:WORD_1 src1_sel:DWORD
	v_add3_u32 v13, v11, v13, s57
	v_add3_u32 v17, v10, v17, s57
	v_add3_u32 v12, v15, v12, s57
	s_waitcnt lgkmcnt(0)
	v_fmac_f32_e32 v81, v11, v25
	v_fmac_f32_e32 v81, v15, v24
	v_fmac_f32_e32 v81, v10, v23
	v_fmac_f32_e32 v81, v14, v22
	ds_read_b128 v[22:25], v134 offset:29696
	v_and_b32_e32 v13, 0xffff0000, v13
	v_and_b32_e32 v17, 0xffff0000, v17
	v_or_b32_sdwa v13, v13, v12 dst_sel:DWORD dst_unused:UNUSED_PAD src0_sel:DWORD src1_sel:WORD_1
	v_or_b32_sdwa v12, v17, v16 dst_sel:DWORD dst_unused:UNUSED_PAD src0_sel:DWORD src1_sel:WORD_1
	s_waitcnt lgkmcnt(0)
	v_fmac_f32_e32 v77, v11, v25
	v_fmac_f32_e32 v77, v15, v24
	v_fmac_f32_e32 v77, v10, v23
	v_fmac_f32_e32 v77, v14, v22
	ds_read_b128 v[22:25], v134 offset:37888
	global_store_dwordx2 v[94:95], v[12:13], off offset:2560
	s_waitcnt lgkmcnt(0)
	v_fmac_f32_e32 v73, v11, v25
	v_fmac_f32_e32 v73, v15, v24
	v_fmac_f32_e32 v73, v10, v23
	v_fmac_f32_e32 v73, v14, v22
	ds_read_b128 v[22:25], v134 offset:46080
	s_waitcnt lgkmcnt(0)
	v_fmac_f32_e32 v69, v11, v25
	v_fmac_f32_e32 v69, v15, v24
	v_fmac_f32_e32 v69, v10, v23
	v_fmac_f32_e32 v69, v14, v22
	ds_read_b128 v[22:25], v134 offset:54272
	s_waitcnt lgkmcnt(0)
	v_fmac_f32_e32 v65, v11, v25
	v_fmac_f32_e32 v65, v15, v24
	v_fmac_f32_e32 v65, v10, v23
	v_fmac_f32_e32 v65, v14, v22
	ds_read_b128 v[22:25], v134 offset:62464
	s_waitcnt lgkmcnt(0)
	v_fmac_f32_e32 v61, v11, v25
	v_fmac_f32_e32 v61, v15, v24
	v_fmac_f32_e32 v61, v10, v23
	v_fmac_f32_e32 v61, v14, v22
	ds_read_b128 v[22:25], v180
	s_waitcnt lgkmcnt(0)
	v_fmac_f32_e32 v57, v11, v25
	v_fmac_f32_e32 v57, v15, v24
	v_fmac_f32_e32 v57, v10, v23
	v_fmac_f32_e32 v57, v14, v22
	ds_read_b128 v[22:25], v181
	s_waitcnt lgkmcnt(0)
	v_fmac_f32_e32 v53, v11, v25
	v_fmac_f32_e32 v53, v15, v24
	v_fmac_f32_e32 v53, v10, v23
	v_fmac_f32_e32 v53, v14, v22
	ds_read_b128 v[22:25], v182
	s_waitcnt lgkmcnt(0)
	v_fmac_f32_e32 v49, v11, v25
	v_fmac_f32_e32 v49, v15, v24
	v_fmac_f32_e32 v49, v10, v23
	v_fmac_f32_e32 v49, v14, v22
	ds_read_b128 v[22:25], v183
	s_waitcnt lgkmcnt(0)
	v_fmac_f32_e32 v45, v11, v25
	v_fmac_f32_e32 v45, v15, v24
	v_fmac_f32_e32 v45, v10, v23
	v_fmac_f32_e32 v45, v14, v22
	ds_read_b128 v[22:25], v184
	s_waitcnt lgkmcnt(0)
	v_fmac_f32_e32 v41, v11, v25
	v_fmac_f32_e32 v41, v15, v24
	v_fmac_f32_e32 v41, v10, v23
	v_fmac_f32_e32 v41, v14, v22
	ds_read_b128 v[22:25], v185
	s_waitcnt lgkmcnt(0)
	v_fmac_f32_e32 v37, v11, v25
	v_fmac_f32_e32 v37, v15, v24
	v_fmac_f32_e32 v37, v10, v23
	v_fmac_f32_e32 v37, v14, v22
	ds_read_b128 v[22:25], v186
	s_waitcnt lgkmcnt(0)
	v_fmac_f32_e32 v33, v11, v25
	v_fmac_f32_e32 v33, v15, v24
	v_fmac_f32_e32 v33, v10, v23
	v_fmac_f32_e32 v33, v14, v22
	ds_read_b128 v[22:25], v187
	s_waitcnt lgkmcnt(0)
	v_fmac_f32_e32 v30, v11, v25
	v_fmac_f32_e32 v30, v15, v24
	v_fmac_f32_e32 v30, v10, v23
	v_fmac_f32_e32 v30, v14, v22
	ds_read_b128 v[12:15], v188
	ds_read_b128 v[22:25], v18 offset:2048
	ds_read_b128 v[26:29], v20 offset:2048
	v_mov_b32_e32 v10, v6
	v_mov_b32_e32 v11, v8
	v_pk_mul_f32 v[10:11], v[10:11], v[114:115] op_sel_hi:[1,0]
	s_waitcnt lgkmcnt(0)
	v_mov_b32_e32 v16, v12
	v_mov_b32_e32 v17, v14
	v_pk_mul_f32 v[10:11], v[10:11], v[16:17]
	v_mov_b32_e32 v8, v7
	v_pk_mul_f32 v[6:7], v[8:9], v[114:115] op_sel_hi:[1,0]
	v_mov_b32_e32 v14, v13
	v_pk_mul_f32 v[6:7], v[6:7], v[14:15]
	s_waitcnt lgkmcnt(0)
	v_mov_b32_e32 v34, v22
	v_mov_b32_e32 v16, v26
	v_mov_b32_e32 v17, v28
	v_pk_add_f32 v[16:17], v[16:17], 1.0 op_sel_hi:[1,0]
	v_mov_b32_e32 v35, v24
	v_mov_b32_e32 v28, v27
	v_pk_fma_f32 v[10:11], v[10:11], v[16:17], v[34:35]
	v_pk_add_f32 v[8:9], v[28:29], 1.0 op_sel_hi:[1,0]
	v_mov_b32_e32 v24, v23
	v_pk_fma_f32 v[6:7], v[6:7], v[8:9], v[24:25]
	v_and_b32_sdwa v9, v10, v208 dst_sel:DWORD dst_unused:UNUSED_PAD src0_sel:WORD_1 src1_sel:DWORD
	v_add3_u32 v12, v10, v9, s57
	v_and_b32_sdwa v9, v7, v208 dst_sel:DWORD dst_unused:UNUSED_PAD src0_sel:WORD_1 src1_sel:DWORD
	v_and_b32_sdwa v13, v6, v208 dst_sel:DWORD dst_unused:UNUSED_PAD src0_sel:WORD_1 src1_sel:DWORD
	v_and_b32_sdwa v8, v11, v208 dst_sel:DWORD dst_unused:UNUSED_PAD src0_sel:WORD_1 src1_sel:DWORD
	v_add3_u32 v9, v7, v9, s57
	v_add3_u32 v13, v6, v13, s57
	v_add3_u32 v8, v11, v8, s57
	v_and_b32_e32 v9, 0xffff0000, v9
	v_and_b32_e32 v13, 0xffff0000, v13
	v_or_b32_sdwa v9, v9, v8 dst_sel:DWORD dst_unused:UNUSED_PAD src0_sel:DWORD src1_sel:WORD_1
	v_or_b32_sdwa v8, v13, v12 dst_sel:DWORD dst_unused:UNUSED_PAD src0_sel:DWORD src1_sel:WORD_1
	ds_read_b128 v[12:15], v134 offset:6144
	global_store_dwordx2 v[94:95], v[8:9], off offset:3072
	s_waitcnt lgkmcnt(0)
	v_fmac_f32_e32 v89, v7, v15
	v_fmac_f32_e32 v89, v11, v14
	v_fmac_f32_e32 v89, v6, v13
	v_fmac_f32_e32 v89, v10, v12
	ds_read_b128 v[12:15], v134 offset:14336
	s_waitcnt lgkmcnt(0)
	v_fmac_f32_e32 v85, v7, v15
	v_fmac_f32_e32 v85, v11, v14
	v_fmac_f32_e32 v85, v6, v13
	v_fmac_f32_e32 v85, v10, v12
	ds_read_b128 v[12:15], v134 offset:22528
	s_waitcnt lgkmcnt(0)
	v_fmac_f32_e32 v81, v7, v15
	v_fmac_f32_e32 v81, v11, v14
	v_fmac_f32_e32 v81, v6, v13
	v_fmac_f32_e32 v81, v10, v12
	ds_read_b128 v[12:15], v134 offset:30720
	s_waitcnt lgkmcnt(0)
	v_fmac_f32_e32 v77, v7, v15
	v_fmac_f32_e32 v77, v11, v14
	v_fmac_f32_e32 v77, v6, v13
	v_fmac_f32_e32 v77, v10, v12
	ds_read_b128 v[12:15], v134 offset:38912
	s_waitcnt lgkmcnt(0)
	v_fmac_f32_e32 v73, v7, v15
	v_fmac_f32_e32 v73, v11, v14
	v_fmac_f32_e32 v73, v6, v13
	v_fmac_f32_e32 v73, v10, v12
	ds_read_b128 v[12:15], v134 offset:47104
	s_waitcnt lgkmcnt(0)
	v_fmac_f32_e32 v69, v7, v15
	v_fmac_f32_e32 v69, v11, v14
	v_fmac_f32_e32 v69, v6, v13
	v_fmac_f32_e32 v69, v10, v12
	ds_read_b128 v[12:15], v134 offset:55296
	s_waitcnt lgkmcnt(0)
	v_fmac_f32_e32 v65, v7, v15
	v_fmac_f32_e32 v65, v11, v14
	v_fmac_f32_e32 v65, v6, v13
	v_fmac_f32_e32 v65, v10, v12
	ds_read_b128 v[12:15], v134 offset:63488
	s_waitcnt lgkmcnt(0)
	v_fmac_f32_e32 v61, v7, v15
	v_fmac_f32_e32 v61, v11, v14
	v_fmac_f32_e32 v61, v6, v13
	v_fmac_f32_e32 v61, v10, v12
	ds_read_b128 v[12:15], v189
	s_waitcnt lgkmcnt(0)
	v_fmac_f32_e32 v57, v7, v15
	v_fmac_f32_e32 v57, v11, v14
	v_fmac_f32_e32 v57, v6, v13
	v_fmac_f32_e32 v57, v10, v12
	ds_read_b128 v[12:15], v191
	s_waitcnt lgkmcnt(0)
	v_fmac_f32_e32 v53, v7, v15
	v_fmac_f32_e32 v53, v11, v14
	v_fmac_f32_e32 v53, v6, v13
	v_fmac_f32_e32 v53, v10, v12
	ds_read_b128 v[12:15], v192
	s_waitcnt lgkmcnt(0)
	v_fmac_f32_e32 v49, v7, v15
	v_fmac_f32_e32 v49, v11, v14
	v_fmac_f32_e32 v49, v6, v13
	v_fmac_f32_e32 v49, v10, v12
	ds_read_b128 v[12:15], v193
	s_waitcnt lgkmcnt(0)
	v_fmac_f32_e32 v45, v7, v15
	v_fmac_f32_e32 v45, v11, v14
	v_fmac_f32_e32 v45, v6, v13
	v_fmac_f32_e32 v45, v10, v12
	ds_read_b128 v[12:15], v194
	s_waitcnt lgkmcnt(0)
	v_fmac_f32_e32 v41, v7, v15
	v_fmac_f32_e32 v41, v11, v14
	v_fmac_f32_e32 v41, v6, v13
	v_fmac_f32_e32 v41, v10, v12
	ds_read_b128 v[12:15], v195
	s_waitcnt lgkmcnt(0)
	v_fmac_f32_e32 v37, v7, v15
	v_fmac_f32_e32 v37, v11, v14
	v_fmac_f32_e32 v37, v6, v13
	v_fmac_f32_e32 v37, v10, v12
	ds_read_b128 v[12:15], v196
	s_waitcnt lgkmcnt(0)
	v_fmac_f32_e32 v33, v7, v15
	v_fmac_f32_e32 v33, v11, v14
	v_fmac_f32_e32 v33, v6, v13
	v_fmac_f32_e32 v33, v10, v12
	ds_read_b128 v[12:15], v197
	s_waitcnt lgkmcnt(0)
	v_fmac_f32_e32 v30, v7, v15
	v_fmac_f32_e32 v30, v11, v14
	v_fmac_f32_e32 v30, v6, v13
	v_fmac_f32_e32 v30, v10, v12
	ds_read_b128 v[8:11], v198
	ds_read_b128 v[12:15], v18 offset:3072
	s_nop 0
	ds_read_b128 v[16:19], v20 offset:3072
	v_mov_b32_e32 v6, v2
	v_mov_b32_e32 v7, v4
	v_pk_mul_f32 v[6:7], v[6:7], v[114:115] op_sel_hi:[1,0]
	s_waitcnt lgkmcnt(0)
	v_mov_b32_e32 v20, v8
	v_mov_b32_e32 v21, v10
	v_pk_mul_f32 v[6:7], v[6:7], v[20:21]
	v_mov_b32_e32 v4, v3
	v_pk_mul_f32 v[2:3], v[4:5], v[114:115] op_sel_hi:[1,0]
	v_mov_b32_e32 v10, v9
	v_pk_mul_f32 v[2:3], v[2:3], v[10:11]
	s_waitcnt lgkmcnt(0)
	v_mov_b32_e32 v22, v12
	v_mov_b32_e32 v20, v16
	v_mov_b32_e32 v21, v18
	v_pk_add_f32 v[20:21], v[20:21], 1.0 op_sel_hi:[1,0]
	v_mov_b32_e32 v23, v14
	v_mov_b32_e32 v18, v17
	v_pk_fma_f32 v[6:7], v[6:7], v[20:21], v[22:23]
	v_pk_add_f32 v[4:5], v[18:19], 1.0 op_sel_hi:[1,0]
	v_mov_b32_e32 v14, v13
	v_pk_fma_f32 v[2:3], v[2:3], v[4:5], v[14:15]
	v_and_b32_sdwa v5, v6, v208 dst_sel:DWORD dst_unused:UNUSED_PAD src0_sel:WORD_1 src1_sel:DWORD
	v_add3_u32 v8, v6, v5, s57
	v_and_b32_sdwa v5, v3, v208 dst_sel:DWORD dst_unused:UNUSED_PAD src0_sel:WORD_1 src1_sel:DWORD
	v_and_b32_sdwa v9, v2, v208 dst_sel:DWORD dst_unused:UNUSED_PAD src0_sel:WORD_1 src1_sel:DWORD
	v_and_b32_sdwa v4, v7, v208 dst_sel:DWORD dst_unused:UNUSED_PAD src0_sel:WORD_1 src1_sel:DWORD
	v_add3_u32 v5, v3, v5, s57
	v_add3_u32 v9, v2, v9, s57
	v_add3_u32 v4, v7, v4, s57
	v_and_b32_e32 v5, 0xffff0000, v5
	v_and_b32_e32 v9, 0xffff0000, v9
	v_or_b32_sdwa v5, v5, v4 dst_sel:DWORD dst_unused:UNUSED_PAD src0_sel:DWORD src1_sel:WORD_1
	v_or_b32_sdwa v4, v9, v8 dst_sel:DWORD dst_unused:UNUSED_PAD src0_sel:DWORD src1_sel:WORD_1
	ds_read_b128 v[8:11], v134 offset:7168
	global_store_dwordx2 v[94:95], v[4:5], off offset:3584
	s_waitcnt lgkmcnt(0)
	v_fmac_f32_e32 v89, v3, v11
	v_fmac_f32_e32 v89, v7, v10
	v_fmac_f32_e32 v89, v2, v9
	v_fmac_f32_e32 v89, v6, v8
	ds_read_b128 v[8:11], v134 offset:15360
	s_waitcnt lgkmcnt(0)
	v_fmac_f32_e32 v85, v3, v11
	v_fmac_f32_e32 v85, v7, v10
	v_fmac_f32_e32 v85, v2, v9
	v_fmac_f32_e32 v85, v6, v8
	ds_read_b128 v[8:11], v134 offset:23552
	s_waitcnt lgkmcnt(0)
	v_fmac_f32_e32 v81, v3, v11
	v_fmac_f32_e32 v81, v7, v10
	v_fmac_f32_e32 v81, v2, v9
	v_fmac_f32_e32 v81, v6, v8
	ds_read_b128 v[8:11], v134 offset:31744
	s_waitcnt lgkmcnt(0)
	v_fmac_f32_e32 v77, v3, v11
	v_fmac_f32_e32 v77, v7, v10
	v_fmac_f32_e32 v77, v2, v9
	v_fmac_f32_e32 v77, v6, v8
	ds_read_b128 v[8:11], v134 offset:39936
	s_waitcnt lgkmcnt(0)
	v_fmac_f32_e32 v73, v3, v11
	v_fmac_f32_e32 v73, v7, v10
	v_fmac_f32_e32 v73, v2, v9
	v_fmac_f32_e32 v73, v6, v8
	ds_read_b128 v[8:11], v134 offset:48128
	s_waitcnt lgkmcnt(0)
	v_fmac_f32_e32 v69, v3, v11
	v_fmac_f32_e32 v69, v7, v10
	v_fmac_f32_e32 v69, v2, v9
	v_fmac_f32_e32 v69, v6, v8
	ds_read_b128 v[8:11], v134 offset:56320
	s_waitcnt lgkmcnt(0)
	v_fmac_f32_e32 v65, v3, v11
	v_fmac_f32_e32 v65, v7, v10
	v_fmac_f32_e32 v65, v2, v9
	v_fmac_f32_e32 v65, v6, v8
	ds_read_b128 v[8:11], v134 offset:64512
	s_waitcnt lgkmcnt(0)
	v_fmac_f32_e32 v61, v3, v11
	v_fmac_f32_e32 v61, v7, v10
	v_fmac_f32_e32 v61, v2, v9
	v_fmac_f32_e32 v61, v6, v8
	ds_read_b128 v[8:11], v199
	s_waitcnt lgkmcnt(0)
	v_fmac_f32_e32 v57, v3, v11
	v_fmac_f32_e32 v57, v7, v10
	v_fmac_f32_e32 v57, v2, v9
	v_fmac_f32_e32 v57, v6, v8
	ds_read_b128 v[8:11], v200
	s_waitcnt lgkmcnt(0)
	v_fmac_f32_e32 v53, v3, v11
	v_fmac_f32_e32 v53, v7, v10
	v_fmac_f32_e32 v53, v2, v9
	v_fmac_f32_e32 v53, v6, v8
	ds_read_b128 v[8:11], v201
	s_waitcnt lgkmcnt(0)
	v_fmac_f32_e32 v49, v3, v11
	v_fmac_f32_e32 v49, v7, v10
	v_fmac_f32_e32 v49, v2, v9
	v_fmac_f32_e32 v49, v6, v8
	ds_read_b128 v[8:11], v202
	s_waitcnt lgkmcnt(0)
	v_fmac_f32_e32 v45, v3, v11
	v_fmac_f32_e32 v45, v7, v10
	v_fmac_f32_e32 v45, v2, v9
	v_fmac_f32_e32 v45, v6, v8
	ds_read_b128 v[8:11], v203
	s_waitcnt lgkmcnt(0)
	v_fmac_f32_e32 v41, v3, v11
	v_fmac_f32_e32 v41, v7, v10
	v_fmac_f32_e32 v41, v2, v9
	v_fmac_f32_e32 v41, v6, v8
	ds_read_b128 v[8:11], v204
	s_waitcnt lgkmcnt(0)
	v_fmac_f32_e32 v37, v3, v11
	v_fmac_f32_e32 v37, v7, v10
	v_fmac_f32_e32 v37, v2, v9
	v_fmac_f32_e32 v37, v6, v8
	ds_read_b128 v[8:11], v205
	s_waitcnt lgkmcnt(0)
	v_fmac_f32_e32 v33, v3, v11
	v_fmac_f32_e32 v33, v7, v10
	v_fmac_f32_e32 v33, v2, v9
	v_fmac_f32_e32 v33, v6, v8
	ds_read_b128 v[8:11], v206
	s_waitcnt lgkmcnt(0)
	v_fmac_f32_e32 v30, v3, v11
	v_fmac_f32_e32 v30, v7, v10
	v_fmac_f32_e32 v30, v2, v9
	v_fmac_f32_e32 v30, v6, v8
	ds_bpermute_b32 v6, v1, v81
	ds_bpermute_b32 v7, v1, v77
	ds_bpermute_b32 v22, v1, v49
	ds_bpermute_b32 v10, v1, v73
	ds_bpermute_b32 v24, v1, v41
	s_waitcnt lgkmcnt(4)
	v_add_f32_e32 v6, v81, v6
	ds_bpermute_b32 v8, v128, v6
	s_waitcnt lgkmcnt(4)
	v_add_f32_e32 v7, v77, v7
	ds_bpermute_b32 v9, v128, v7
	s_waitcnt lgkmcnt(4)
	v_add_f32_e32 v22, v49, v22
	ds_bpermute_b32 v23, v128, v22
	s_waitcnt lgkmcnt(2)
	v_add_f32_e32 v6, v6, v8
	ds_bpermute_b32 v8, v129, v6
	s_waitcnt lgkmcnt(2)
	v_add_f32_e32 v7, v7, v9
	ds_bpermute_b32 v9, v129, v7
	s_waitcnt lgkmcnt(2)
	v_add_f32_e32 v22, v22, v23
	ds_bpermute_b32 v23, v129, v22
	s_waitcnt lgkmcnt(2)
	v_add_f32_e32 v6, v6, v8
	ds_bpermute_b32 v8, v130, v6
	s_waitcnt lgkmcnt(2)
	v_add_f32_e32 v7, v7, v9
	ds_bpermute_b32 v9, v130, v7
	v_add_f32_e32 v10, v73, v10
	s_waitcnt lgkmcnt(2)
	v_add_f32_e32 v22, v22, v23
	s_waitcnt lgkmcnt(1)
	v_add_f32_e32 v6, v6, v8
	ds_bpermute_b32 v8, v131, v6
	s_waitcnt lgkmcnt(1)
	v_add_f32_e32 v9, v7, v9
	ds_bpermute_b32 v12, v131, v9
	v_add_f32_e32 v23, v41, v24
	ds_bpermute_b32 v11, v128, v10
	s_waitcnt lgkmcnt(2)
	v_add_f32_e32 v6, v6, v8
	ds_bpermute_b32 v8, v1, v69
	ds_bpermute_b32 v24, v128, v23
	ds_bpermute_b32 v27, v130, v22
	s_waitcnt lgkmcnt(3)
	v_add_f32_e32 v10, v10, v11
	ds_bpermute_b32 v11, v129, v10
	s_waitcnt lgkmcnt(3)
	v_add_f32_e32 v13, v69, v8
	ds_bpermute_b32 v14, v128, v13
	v_add_f32_e32 v8, v9, v12
	s_waitcnt lgkmcnt(3)
	v_add_f32_e32 v23, v23, v24
	ds_bpermute_b32 v24, v129, v23
	s_waitcnt lgkmcnt(2)
	v_add_f32_e32 v10, v10, v11
	s_waitcnt lgkmcnt(1)
	v_add_f32_e32 v12, v13, v14
	ds_bpermute_b32 v14, v1, v65
	v_add_f32_e32 v22, v22, v27
	s_waitcnt lgkmcnt(1)
	v_add_f32_e32 v23, v23, v24
	ds_bpermute_b32 v11, v130, v10
	ds_bpermute_b32 v27, v131, v22
	s_waitcnt lgkmcnt(2)
	v_add_f32_e32 v14, v65, v14
	ds_bpermute_b32 v15, v128, v14
	ds_bpermute_b32 v24, v130, v23
	s_waitcnt lgkmcnt(3)
	v_add_f32_e32 v10, v10, v11
	s_waitcnt lgkmcnt(2)
	v_add_f32_e32 v22, v22, v27
	ds_bpermute_b32 v11, v131, v10
	s_waitcnt lgkmcnt(2)
	v_add_f32_e32 v14, v14, v15
	ds_bpermute_b32 v15, v129, v14
	s_waitcnt lgkmcnt(2)
	v_add_f32_e32 v27, v23, v24
	ds_bpermute_b32 v28, v131, v27
	ds_bpermute_b32 v2, v1, v89
	ds_bpermute_b32 v3, v1, v85
	s_waitcnt lgkmcnt(3)
	v_add_f32_e32 v14, v14, v15
	ds_bpermute_b32 v15, v130, v14
	v_add_f32_e32 v10, v10, v11
	ds_bpermute_b32 v11, v1, v61
	ds_bpermute_b32 v18, v1, v57
	ds_bpermute_b32 v29, v1, v37
	s_waitcnt lgkmcnt(3)
	v_add_f32_e32 v14, v14, v15
	ds_bpermute_b32 v15, v131, v14
	ds_bpermute_b32 v31, v1, v30
	v_add_f32_e32 v2, v89, v2
	v_add_f32_e32 v3, v85, v3
	s_waitcnt lgkmcnt(4)
	v_add_f32_e32 v16, v61, v11
	s_waitcnt lgkmcnt(1)
	v_add_f32_e32 v14, v14, v15
	ds_bpermute_b32 v15, v1, v53
	v_add_f32_e32 v18, v57, v18
	v_add_f32_e32 v29, v37, v29
	s_waitcnt lgkmcnt(1)
	v_add_f32_e32 v30, v30, v31
	ds_bpermute_b32 v4, v128, v2
	s_waitcnt lgkmcnt(1)
	v_add_f32_e32 v20, v53, v15
	ds_bpermute_b32 v21, v128, v20
	ds_bpermute_b32 v5, v128, v3
	ds_bpermute_b32 v17, v128, v16
	ds_bpermute_b32 v19, v128, v18
	ds_bpermute_b32 v32, v128, v29
	s_waitcnt lgkmcnt(4)
	v_add_f32_e32 v20, v20, v21
	ds_bpermute_b32 v21, v129, v20
	ds_bpermute_b32 v31, v128, v30
	v_add_f32_e32 v2, v2, v4
	s_waitcnt lgkmcnt(5)
	v_add_f32_e32 v3, v3, v5
	s_waitcnt lgkmcnt(4)
	v_add_f32_e32 v16, v16, v17
	s_waitcnt lgkmcnt(1)
	v_add_f32_e32 v20, v20, v21
	ds_bpermute_b32 v21, v130, v20
	v_add_f32_e32 v18, v18, v19
	v_add_f32_e32 v29, v29, v32
	s_waitcnt lgkmcnt(1)
	v_add_f32_e32 v30, v30, v31
	ds_bpermute_b32 v4, v129, v2
	s_waitcnt lgkmcnt(1)
	v_add_f32_e32 v20, v20, v21
	ds_bpermute_b32 v21, v1, v45
	ds_bpermute_b32 v25, v131, v20
	ds_bpermute_b32 v5, v129, v3
	ds_bpermute_b32 v13, v129, v12
	ds_bpermute_b32 v17, v129, v16
	s_waitcnt lgkmcnt(4)
	v_add_f32_e32 v21, v45, v21
	ds_bpermute_b32 v26, v128, v21
	s_waitcnt lgkmcnt(4)
	v_add_f32_e32 v20, v20, v25
	ds_bpermute_b32 v19, v129, v18
	ds_bpermute_b32 v32, v129, v29
	ds_bpermute_b32 v31, v129, v30
	s_waitcnt lgkmcnt(3)
	v_add_f32_e32 v21, v21, v26
	ds_bpermute_b32 v26, v129, v21
	v_add_f32_e32 v2, v2, v4
	v_add_f32_e32 v3, v3, v5
	v_add_f32_e32 v12, v12, v13
	v_add_f32_e32 v16, v16, v17
	s_waitcnt lgkmcnt(0)
	v_add_f32_e32 v25, v21, v26
	ds_bpermute_b32 v26, v130, v25
	v_add_f32_e32 v18, v18, v19
	v_add_f32_e32 v29, v29, v32
	v_add_f32_e32 v30, v30, v31
	ds_bpermute_b32 v4, v130, v2
	s_waitcnt lgkmcnt(1)
	v_add_f32_e32 v25, v25, v26
	ds_bpermute_b32 v26, v131, v25
	ds_bpermute_b32 v5, v130, v3
	ds_bpermute_b32 v13, v130, v12
	ds_bpermute_b32 v17, v130, v16
	ds_bpermute_b32 v19, v130, v18
	s_waitcnt lgkmcnt(4)
	v_add_f32_e32 v24, v25, v26
	v_add_f32_e32 v26, v27, v28
	ds_bpermute_b32 v28, v1, v33
	ds_bpermute_b32 v32, v130, v29
	ds_bpermute_b32 v31, v130, v30
	v_add_f32_e32 v2, v2, v4
	s_waitcnt lgkmcnt(6)
	v_add_f32_e32 v3, v3, v5
	s_waitcnt lgkmcnt(2)
	v_add_f32_e32 v28, v33, v28
	ds_bpermute_b32 v33, v128, v28
	v_add_f32_e32 v12, v12, v13
	v_add_f32_e32 v16, v16, v17
	v_add_f32_e32 v18, v18, v19
	s_waitcnt lgkmcnt(2)
	v_add_f32_e32 v29, v29, v32
	s_waitcnt lgkmcnt(0)
	v_add_f32_e32 v28, v28, v33
	ds_bpermute_b32 v33, v129, v28
	v_add_f32_e32 v35, v30, v31
	ds_bpermute_b32 v4, v131, v2
	ds_bpermute_b32 v5, v131, v3
	ds_bpermute_b32 v13, v131, v12
	s_waitcnt lgkmcnt(3)
	v_add_f32_e32 v28, v28, v33
	ds_bpermute_b32 v33, v130, v28
	ds_bpermute_b32 v17, v131, v16
	ds_bpermute_b32 v19, v131, v18
	ds_bpermute_b32 v32, v131, v29
	ds_bpermute_b32 v36, v131, v35
	s_waitcnt lgkmcnt(4)
	v_add_f32_e32 v33, v28, v33
	ds_bpermute_b32 v34, v131, v33
	v_add_f32_e32 v2, v2, v4
	v_add_f32_e32 v3, v3, v5
	v_add_f32_e32 v12, v12, v13
	s_waitcnt lgkmcnt(4)
	v_add_f32_e32 v16, v16, v17
	s_waitcnt lgkmcnt(3)
	v_add_f32_e32 v18, v18, v19
	s_waitcnt lgkmcnt(2)
	v_add_f32_e32 v28, v29, v32
	s_waitcnt lgkmcnt(0)
	v_add_f32_e32 v29, v33, v34
	v_add_f32_e32 v32, v35, v36
	ds_bpermute_b32 v4, v132, v2
	ds_bpermute_b32 v5, v132, v3
	ds_bpermute_b32 v7, v132, v6
	ds_bpermute_b32 v9, v132, v8
	ds_bpermute_b32 v11, v132, v10
	ds_bpermute_b32 v13, v132, v12
	ds_bpermute_b32 v15, v132, v14
	ds_bpermute_b32 v17, v132, v16
	ds_bpermute_b32 v19, v132, v18
	ds_bpermute_b32 v21, v132, v20
	ds_bpermute_b32 v23, v132, v22
	ds_bpermute_b32 v25, v132, v24
	ds_bpermute_b32 v27, v132, v26
	ds_bpermute_b32 v30, v132, v28
	ds_bpermute_b32 v31, v132, v29
	ds_bpermute_b32 v33, v132, v32
	s_and_saveexec_b64 s[52:53], s[2:3]
	s_cbranch_execz .LBB0_1364
	s_waitcnt lgkmcnt(14)
	v_add_f32_e32 v2, v2, v4
	v_add_f32_e32 v3, v3, v5
	s_mov_b32 s61, 0xff61b1e6
	v_max3_f32 v4, v2, s61, v3
	s_waitcnt lgkmcnt(13)
	v_add_f32_e32 v5, v6, v7
	s_waitcnt lgkmcnt(12)
	v_add_f32_e32 v6, v8, v9
	v_max3_f32 v4, v4, v5, v6
	s_waitcnt lgkmcnt(11)
	v_add_f32_e32 v7, v10, v11
	s_waitcnt lgkmcnt(10)
	v_add_f32_e32 v8, v12, v13
	v_max3_f32 v4, v4, v7, v8
	s_waitcnt lgkmcnt(9)
	v_add_f32_e32 v11, v14, v15
	s_waitcnt lgkmcnt(8)
	v_add_f32_e32 v15, v16, v17
	v_max3_f32 v4, v4, v11, v15
	s_waitcnt lgkmcnt(7)
	v_add_f32_e32 v16, v18, v19
	s_waitcnt lgkmcnt(6)
	v_add_f32_e32 v17, v20, v21
	v_max3_f32 v4, v4, v16, v17
	s_waitcnt lgkmcnt(5)
	v_add_f32_e32 v18, v22, v23
	s_waitcnt lgkmcnt(4)
	v_add_f32_e32 v19, v24, v25
	v_max3_f32 v4, v4, v18, v19
	s_waitcnt lgkmcnt(3)
	v_add_f32_e32 v14, v26, v27
	s_waitcnt lgkmcnt(2)
	v_add_f32_e32 v13, v28, v30
	s_waitcnt lgkmcnt(0)
	v_add_f32_e32 v32, v32, v33
	v_max3_f32 v4, v4, v14, v13
	v_add_f32_e32 v10, v29, v31
	v_max3_f32 v12, v4, v10, v32
	v_sub_f32_e32 v4, v32, v12
	v_mul_f32_e32 v9, 0x3fb8aa3b, v4
	v_fma_f32 v20, v4, s58, -v9
	v_rndne_f32_e32 v21, v9
	v_fmac_f32_e32 v20, 0x32a5705f, v4
	v_sub_f32_e32 v9, v9, v21
	v_add_f32_e32 v9, v9, v20
	v_exp_f32_e32 v9, v9
	v_cvt_i32_f32_e32 v20, v21
	v_cmp_ngt_f32_e32 vcc, s59, v4
	v_sub_f32_e32 v2, v2, v12
	v_sub_f32_e32 v3, v3, v12
	v_ldexp_f32 v9, v9, v20
	v_cndmask_b32_e32 v9, 0, v9, vcc
	v_cmp_nlt_f32_e32 vcc, s60, v4
	v_mul_f32_e32 v4, 0x3fb8aa3b, v2
	v_fma_f32 v20, v2, s58, -v4
	v_rndne_f32_e32 v21, v4
	v_fmac_f32_e32 v20, 0x32a5705f, v2
	v_sub_f32_e32 v4, v4, v21
	v_add_f32_e32 v4, v4, v20
	v_exp_f32_e32 v4, v4
	v_cvt_i32_f32_e32 v20, v21
	v_cndmask_b32_e32 v9, v209, v9, vcc
	v_cmp_ngt_f32_e32 vcc, s59, v2
	v_sub_f32_e32 v17, v17, v12
	v_ldexp_f32 v4, v4, v20
	v_cndmask_b32_e32 v4, 0, v4, vcc
	v_cmp_nlt_f32_e32 vcc, s60, v2
	v_sub_f32_e32 v18, v18, v12
	v_sub_f32_e32 v19, v19, v12
	v_cndmask_b32_e32 v2, v209, v4, vcc
	v_mul_f32_e32 v4, 0x3fb8aa3b, v3
	v_fma_f32 v20, v3, s58, -v4
	v_rndne_f32_e32 v21, v4
	v_fmac_f32_e32 v20, 0x32a5705f, v3
	v_sub_f32_e32 v4, v4, v21
	v_add_f32_e32 v4, v4, v20
	v_exp_f32_e32 v4, v4
	v_cvt_i32_f32_e32 v20, v21
	v_cmp_ngt_f32_e32 vcc, s59, v3
	v_sub_f32_e32 v14, v14, v12
	v_sub_f32_e32 v13, v13, v12
	v_ldexp_f32 v4, v4, v20
	v_cndmask_b32_e32 v4, 0, v4, vcc
	v_cmp_nlt_f32_e32 vcc, s60, v3
	v_sub_f32_e32 v10, v10, v12
	s_nop 0
	v_cndmask_b32_e32 v3, v209, v4, vcc
	v_sub_f32_e32 v4, v5, v12
	v_mul_f32_e32 v5, 0x3fb8aa3b, v4
	v_fma_f32 v21, v4, s58, -v5
	v_rndne_f32_e32 v22, v5
	v_fmac_f32_e32 v21, 0x32a5705f, v4
	v_sub_f32_e32 v5, v5, v22
	v_add_f32_e32 v5, v5, v21
	v_exp_f32_e32 v5, v5
	v_cvt_i32_f32_e32 v21, v22
	v_cmp_ngt_f32_e32 vcc, s59, v4
	v_add_f32_e32 v20, v2, v3
	v_ldexp_f32 v5, v5, v21
	v_cndmask_b32_e32 v5, 0, v5, vcc
	v_cmp_nlt_f32_e32 vcc, s60, v4
	s_nop 1
	v_cndmask_b32_e32 v4, v209, v5, vcc
	v_sub_f32_e32 v5, v6, v12
	v_mul_f32_e32 v6, 0x3fb8aa3b, v5
	v_fma_f32 v21, v5, s58, -v6
	v_rndne_f32_e32 v22, v6
	v_fmac_f32_e32 v21, 0x32a5705f, v5
	v_sub_f32_e32 v6, v6, v22
	v_add_f32_e32 v6, v6, v21
	v_exp_f32_e32 v6, v6
	v_cvt_i32_f32_e32 v21, v22
	v_cmp_ngt_f32_e32 vcc, s59, v5
	v_add_f32_e32 v20, v4, v20
	v_ldexp_f32 v6, v6, v21
	v_cndmask_b32_e32 v6, 0, v6, vcc
	v_cmp_nlt_f32_e32 vcc, s60, v5
	s_nop 1
	v_cndmask_b32_e32 v5, v209, v6, vcc
	v_sub_f32_e32 v6, v7, v12
	v_mul_f32_e32 v7, 0x3fb8aa3b, v6
	v_fma_f32 v21, v6, s58, -v7
	v_rndne_f32_e32 v22, v7
	v_fmac_f32_e32 v21, 0x32a5705f, v6
	v_sub_f32_e32 v7, v7, v22
	v_add_f32_e32 v7, v7, v21
	v_exp_f32_e32 v7, v7
	v_cvt_i32_f32_e32 v21, v22
	v_cmp_ngt_f32_e32 vcc, s59, v6
	v_add_f32_e32 v20, v5, v20
	v_ldexp_f32 v7, v7, v21
	v_cndmask_b32_e32 v7, 0, v7, vcc
	v_cmp_nlt_f32_e32 vcc, s60, v6
	s_nop 1
	v_cndmask_b32_e32 v6, v209, v7, vcc
	v_sub_f32_e32 v7, v8, v12
	v_mul_f32_e32 v8, 0x3fb8aa3b, v7
	v_fma_f32 v21, v7, s58, -v8
	v_rndne_f32_e32 v22, v8
	v_fmac_f32_e32 v21, 0x32a5705f, v7
	v_sub_f32_e32 v8, v8, v22
	v_add_f32_e32 v8, v8, v21
	v_exp_f32_e32 v8, v8
	v_cvt_i32_f32_e32 v21, v22
	v_cmp_ngt_f32_e32 vcc, s59, v7
	v_add_f32_e32 v20, v6, v20
	v_ldexp_f32 v8, v8, v21
	v_cndmask_b32_e32 v8, 0, v8, vcc
	v_cmp_nlt_f32_e32 vcc, s60, v7
	s_nop 1
	v_cndmask_b32_e32 v7, v209, v8, vcc
	v_sub_f32_e32 v8, v11, v12
	v_mul_f32_e32 v11, 0x3fb8aa3b, v8
	v_fma_f32 v21, v8, s58, -v11
	v_rndne_f32_e32 v22, v11
	v_fmac_f32_e32 v21, 0x32a5705f, v8
	v_sub_f32_e32 v11, v11, v22
	v_add_f32_e32 v11, v11, v21
	v_exp_f32_e32 v11, v11
	v_cvt_i32_f32_e32 v21, v22
	v_cmp_ngt_f32_e32 vcc, s59, v8
	v_add_f32_e32 v20, v7, v20
	v_ldexp_f32 v11, v11, v21
	v_cndmask_b32_e32 v11, 0, v11, vcc
	v_cmp_nlt_f32_e32 vcc, s60, v8
	s_nop 1
	v_cndmask_b32_e32 v8, v209, v11, vcc
	v_sub_f32_e32 v11, v15, v12
	v_mul_f32_e32 v15, 0x3fb8aa3b, v11
	v_fma_f32 v21, v11, s58, -v15
	v_rndne_f32_e32 v22, v15
	v_fmac_f32_e32 v21, 0x32a5705f, v11
	v_sub_f32_e32 v15, v15, v22
	v_add_f32_e32 v15, v15, v21
	v_exp_f32_e32 v15, v15
	v_cvt_i32_f32_e32 v21, v22
	v_cmp_ngt_f32_e32 vcc, s59, v11
	v_add_f32_e32 v20, v8, v20
	v_ldexp_f32 v15, v15, v21
	v_cndmask_b32_e32 v15, 0, v15, vcc
	v_cmp_nlt_f32_e32 vcc, s60, v11
	s_nop 1
	v_cndmask_b32_e32 v11, v209, v15, vcc
	v_sub_f32_e32 v15, v16, v12
	v_mul_f32_e32 v16, 0x3fb8aa3b, v15
	v_fma_f32 v21, v15, s58, -v16
	v_rndne_f32_e32 v22, v16
	v_fmac_f32_e32 v21, 0x32a5705f, v15
	v_sub_f32_e32 v16, v16, v22
	v_add_f32_e32 v16, v16, v21
	v_exp_f32_e32 v16, v16
	v_cvt_i32_f32_e32 v21, v22
	v_cmp_ngt_f32_e32 vcc, s59, v15
	v_add_f32_e32 v20, v11, v20
	v_mul_f32_e32 v12, 0x3fb8aa3b, v10
	v_ldexp_f32 v16, v16, v21
	v_cndmask_b32_e32 v16, 0, v16, vcc
	v_cmp_nlt_f32_e32 vcc, s60, v15
	s_nop 1
	v_cndmask_b32_e32 v15, v209, v16, vcc
	v_add_f32_e32 v16, v15, v20
	v_mul_f32_e32 v20, 0x3fb8aa3b, v17
	v_fma_f32 v21, v17, s58, -v20
	v_rndne_f32_e32 v22, v20
	v_fmac_f32_e32 v21, 0x32a5705f, v17
	v_sub_f32_e32 v20, v20, v22
	v_add_f32_e32 v20, v20, v21
	v_exp_f32_e32 v20, v20
	v_cvt_i32_f32_e32 v21, v22
	v_cmp_ngt_f32_e32 vcc, s59, v17
	v_ldexp_f32 v20, v20, v21
	s_nop 0
	v_cndmask_b32_e32 v20, 0, v20, vcc
	v_cmp_nlt_f32_e32 vcc, s60, v17
	s_nop 1
	v_cndmask_b32_e32 v17, v209, v20, vcc
	v_mul_f32_e32 v20, 0x3fb8aa3b, v18
	v_fma_f32 v21, v18, s58, -v20
	v_rndne_f32_e32 v22, v20
	v_fmac_f32_e32 v21, 0x32a5705f, v18
	v_sub_f32_e32 v20, v20, v22
	v_add_f32_e32 v20, v20, v21
	v_exp_f32_e32 v20, v20
	v_cvt_i32_f32_e32 v21, v22
	v_cmp_ngt_f32_e32 vcc, s59, v18
	v_add_f32_e32 v16, v17, v16
	v_ldexp_f32 v20, v20, v21
	v_cndmask_b32_e32 v20, 0, v20, vcc
	v_cmp_nlt_f32_e32 vcc, s60, v18
	s_nop 1
	v_cndmask_b32_e32 v18, v209, v20, vcc
	v_mul_f32_e32 v20, 0x3fb8aa3b, v19
	v_fma_f32 v21, v19, s58, -v20
	v_rndne_f32_e32 v22, v20
	v_fmac_f32_e32 v21, 0x32a5705f, v19
	v_sub_f32_e32 v20, v20, v22
	v_add_f32_e32 v20, v20, v21
	v_exp_f32_e32 v20, v20
	v_cvt_i32_f32_e32 v21, v22
	v_cmp_ngt_f32_e32 vcc, s59, v19
	v_add_f32_e32 v16, v18, v16
	v_ldexp_f32 v20, v20, v21
	v_cndmask_b32_e32 v20, 0, v20, vcc
	v_cmp_nlt_f32_e32 vcc, s60, v19
	s_nop 1
	v_cndmask_b32_e32 v19, v209, v20, vcc
	v_mul_f32_e32 v20, 0x3fb8aa3b, v14
	v_fma_f32 v21, v14, s58, -v20
	v_rndne_f32_e32 v22, v20
	v_fmac_f32_e32 v21, 0x32a5705f, v14
	v_sub_f32_e32 v20, v20, v22
	v_add_f32_e32 v20, v20, v21
	v_exp_f32_e32 v20, v20
	v_cvt_i32_f32_e32 v21, v22
	v_cmp_ngt_f32_e32 vcc, s59, v14
	v_add_f32_e32 v16, v19, v16
	v_ldexp_f32 v20, v20, v21
	v_cndmask_b32_e32 v20, 0, v20, vcc
	v_cmp_nlt_f32_e32 vcc, s60, v14
	s_nop 1
	v_cndmask_b32_e32 v14, v209, v20, vcc
	v_mul_f32_e32 v20, 0x3fb8aa3b, v13
	v_fma_f32 v21, v13, s58, -v20
	v_rndne_f32_e32 v22, v20
	v_fmac_f32_e32 v21, 0x32a5705f, v13
	v_sub_f32_e32 v20, v20, v22
	v_add_f32_e32 v20, v20, v21
	v_exp_f32_e32 v20, v20
	v_cvt_i32_f32_e32 v21, v22
	v_cmp_ngt_f32_e32 vcc, s59, v13
	v_add_f32_e32 v16, v14, v16
	v_ldexp_f32 v20, v20, v21
	v_cndmask_b32_e32 v20, 0, v20, vcc
	v_cmp_nlt_f32_e32 vcc, s60, v13
	v_rndne_f32_e32 v21, v12
	s_nop 0
	v_cndmask_b32_e32 v13, v209, v20, vcc
	v_fma_f32 v20, v10, s58, -v12
	v_fmac_f32_e32 v20, 0x32a5705f, v10
	v_sub_f32_e32 v12, v12, v21
	v_add_f32_e32 v12, v12, v20
	v_exp_f32_e32 v12, v12
	v_cvt_i32_f32_e32 v20, v21
	v_cmp_ngt_f32_e32 vcc, s59, v10
	v_add_f32_e32 v16, v13, v16
	v_ldexp_f32 v12, v12, v20
	v_cndmask_b32_e32 v12, 0, v12, vcc
	v_cmp_nlt_f32_e32 vcc, s60, v10
	s_nop 1
	v_cndmask_b32_e32 v12, v209, v12, vcc
	v_add_f32_e32 v10, v12, v16
	v_add_f32_e32 v10, v9, v10
	v_div_scale_f32 v16, s[62:63], v10, v10, v9
	v_rcp_f32_e32 v20, v16
	s_nop 0
	v_fma_f32 v21, -v16, v20, 1.0
	v_fmac_f32_e32 v20, v21, v20
	v_div_scale_f32 v21, vcc, v9, v10, v9
	v_mul_f32_e32 v22, v21, v20
	v_fma_f32 v23, -v16, v22, v21
	v_fmac_f32_e32 v22, v23, v20
	v_fma_f32 v16, -v16, v22, v21
	v_div_fmas_f32 v16, v16, v20, v22
	v_div_fixup_f32 v9, v16, v10, v9
	v_div_scale_f32 v16, s[62:63], v10, v10, v12
	v_rcp_f32_e32 v20, v16
	s_nop 0
	v_fma_f32 v21, -v16, v20, 1.0
	v_fmac_f32_e32 v20, v21, v20
	v_div_scale_f32 v21, vcc, v12, v10, v12
	v_mul_f32_e32 v22, v21, v20
	v_fma_f32 v23, -v16, v22, v21
	v_fmac_f32_e32 v22, v23, v20
	v_fma_f32 v16, -v16, v22, v21
	v_div_fmas_f32 v16, v16, v20, v22
	v_div_fixup_f32 v12, v16, v10, v12
	v_div_scale_f32 v16, s[62:63], v10, v10, v13
	v_rcp_f32_e32 v20, v16
	s_nop 0
	v_fma_f32 v21, -v16, v20, 1.0
	v_fmac_f32_e32 v20, v21, v20
	v_div_scale_f32 v21, vcc, v13, v10, v13
	v_mul_f32_e32 v22, v21, v20
	v_fma_f32 v23, -v16, v22, v21
	v_fmac_f32_e32 v22, v23, v20
	v_fma_f32 v16, -v16, v22, v21
	v_div_fmas_f32 v16, v16, v20, v22
	v_div_fixup_f32 v13, v16, v10, v13
	v_div_scale_f32 v16, s[62:63], v10, v10, v14
	v_rcp_f32_e32 v20, v16
	s_nop 0
	v_fma_f32 v21, -v16, v20, 1.0
	v_fmac_f32_e32 v20, v21, v20
	v_div_scale_f32 v21, vcc, v14, v10, v14
	v_mul_f32_e32 v22, v21, v20
	v_fma_f32 v23, -v16, v22, v21
	v_fmac_f32_e32 v22, v23, v20
	v_fma_f32 v16, -v16, v22, v21
	v_div_fmas_f32 v16, v16, v20, v22
	v_div_fixup_f32 v14, v16, v10, v14
	v_div_scale_f32 v16, s[62:63], v10, v10, v19
	v_rcp_f32_e32 v20, v16
	s_nop 0
	v_fma_f32 v21, -v16, v20, 1.0
	v_fmac_f32_e32 v20, v21, v20
	v_div_scale_f32 v21, vcc, v19, v10, v19
	v_mul_f32_e32 v22, v21, v20
	v_fma_f32 v23, -v16, v22, v21
	v_fmac_f32_e32 v22, v23, v20
	v_fma_f32 v16, -v16, v22, v21
	v_div_fmas_f32 v16, v16, v20, v22
	v_div_fixup_f32 v16, v16, v10, v19
	v_div_scale_f32 v19, s[62:63], v10, v10, v18
	v_rcp_f32_e32 v20, v19
	s_nop 0
	v_fma_f32 v21, -v19, v20, 1.0
	v_fmac_f32_e32 v20, v21, v20
	v_div_scale_f32 v21, vcc, v18, v10, v18
	v_mul_f32_e32 v22, v21, v20
	v_fma_f32 v23, -v19, v22, v21
	v_fmac_f32_e32 v22, v23, v20
	v_fma_f32 v19, -v19, v22, v21
	v_div_fmas_f32 v19, v19, v20, v22
	v_div_fixup_f32 v18, v19, v10, v18
	v_div_scale_f32 v19, s[62:63], v10, v10, v17
	v_rcp_f32_e32 v20, v19
	s_nop 0
	v_fma_f32 v21, -v19, v20, 1.0
	v_fmac_f32_e32 v20, v21, v20
	v_div_scale_f32 v21, vcc, v17, v10, v17
	v_mul_f32_e32 v22, v21, v20
	v_fma_f32 v23, -v19, v22, v21
	v_fmac_f32_e32 v22, v23, v20
	v_fma_f32 v19, -v19, v22, v21
	v_div_fmas_f32 v19, v19, v20, v22
	v_div_fixup_f32 v17, v19, v10, v17
	v_div_scale_f32 v19, s[62:63], v10, v10, v15
	v_rcp_f32_e32 v20, v19
	s_nop 0
	v_fma_f32 v21, -v19, v20, 1.0
	v_fmac_f32_e32 v20, v21, v20
	v_div_scale_f32 v21, vcc, v15, v10, v15
	v_mul_f32_e32 v22, v21, v20
	v_fma_f32 v23, -v19, v22, v21
	v_fmac_f32_e32 v22, v23, v20
	v_fma_f32 v19, -v19, v22, v21
	v_div_fmas_f32 v19, v19, v20, v22
	v_div_fixup_f32 v15, v19, v10, v15
	v_div_scale_f32 v19, s[62:63], v10, v10, v11
	v_rcp_f32_e32 v20, v19
	s_nop 0
	v_fma_f32 v21, -v19, v20, 1.0
	v_fmac_f32_e32 v20, v21, v20
	v_div_scale_f32 v21, vcc, v11, v10, v11
	v_mul_f32_e32 v22, v21, v20
	v_fma_f32 v23, -v19, v22, v21
	v_fmac_f32_e32 v22, v23, v20
	v_fma_f32 v19, -v19, v22, v21
	v_div_fmas_f32 v19, v19, v20, v22
	v_div_fixup_f32 v11, v19, v10, v11
	v_div_scale_f32 v19, s[62:63], v10, v10, v8
	v_rcp_f32_e32 v20, v19
	s_nop 0
	v_fma_f32 v21, -v19, v20, 1.0
	v_fmac_f32_e32 v20, v21, v20
	v_div_scale_f32 v21, vcc, v8, v10, v8
	v_mul_f32_e32 v22, v21, v20
	v_fma_f32 v23, -v19, v22, v21
	v_fmac_f32_e32 v22, v23, v20
	v_fma_f32 v19, -v19, v22, v21
	v_div_fmas_f32 v19, v19, v20, v22
	v_div_fixup_f32 v8, v19, v10, v8
	v_div_scale_f32 v19, s[62:63], v10, v10, v7
	v_rcp_f32_e32 v20, v19
	s_nop 0
	v_fma_f32 v21, -v19, v20, 1.0
	v_fmac_f32_e32 v20, v21, v20
	v_div_scale_f32 v21, vcc, v7, v10, v7
	v_mul_f32_e32 v22, v21, v20
	v_fma_f32 v23, -v19, v22, v21
	v_fmac_f32_e32 v22, v23, v20
	v_fma_f32 v19, -v19, v22, v21
	v_div_fmas_f32 v19, v19, v20, v22
	v_div_fixup_f32 v7, v19, v10, v7
	v_div_scale_f32 v19, s[62:63], v10, v10, v6
	v_rcp_f32_e32 v20, v19
	s_nop 0
	v_fma_f32 v21, -v19, v20, 1.0
	v_fmac_f32_e32 v20, v21, v20
	v_div_scale_f32 v21, vcc, v6, v10, v6
	v_mul_f32_e32 v22, v21, v20
	v_fma_f32 v23, -v19, v22, v21
	v_fmac_f32_e32 v22, v23, v20
	v_fma_f32 v19, -v19, v22, v21
	v_div_fmas_f32 v19, v19, v20, v22
	v_div_fixup_f32 v6, v19, v10, v6
	v_div_scale_f32 v19, s[62:63], v10, v10, v5
	v_rcp_f32_e32 v20, v19
	s_nop 0
	v_fma_f32 v21, -v19, v20, 1.0
	v_fmac_f32_e32 v20, v21, v20
	v_div_scale_f32 v21, vcc, v5, v10, v5
	v_mul_f32_e32 v22, v21, v20
	v_fma_f32 v23, -v19, v22, v21
	v_fmac_f32_e32 v22, v23, v20
	v_fma_f32 v19, -v19, v22, v21
	v_div_fmas_f32 v19, v19, v20, v22
	v_div_fixup_f32 v5, v19, v10, v5
	v_div_scale_f32 v19, s[62:63], v10, v10, v4
	v_rcp_f32_e32 v20, v19
	s_nop 0
	v_fma_f32 v21, -v19, v20, 1.0
	v_fmac_f32_e32 v20, v21, v20
	v_div_scale_f32 v21, vcc, v4, v10, v4
	v_mul_f32_e32 v22, v21, v20
	v_fma_f32 v23, -v19, v22, v21
	v_fmac_f32_e32 v22, v23, v20
	v_fma_f32 v19, -v19, v22, v21
	v_div_fmas_f32 v19, v19, v20, v22
	v_div_fixup_f32 v4, v19, v10, v4
	v_div_scale_f32 v19, s[62:63], v10, v10, v3
	v_rcp_f32_e32 v20, v19
	s_nop 0
	v_fma_f32 v21, -v19, v20, 1.0
	v_fmac_f32_e32 v20, v21, v20
	v_div_scale_f32 v21, vcc, v3, v10, v3
	v_mul_f32_e32 v22, v21, v20
	v_fma_f32 v23, -v19, v22, v21
	v_fmac_f32_e32 v22, v23, v20
	v_fma_f32 v19, -v19, v22, v21
	v_div_fmas_f32 v19, v19, v20, v22
	v_div_fixup_f32 v3, v19, v10, v3
	v_div_scale_f32 v19, s[62:63], v10, v10, v2
	v_rcp_f32_e32 v20, v19
	s_nop 0
	v_fma_f32 v21, -v19, v20, 1.0
	v_fmac_f32_e32 v20, v21, v20
	v_div_scale_f32 v21, vcc, v2, v10, v2
	v_mul_f32_e32 v22, v21, v20
	v_fma_f32 v23, -v19, v22, v21
	v_fmac_f32_e32 v22, v23, v20
	v_fma_f32 v19, -v19, v22, v21
	v_div_fmas_f32 v19, v19, v20, v22
	v_div_fixup_f32 v2, v19, v10, v2
	v_cndmask_b32_e64 v2, 0, v2, s[36:37]
	v_cndmask_b32_e64 v2, v2, v3, s[34:35]
	v_cndmask_b32_e64 v2, v2, v4, s[30:31]
	v_cndmask_b32_e64 v2, v2, v5, s[28:29]
	v_cndmask_b32_e64 v2, v2, v6, s[26:27]
	v_cndmask_b32_e64 v2, v2, v7, s[24:25]
	v_cndmask_b32_e64 v2, v2, v8, s[22:23]
	v_cndmask_b32_e64 v2, v2, v11, s[20:21]
	v_cndmask_b32_e64 v2, v2, v15, s[18:19]
	v_cndmask_b32_e64 v2, v2, v17, s[16:17]
	v_cndmask_b32_e64 v2, v2, v18, s[14:15]
	v_cndmask_b32_e64 v2, v2, v16, s[12:13]
	v_cndmask_b32_e64 v2, v2, v14, s[10:11]
	v_cndmask_b32_e64 v2, v2, v13, s[8:9]
	v_cndmask_b32_e64 v2, v2, v12, s[6:7]
	v_cndmask_b32_e64 v4, v2, v9, s[4:5]
	v_lshl_add_u64 v[2:3], s[40:41], 0, v[106:107]
	global_store_dword v[2:3], v4, off
	s_branch .LBB0_1364
